# GEMM K-loop load segments trimmed: SGPR-base LDS-DMA form, merged pre-barrier waits, redundant post-barrier lgkmcnt wait removed, B-fragment LDS base hoisted out of 12 loops (on top of v045)
# speedup vs baseline: 1.0098x; 1.0039x over previous
.Lnobar_e1o:
	v_add_u32_e32 v165, 0x10000, v186
.LBB0_417:
	s_add_u32 s28, s6, 0xfffc0080
	s_addc_u32 s29, s7, -1
	s_add_i32 s43, 0, 0x10000
	s_cmp_eq_u32 s42, 12
	s_cselect_b32 s31, s5, s29
	s_cselect_b32 s30, s8, s28
	s_cselect_b32 s29, s9, s33
	s_cselect_b32 s28, s21, s23
	s_add_i32 s63, 0, 0x14000
	ds_read_b128 v[130:133], v165
	ds_read_b128 v[134:137], v165 offset:1024
	ds_read_b128 v[138:141], v165 offset:2048
	ds_read_b128 v[142:145], v165 offset:3072
	ds_read_b128 v[146:149], v165 offset:16384
	ds_read_b128 v[150:153], v165 offset:17408
	ds_read_b128 v[154:157], v165 offset:18432
	ds_read_b128 v[168:171], v165 offset:19456
	s_add_i32 m0, s45, 0xc000
	ds_read_b128 v[172:175], v188
	ds_read_b128 v[176:179], v188 offset:1024
	ds_read_b128 v[180:183], v188 offset:2048
	ds_read_b128 v[190:193], v188 offset:3072
	ds_read_b128 v[194:197], v188 offset:4096
	ds_read_b128 v[198:201], v188 offset:5120
	ds_read_b128 v[202:205], v188 offset:6144
	global_load_lds_dwordx4 v166, s[6:7]
	s_add_i32 m0, s45, 0xe000
	ds_read_b128 v[206:209], v188 offset:7168
	global_load_lds_dwordx4 v164, s[6:7]
	s_waitcnt vmcnt(8) lgkmcnt(0)
	s_barrier
	v_mfma_f32_16x16x32_bf16 v[126:129], v[130:133], v[172:175], v[126:129]
	v_mfma_f32_16x16x32_bf16 v[122:125], v[138:141], v[172:175], v[122:125]
	v_mfma_f32_16x16x32_bf16 v[114:117], v[130:133], v[180:183], v[114:117]
	v_mfma_f32_16x16x32_bf16 v[106:109], v[138:141], v[180:183], v[106:109]
	v_mfma_f32_16x16x32_bf16 v[98:101], v[130:133], v[194:197], v[98:101]
	v_mfma_f32_16x16x32_bf16 v[90:93], v[138:141], v[194:197], v[90:93]
	v_mfma_f32_16x16x32_bf16 v[82:85], v[130:133], v[202:205], v[82:85]
	v_mfma_f32_16x16x32_bf16 v[74:77], v[138:141], v[202:205], v[74:77]
	v_mfma_f32_16x16x32_bf16 v[126:129], v[134:137], v[176:179], v[126:129]
	v_mfma_f32_16x16x32_bf16 v[122:125], v[142:145], v[176:179], v[122:125]
	v_mfma_f32_16x16x32_bf16 v[114:117], v[134:137], v[190:193], v[114:117]
	v_mfma_f32_16x16x32_bf16 v[106:109], v[142:145], v[190:193], v[106:109]
	v_mfma_f32_16x16x32_bf16 v[98:101], v[134:137], v[198:201], v[98:101]
	v_mfma_f32_16x16x32_bf16 v[90:93], v[142:145], v[198:201], v[90:93]
	v_mfma_f32_16x16x32_bf16 v[82:85], v[134:137], v[206:209], v[82:85]
	v_mfma_f32_16x16x32_bf16 v[74:77], v[142:145], v[206:209], v[74:77]
	v_mfma_f32_16x16x32_bf16 v[118:121], v[146:149], v[172:175], v[118:121]
	v_mfma_f32_16x16x32_bf16 v[110:113], v[154:157], v[172:175], v[110:113]
	v_mfma_f32_16x16x32_bf16 v[102:105], v[146:149], v[180:183], v[102:105]
	v_mfma_f32_16x16x32_bf16 v[94:97], v[154:157], v[180:183], v[94:97]
	v_mfma_f32_16x16x32_bf16 v[86:89], v[146:149], v[194:197], v[86:89]
	v_mfma_f32_16x16x32_bf16 v[78:81], v[154:157], v[194:197], v[78:81]
	v_mfma_f32_16x16x32_bf16 v[70:73], v[146:149], v[202:205], v[70:73]
	v_mfma_f32_16x16x32_bf16 v[66:69], v[154:157], v[202:205], v[66:69]
	v_mfma_f32_16x16x32_bf16 v[118:121], v[150:153], v[176:179], v[118:121]
	v_mfma_f32_16x16x32_bf16 v[110:113], v[168:171], v[176:179], v[110:113]
	v_mfma_f32_16x16x32_bf16 v[102:105], v[150:153], v[190:193], v[102:105]
	v_mfma_f32_16x16x32_bf16 v[94:97], v[168:171], v[190:193], v[94:97]
	v_mfma_f32_16x16x32_bf16 v[86:89], v[150:153], v[198:201], v[86:89]
	v_mfma_f32_16x16x32_bf16 v[78:81], v[168:171], v[198:201], v[78:81]
	v_mfma_f32_16x16x32_bf16 v[70:73], v[150:153], v[206:209], v[70:73]
	v_mfma_f32_16x16x32_bf16 v[66:69], v[168:171], v[206:209], v[66:69]
	s_barrier
	s_add_i32 s43, s43, s44
	v_lshl_add_u64 v[216:217], s[28:29], 0, v[0:1]
	s_mov_b32 m0, s43
	ds_read_b128 v[172:175], v188 offset:16384
	ds_read_b128 v[176:179], v188 offset:17408
	ds_read_b128 v[180:183], v188 offset:18432
	ds_read_b128 v[190:193], v188 offset:19456
	ds_read_b128 v[194:197], v188 offset:20480
	ds_read_b128 v[198:201], v188 offset:21504
	ds_read_b128 v[202:205], v188 offset:22528
	ds_read_b128 v[206:209], v188 offset:23552
	global_load_lds_dwordx4 v0, s[28:29]
	s_add_i32 m0, s43, 0x2000
	s_add_u32 s58, s28, 0x40000
	v_lshl_add_u64 v[218:219], s[28:29], 0, v[158:159]
	s_addc_u32 s59, s29, 0
	s_add_i32 s43, s63, s44
	global_load_lds_dwordx4 v158, s[28:29]
	s_mov_b32 m0, s43
	v_lshl_add_u64 v[222:223], s[30:31], 0, v[160:161]
	global_load_lds_dwordx4 v0, s[58:59]
	s_add_i32 m0, s43, 0x2000
	s_nop 0
	global_load_lds_dwordx4 v158, s[58:59]
	s_mov_b32 m0, s45
	v_lshl_add_u64 v[220:221], s[30:31], 0, v[162:163]
	global_load_lds_dwordx4 v162, s[30:31]
	s_mov_b32 m0, s46
	s_nop 0
	global_load_lds_dwordx4 v160, s[30:31]
	s_waitcnt vmcnt(8) lgkmcnt(0)
	s_barrier
	v_mfma_f32_16x16x32_bf16 v[62:65], v[130:133], v[172:175], v[62:65]
	v_mfma_f32_16x16x32_bf16 v[58:61], v[138:141], v[172:175], v[58:61]
	v_mfma_f32_16x16x32_bf16 v[50:53], v[130:133], v[180:183], v[50:53]
	v_mfma_f32_16x16x32_bf16 v[42:45], v[138:141], v[180:183], v[42:45]
	v_mfma_f32_16x16x32_bf16 v[34:37], v[130:133], v[194:197], v[34:37]
	v_mfma_f32_16x16x32_bf16 v[26:29], v[138:141], v[194:197], v[26:29]
	v_mfma_f32_16x16x32_bf16 v[18:21], v[130:133], v[202:205], v[18:21]
	v_mfma_f32_16x16x32_bf16 v[10:13], v[138:141], v[202:205], v[10:13]
	v_mfma_f32_16x16x32_bf16 v[62:65], v[134:137], v[176:179], v[62:65]
	v_mfma_f32_16x16x32_bf16 v[58:61], v[142:145], v[176:179], v[58:61]
	v_mfma_f32_16x16x32_bf16 v[50:53], v[134:137], v[190:193], v[50:53]
	v_mfma_f32_16x16x32_bf16 v[42:45], v[142:145], v[190:193], v[42:45]
	v_mfma_f32_16x16x32_bf16 v[34:37], v[134:137], v[198:201], v[34:37]
	v_mfma_f32_16x16x32_bf16 v[26:29], v[142:145], v[198:201], v[26:29]
	v_mfma_f32_16x16x32_bf16 v[18:21], v[134:137], v[206:209], v[18:21]
	v_mfma_f32_16x16x32_bf16 v[10:13], v[142:145], v[206:209], v[10:13]
	v_mfma_f32_16x16x32_bf16 v[54:57], v[146:149], v[172:175], v[54:57]
	v_mfma_f32_16x16x32_bf16 v[46:49], v[154:157], v[172:175], v[46:49]
	v_mfma_f32_16x16x32_bf16 v[38:41], v[146:149], v[180:183], v[38:41]
	v_mfma_f32_16x16x32_bf16 v[30:33], v[154:157], v[180:183], v[30:33]
	v_mfma_f32_16x16x32_bf16 v[22:25], v[146:149], v[194:197], v[22:25]
	v_mfma_f32_16x16x32_bf16 v[14:17], v[154:157], v[194:197], v[14:17]
	v_mfma_f32_16x16x32_bf16 v[6:9], v[146:149], v[202:205], v[6:9]
	v_mfma_f32_16x16x32_bf16 v[2:5], v[154:157], v[202:205], v[2:5]
	v_mfma_f32_16x16x32_bf16 v[54:57], v[150:153], v[176:179], v[54:57]
	v_mfma_f32_16x16x32_bf16 v[46:49], v[168:171], v[176:179], v[46:49]
	v_mfma_f32_16x16x32_bf16 v[38:41], v[150:153], v[190:193], v[38:41]
	v_mfma_f32_16x16x32_bf16 v[30:33], v[168:171], v[190:193], v[30:33]
	v_mfma_f32_16x16x32_bf16 v[22:25], v[150:153], v[198:201], v[22:25]
	v_mfma_f32_16x16x32_bf16 v[14:17], v[168:171], v[198:201], v[14:17]
	v_mfma_f32_16x16x32_bf16 v[6:9], v[150:153], v[206:209], v[6:9]
	v_mfma_f32_16x16x32_bf16 v[2:5], v[168:171], v[206:209], v[2:5]
	s_barrier
	s_add_i32 s43, 0, 0x18000
	s_add_i32 s58, 0, 0x1c000
	ds_read_b128 v[130:133], v165 offset:32768
	ds_read_b128 v[134:137], v165 offset:33792
	ds_read_b128 v[138:141], v165 offset:34816
	ds_read_b128 v[142:145], v165 offset:35840
	ds_read_b128 v[146:149], v165 offset:49152
	ds_read_b128 v[150:153], v165 offset:50176
	ds_read_b128 v[154:157], v165 offset:51200
	ds_read_b128 v[168:171], v165 offset:52224
	s_add_u32 s30, s30, 0x40000
	s_addc_u32 s31, s31, 0
	s_mov_b32 m0, s47
	ds_read_b128 v[172:175], v188 offset:32768
	ds_read_b128 v[176:179], v188 offset:33792
	ds_read_b128 v[180:183], v188 offset:34816
	ds_read_b128 v[190:193], v188 offset:35840
	ds_read_b128 v[194:197], v188 offset:36864
	ds_read_b128 v[198:201], v188 offset:37888
	ds_read_b128 v[202:205], v188 offset:38912
	global_load_lds_dwordx4 v162, s[30:31]
	s_mov_b32 m0, s48
	ds_read_b128 v[206:209], v188 offset:39936
	global_load_lds_dwordx4 v160, s[30:31]
	s_waitcnt vmcnt(8) lgkmcnt(0)
	s_barrier
	v_mfma_f32_16x16x32_bf16 v[126:129], v[130:133], v[172:175], v[126:129]
	v_mfma_f32_16x16x32_bf16 v[122:125], v[138:141], v[172:175], v[122:125]
	v_mfma_f32_16x16x32_bf16 v[114:117], v[130:133], v[180:183], v[114:117]
	v_mfma_f32_16x16x32_bf16 v[106:109], v[138:141], v[180:183], v[106:109]
	v_mfma_f32_16x16x32_bf16 v[98:101], v[130:133], v[194:197], v[98:101]
	v_mfma_f32_16x16x32_bf16 v[90:93], v[138:141], v[194:197], v[90:93]
	v_mfma_f32_16x16x32_bf16 v[82:85], v[130:133], v[202:205], v[82:85]
	v_mfma_f32_16x16x32_bf16 v[74:77], v[138:141], v[202:205], v[74:77]
	v_mfma_f32_16x16x32_bf16 v[126:129], v[134:137], v[176:179], v[126:129]
	v_mfma_f32_16x16x32_bf16 v[122:125], v[142:145], v[176:179], v[122:125]
	v_mfma_f32_16x16x32_bf16 v[114:117], v[134:137], v[190:193], v[114:117]
	v_mfma_f32_16x16x32_bf16 v[106:109], v[142:145], v[190:193], v[106:109]
	v_mfma_f32_16x16x32_bf16 v[98:101], v[134:137], v[198:201], v[98:101]
	v_mfma_f32_16x16x32_bf16 v[90:93], v[142:145], v[198:201], v[90:93]
	v_mfma_f32_16x16x32_bf16 v[82:85], v[134:137], v[206:209], v[82:85]
	v_mfma_f32_16x16x32_bf16 v[74:77], v[142:145], v[206:209], v[74:77]
	v_mfma_f32_16x16x32_bf16 v[118:121], v[146:149], v[172:175], v[118:121]
	v_mfma_f32_16x16x32_bf16 v[110:113], v[154:157], v[172:175], v[110:113]
	v_mfma_f32_16x16x32_bf16 v[102:105], v[146:149], v[180:183], v[102:105]
	v_mfma_f32_16x16x32_bf16 v[94:97], v[154:157], v[180:183], v[94:97]
	v_mfma_f32_16x16x32_bf16 v[86:89], v[146:149], v[194:197], v[86:89]
	v_mfma_f32_16x16x32_bf16 v[78:81], v[154:157], v[194:197], v[78:81]
	v_mfma_f32_16x16x32_bf16 v[70:73], v[146:149], v[202:205], v[70:73]
	v_mfma_f32_16x16x32_bf16 v[66:69], v[154:157], v[202:205], v[66:69]
	v_mfma_f32_16x16x32_bf16 v[118:121], v[150:153], v[176:179], v[118:121]
	v_mfma_f32_16x16x32_bf16 v[110:113], v[168:171], v[176:179], v[110:113]
	v_mfma_f32_16x16x32_bf16 v[102:105], v[150:153], v[190:193], v[102:105]
	v_mfma_f32_16x16x32_bf16 v[94:97], v[168:171], v[190:193], v[94:97]
	v_mfma_f32_16x16x32_bf16 v[86:89], v[150:153], v[198:201], v[86:89]
	v_mfma_f32_16x16x32_bf16 v[78:81], v[168:171], v[198:201], v[78:81]
	v_mfma_f32_16x16x32_bf16 v[70:73], v[150:153], v[206:209], v[70:73]
	v_mfma_f32_16x16x32_bf16 v[66:69], v[168:171], v[206:209], v[66:69]
	s_barrier
	s_add_i32 s30, s43, s44
	v_lshl_add_u64 v[216:217], v[216:217], 0, s[56:57]
	s_mov_b32 m0, s30
	ds_read_b128 v[172:175], v188 offset:49152
	ds_read_b128 v[176:179], v188 offset:50176
	ds_read_b128 v[180:183], v188 offset:51200
	ds_read_b128 v[190:193], v188 offset:52224
	ds_read_b128 v[194:197], v188 offset:53248
	ds_read_b128 v[198:201], v188 offset:54272
	ds_read_b128 v[202:205], v188 offset:55296
	ds_read_b128 v[206:209], v188 offset:56320
	global_load_lds_dwordx4 v[216:217], off
	s_add_i32 m0, s30, 0x2000
	s_add_u32 s28, s28, 0x40080
	v_lshl_add_u64 v[216:217], v[218:219], 0, s[56:57]
	s_addc_u32 s29, s29, 0
	s_add_i32 s30, s58, s44
	global_load_lds_dwordx4 v[216:217], off
	s_mov_b32 m0, s30
	s_nop 0
	global_load_lds_dwordx4 v0, s[28:29]
	s_add_i32 m0, s30, 0x2000
	s_nop 0
	global_load_lds_dwordx4 v158, s[28:29]
	s_mov_b32 m0, s49
	v_lshl_add_u64 v[216:217], v[220:221], 0, s[56:57]
	global_load_lds_dwordx4 v[216:217], off
	s_mov_b32 m0, s52
	v_lshl_add_u64 v[216:217], v[222:223], 0, s[56:57]
	global_load_lds_dwordx4 v[216:217], off
	s_waitcnt vmcnt(8) lgkmcnt(0)
	s_barrier
	v_mfma_f32_16x16x32_bf16 v[62:65], v[130:133], v[172:175], v[62:65]
	v_mfma_f32_16x16x32_bf16 v[58:61], v[138:141], v[172:175], v[58:61]
	v_mfma_f32_16x16x32_bf16 v[50:53], v[130:133], v[180:183], v[50:53]
	v_mfma_f32_16x16x32_bf16 v[42:45], v[138:141], v[180:183], v[42:45]
	v_mfma_f32_16x16x32_bf16 v[34:37], v[130:133], v[194:197], v[34:37]
	v_mfma_f32_16x16x32_bf16 v[26:29], v[138:141], v[194:197], v[26:29]
	v_mfma_f32_16x16x32_bf16 v[18:21], v[130:133], v[202:205], v[18:21]
	v_mfma_f32_16x16x32_bf16 v[10:13], v[138:141], v[202:205], v[10:13]
	v_mfma_f32_16x16x32_bf16 v[62:65], v[134:137], v[176:179], v[62:65]
	v_mfma_f32_16x16x32_bf16 v[58:61], v[142:145], v[176:179], v[58:61]
	v_mfma_f32_16x16x32_bf16 v[50:53], v[134:137], v[190:193], v[50:53]
	v_mfma_f32_16x16x32_bf16 v[42:45], v[142:145], v[190:193], v[42:45]
	v_mfma_f32_16x16x32_bf16 v[34:37], v[134:137], v[198:201], v[34:37]
	v_mfma_f32_16x16x32_bf16 v[26:29], v[142:145], v[198:201], v[26:29]
	v_mfma_f32_16x16x32_bf16 v[18:21], v[134:137], v[206:209], v[18:21]
	v_mfma_f32_16x16x32_bf16 v[10:13], v[142:145], v[206:209], v[10:13]
	v_mfma_f32_16x16x32_bf16 v[54:57], v[146:149], v[172:175], v[54:57]
	v_mfma_f32_16x16x32_bf16 v[46:49], v[154:157], v[172:175], v[46:49]
	v_mfma_f32_16x16x32_bf16 v[38:41], v[146:149], v[180:183], v[38:41]
	v_mfma_f32_16x16x32_bf16 v[30:33], v[154:157], v[180:183], v[30:33]
	v_mfma_f32_16x16x32_bf16 v[22:25], v[146:149], v[194:197], v[22:25]
	v_mfma_f32_16x16x32_bf16 v[14:17], v[154:157], v[194:197], v[14:17]
	v_mfma_f32_16x16x32_bf16 v[6:9], v[146:149], v[202:205], v[6:9]
	v_mfma_f32_16x16x32_bf16 v[2:5], v[154:157], v[202:205], v[2:5]
	v_mfma_f32_16x16x32_bf16 v[54:57], v[150:153], v[176:179], v[54:57]
	v_mfma_f32_16x16x32_bf16 v[46:49], v[168:171], v[176:179], v[46:49]
	v_mfma_f32_16x16x32_bf16 v[38:41], v[150:153], v[190:193], v[38:41]
	v_mfma_f32_16x16x32_bf16 v[30:33], v[168:171], v[190:193], v[30:33]
	v_mfma_f32_16x16x32_bf16 v[22:25], v[150:153], v[198:201], v[22:25]
	v_mfma_f32_16x16x32_bf16 v[14:17], v[168:171], v[198:201], v[14:17]
	v_mfma_f32_16x16x32_bf16 v[6:9], v[150:153], v[206:209], v[6:9]
	v_mfma_f32_16x16x32_bf16 v[2:5], v[168:171], v[206:209], v[2:5]
	s_barrier
	s_add_i32 s42, s42, 2
	s_add_u32 s23, s23, 0x100
	s_addc_u32 s33, s33, 0
	s_add_u32 s6, s6, 0x100
	s_addc_u32 s7, s7, 0
	s_cmp_gt_u32 s42, 13
	s_cbranch_scc0 .LBB0_417
	s_and_b64 vcc, exec, s[18:19]
	s_cbranch_vccz .LBB0_420
	s_barrier

.LBB0_586:
	s_add_u32 s8, s62, 0x100
	s_addc_u32 s9, s63, 0
	s_ashr_i32 s47, s46, 31
	s_lshl_b64 s[48:49], s[46:47], 19
	s_add_u32 s52, s85, s48
	s_addc_u32 s53, s93, s49
	s_and_b64 s[48:49], s[44:45], exec
	s_cselect_b32 s47, s53, s35
	s_cselect_b32 s59, s52, s34
	s_ashr_i32 s37, s36, 31
	s_lshl_b64 s[48:49], s[36:37], 19
	s_add_u32 s48, s94, s48
	s_addc_u32 s49, s95, s49
	s_and_b64 s[70:71], s[44:45], exec
	s_cselect_b32 s37, s49, s63
	s_cselect_b32 vcc_lo, s48, s62
	s_add_u32 s62, s34, 0x40080
	s_addc_u32 s63, s35, 0
	v_lshl_add_u64 v[140:141], s[62:63], 0, v[128:129]
	v_lshl_add_u64 v[142:143], s[62:63], 0, v[138:139]
	s_mov_b32 vcc_hi, -2
	s_mov_b64 s[62:63], 0
	v_add_u32_e32 v241, 0x10000, v144
.LBB0_587:
	s_add_u32 s18, s34, s62
	s_addc_u32 s19, s35, s63
	s_add_u32 s18, s18, 0x100
	s_addc_u32 s19, s19, 0
	s_add_u32 s70, s8, s62
	s_addc_u32 s71, s9, s63
	s_add_i32 s26, 0, 0x10000
	s_cmpk_eq_i32 s62, 0x700
	s_cselect_b32 s77, s47, s19
	s_cselect_b32 s76, s59, s18
	s_cselect_b32 s71, s37, s71
	s_cselect_b32 s70, vcc_lo, s70
	s_add_i32 s27, 0, 0x14000
	ds_read_b128 v[146:149], v241
	ds_read_b128 v[150:153], v241 offset:1024
	ds_read_b128 v[154:157], v241 offset:2048
	ds_read_b128 v[158:161], v241 offset:3072
	ds_read_b128 v[162:165], v241 offset:16384
	ds_read_b128 v[168:171], v241 offset:17408
	ds_read_b128 v[172:175], v241 offset:18432
	ds_read_b128 v[176:179], v241 offset:19456
	v_lshl_add_u64 v[208:209], v[142:143], 0, s[62:63]
	s_add_i32 m0, s4, 0xc000
	ds_read_b128 v[180:183], v145
	ds_read_b128 v[184:187], v145 offset:1024
	ds_read_b128 v[188:191], v145 offset:2048
	ds_read_b128 v[192:195], v145 offset:3072
	ds_read_b128 v[196:199], v145 offset:4096
	ds_read_b128 v[200:203], v145 offset:5120
	ds_read_b128 v[204:207], v145 offset:6144
	ds_read_b128 v[216:219], v145 offset:7168
	global_load_lds_dwordx4 v[208:209], off
	s_add_i32 m0, s4, 0xe000
	v_lshl_add_u64 v[208:209], v[140:141], 0, s[62:63]
	global_load_lds_dwordx4 v[208:209], off
	s_waitcnt vmcnt(8) lgkmcnt(0)
	s_barrier
	v_mfma_f32_16x16x32_bf16 v[134:137], v[146:149], v[180:183], v[134:137]
	v_mfma_f32_16x16x32_bf16 v[130:133], v[154:157], v[180:183], v[130:133]
	v_mfma_f32_16x16x32_bf16 v[110:113], v[146:149], v[188:191], v[110:113]
	v_mfma_f32_16x16x32_bf16 v[106:109], v[154:157], v[188:191], v[106:109]
	v_mfma_f32_16x16x32_bf16 v[94:97], v[146:149], v[196:199], v[94:97]
	v_mfma_f32_16x16x32_bf16 v[90:93], v[154:157], v[196:199], v[90:93]
	v_mfma_f32_16x16x32_bf16 v[78:81], v[146:149], v[204:207], v[78:81]
	v_mfma_f32_16x16x32_bf16 v[74:77], v[154:157], v[204:207], v[74:77]
	v_mfma_f32_16x16x32_bf16 v[134:137], v[150:153], v[184:187], v[134:137]
	v_mfma_f32_16x16x32_bf16 v[130:133], v[158:161], v[184:187], v[130:133]
	v_mfma_f32_16x16x32_bf16 v[110:113], v[150:153], v[192:195], v[110:113]
	v_mfma_f32_16x16x32_bf16 v[106:109], v[158:161], v[192:195], v[106:109]
	v_mfma_f32_16x16x32_bf16 v[94:97], v[150:153], v[200:203], v[94:97]
	v_mfma_f32_16x16x32_bf16 v[90:93], v[158:161], v[200:203], v[90:93]
	v_mfma_f32_16x16x32_bf16 v[78:81], v[150:153], v[216:219], v[78:81]
	v_mfma_f32_16x16x32_bf16 v[74:77], v[158:161], v[216:219], v[74:77]
	v_mfma_f32_16x16x32_bf16 v[122:125], v[162:165], v[180:183], v[122:125]
	v_mfma_f32_16x16x32_bf16 v[114:117], v[172:175], v[180:183], v[114:117]
	v_mfma_f32_16x16x32_bf16 v[102:105], v[162:165], v[188:191], v[102:105]
	v_mfma_f32_16x16x32_bf16 v[98:101], v[172:175], v[188:191], v[98:101]
	v_mfma_f32_16x16x32_bf16 v[86:89], v[162:165], v[196:199], v[86:89]
	v_mfma_f32_16x16x32_bf16 v[82:85], v[172:175], v[196:199], v[82:85]
	v_mfma_f32_16x16x32_bf16 v[70:73], v[162:165], v[204:207], v[70:73]
	v_mfma_f32_16x16x32_bf16 v[66:69], v[172:175], v[204:207], v[66:69]
	v_mfma_f32_16x16x32_bf16 v[122:125], v[168:171], v[184:187], v[122:125]
	v_mfma_f32_16x16x32_bf16 v[114:117], v[176:179], v[184:187], v[114:117]
	v_mfma_f32_16x16x32_bf16 v[102:105], v[168:171], v[192:195], v[102:105]
	v_mfma_f32_16x16x32_bf16 v[98:101], v[176:179], v[192:195], v[98:101]
	v_mfma_f32_16x16x32_bf16 v[86:89], v[168:171], v[200:203], v[86:89]
	v_mfma_f32_16x16x32_bf16 v[82:85], v[176:179], v[200:203], v[82:85]
	v_mfma_f32_16x16x32_bf16 v[70:73], v[168:171], v[216:219], v[70:73]
	v_mfma_f32_16x16x32_bf16 v[66:69], v[176:179], v[216:219], v[66:69]
	s_barrier
	s_add_i32 s18, s26, s84
	v_lshl_add_u64 v[208:209], s[70:71], 0, v[0:1]
	s_mov_b32 m0, s18
	ds_read_b128 v[180:183], v145 offset:16384
	ds_read_b128 v[184:187], v145 offset:17408
	ds_read_b128 v[188:191], v145 offset:18432
	ds_read_b128 v[192:195], v145 offset:19456
	ds_read_b128 v[196:199], v145 offset:20480
	ds_read_b128 v[200:203], v145 offset:21504
	ds_read_b128 v[204:207], v145 offset:22528
	ds_read_b128 v[216:219], v145 offset:23552
	global_load_lds_dwordx4 v0, s[70:71]
	s_add_i32 m0, s18, 0x2000
	s_add_u32 s18, s70, 0x40000
	v_lshl_add_u64 v[220:221], s[70:71], 0, v[118:119]
	s_addc_u32 s19, s71, 0
	s_add_i32 s26, s27, s84
	global_load_lds_dwordx4 v118, s[70:71]
	s_mov_b32 m0, s26
	v_lshl_add_u64 v[224:225], s[76:77], 0, v[120:121]
	global_load_lds_dwordx4 v0, s[18:19]
	s_add_i32 m0, s26, 0x2000
	s_nop 0
	global_load_lds_dwordx4 v118, s[18:19]
	s_mov_b32 m0, s4
	v_lshl_add_u64 v[222:223], s[76:77], 0, v[126:127]
	global_load_lds_dwordx4 v126, s[76:77]
	s_mov_b32 m0, s5
	s_nop 0
	global_load_lds_dwordx4 v120, s[76:77]
	s_waitcnt vmcnt(8) lgkmcnt(0)
	s_barrier
	v_mfma_f32_16x16x32_bf16 v[62:65], v[146:149], v[180:183], v[62:65]
	v_mfma_f32_16x16x32_bf16 v[58:61], v[154:157], v[180:183], v[58:61]
	v_mfma_f32_16x16x32_bf16 v[46:49], v[146:149], v[188:191], v[46:49]
	v_mfma_f32_16x16x32_bf16 v[42:45], v[154:157], v[188:191], v[42:45]
	v_mfma_f32_16x16x32_bf16 v[30:33], v[146:149], v[196:199], v[30:33]
	v_mfma_f32_16x16x32_bf16 v[26:29], v[154:157], v[196:199], v[26:29]
	v_mfma_f32_16x16x32_bf16 v[14:17], v[146:149], v[204:207], v[14:17]
	v_mfma_f32_16x16x32_bf16 v[10:13], v[154:157], v[204:207], v[10:13]
	v_mfma_f32_16x16x32_bf16 v[62:65], v[150:153], v[184:187], v[62:65]
	v_mfma_f32_16x16x32_bf16 v[58:61], v[158:161], v[184:187], v[58:61]
	v_mfma_f32_16x16x32_bf16 v[46:49], v[150:153], v[192:195], v[46:49]
	v_mfma_f32_16x16x32_bf16 v[42:45], v[158:161], v[192:195], v[42:45]
	v_mfma_f32_16x16x32_bf16 v[30:33], v[150:153], v[200:203], v[30:33]
	v_mfma_f32_16x16x32_bf16 v[26:29], v[158:161], v[200:203], v[26:29]
	v_mfma_f32_16x16x32_bf16 v[14:17], v[150:153], v[216:219], v[14:17]
	v_mfma_f32_16x16x32_bf16 v[10:13], v[158:161], v[216:219], v[10:13]
	v_mfma_f32_16x16x32_bf16 v[54:57], v[162:165], v[180:183], v[54:57]
	v_mfma_f32_16x16x32_bf16 v[50:53], v[172:175], v[180:183], v[50:53]
	v_mfma_f32_16x16x32_bf16 v[38:41], v[162:165], v[188:191], v[38:41]
	v_mfma_f32_16x16x32_bf16 v[34:37], v[172:175], v[188:191], v[34:37]
	v_mfma_f32_16x16x32_bf16 v[22:25], v[162:165], v[196:199], v[22:25]
	v_mfma_f32_16x16x32_bf16 v[18:21], v[172:175], v[196:199], v[18:21]
	v_mfma_f32_16x16x32_bf16 v[6:9], v[162:165], v[204:207], v[6:9]
	v_mfma_f32_16x16x32_bf16 v[2:5], v[172:175], v[204:207], v[2:5]
	v_mfma_f32_16x16x32_bf16 v[54:57], v[168:171], v[184:187], v[54:57]
	v_mfma_f32_16x16x32_bf16 v[50:53], v[176:179], v[184:187], v[50:53]
	v_mfma_f32_16x16x32_bf16 v[38:41], v[168:171], v[192:195], v[38:41]
	v_mfma_f32_16x16x32_bf16 v[34:37], v[176:179], v[192:195], v[34:37]
	v_mfma_f32_16x16x32_bf16 v[22:25], v[168:171], v[200:203], v[22:25]
	v_mfma_f32_16x16x32_bf16 v[18:21], v[176:179], v[200:203], v[18:21]
	v_mfma_f32_16x16x32_bf16 v[6:9], v[168:171], v[216:219], v[6:9]
	v_mfma_f32_16x16x32_bf16 v[2:5], v[176:179], v[216:219], v[2:5]
	s_barrier
	s_add_i32 s26, 0, 0x18000
	s_add_i32 s27, 0, 0x1c000
	ds_read_b128 v[146:149], v241 offset:32768
	ds_read_b128 v[150:153], v241 offset:33792
	ds_read_b128 v[154:157], v241 offset:34816
	ds_read_b128 v[158:161], v241 offset:35840
	ds_read_b128 v[162:165], v241 offset:49152
	ds_read_b128 v[168:171], v241 offset:50176
	ds_read_b128 v[172:175], v241 offset:51200
	ds_read_b128 v[176:179], v241 offset:52224
	s_add_u32 s18, s76, 0x40000
	s_addc_u32 s19, s77, 0
	s_mov_b32 m0, s33
	ds_read_b128 v[180:183], v145 offset:32768
	ds_read_b128 v[184:187], v145 offset:33792
	ds_read_b128 v[188:191], v145 offset:34816
	ds_read_b128 v[192:195], v145 offset:35840
	ds_read_b128 v[196:199], v145 offset:36864
	ds_read_b128 v[200:203], v145 offset:37888
	ds_read_b128 v[204:207], v145 offset:38912
	ds_read_b128 v[216:219], v145 offset:39936
	global_load_lds_dwordx4 v126, s[18:19]
	s_mov_b32 m0, s92
	v_lshl_add_u64 v[242:243], s[18:19], 0, v[120:121]
	global_load_lds_dwordx4 v120, s[18:19]
	s_waitcnt vmcnt(8) lgkmcnt(0)
	s_barrier
	v_mfma_f32_16x16x32_bf16 v[134:137], v[146:149], v[180:183], v[134:137]
	v_mfma_f32_16x16x32_bf16 v[130:133], v[154:157], v[180:183], v[130:133]
	v_mfma_f32_16x16x32_bf16 v[110:113], v[146:149], v[188:191], v[110:113]
	v_mfma_f32_16x16x32_bf16 v[106:109], v[154:157], v[188:191], v[106:109]
	v_mfma_f32_16x16x32_bf16 v[94:97], v[146:149], v[196:199], v[94:97]
	v_mfma_f32_16x16x32_bf16 v[90:93], v[154:157], v[196:199], v[90:93]
	v_mfma_f32_16x16x32_bf16 v[78:81], v[146:149], v[204:207], v[78:81]
	v_mfma_f32_16x16x32_bf16 v[74:77], v[154:157], v[204:207], v[74:77]
	v_mfma_f32_16x16x32_bf16 v[134:137], v[150:153], v[184:187], v[134:137]
	v_mfma_f32_16x16x32_bf16 v[130:133], v[158:161], v[184:187], v[130:133]
	v_mfma_f32_16x16x32_bf16 v[110:113], v[150:153], v[192:195], v[110:113]
	v_mfma_f32_16x16x32_bf16 v[106:109], v[158:161], v[192:195], v[106:109]
	v_mfma_f32_16x16x32_bf16 v[94:97], v[150:153], v[200:203], v[94:97]
	v_mfma_f32_16x16x32_bf16 v[90:93], v[158:161], v[200:203], v[90:93]
	v_mfma_f32_16x16x32_bf16 v[78:81], v[150:153], v[216:219], v[78:81]
	v_mfma_f32_16x16x32_bf16 v[74:77], v[158:161], v[216:219], v[74:77]
	v_mfma_f32_16x16x32_bf16 v[122:125], v[162:165], v[180:183], v[122:125]
	v_mfma_f32_16x16x32_bf16 v[114:117], v[172:175], v[180:183], v[114:117]
	v_mfma_f32_16x16x32_bf16 v[102:105], v[162:165], v[188:191], v[102:105]
	v_mfma_f32_16x16x32_bf16 v[98:101], v[172:175], v[188:191], v[98:101]
	v_mfma_f32_16x16x32_bf16 v[86:89], v[162:165], v[196:199], v[86:89]
	v_mfma_f32_16x16x32_bf16 v[82:85], v[172:175], v[196:199], v[82:85]
	v_mfma_f32_16x16x32_bf16 v[70:73], v[162:165], v[204:207], v[70:73]
	v_mfma_f32_16x16x32_bf16 v[66:69], v[172:175], v[204:207], v[66:69]
	v_mfma_f32_16x16x32_bf16 v[122:125], v[168:171], v[184:187], v[122:125]
	v_mfma_f32_16x16x32_bf16 v[114:117], v[176:179], v[184:187], v[114:117]
	v_mfma_f32_16x16x32_bf16 v[102:105], v[168:171], v[192:195], v[102:105]
	v_mfma_f32_16x16x32_bf16 v[98:101], v[176:179], v[192:195], v[98:101]
	v_mfma_f32_16x16x32_bf16 v[86:89], v[168:171], v[200:203], v[86:89]
	v_mfma_f32_16x16x32_bf16 v[82:85], v[176:179], v[200:203], v[82:85]
	v_mfma_f32_16x16x32_bf16 v[70:73], v[168:171], v[216:219], v[70:73]
	v_mfma_f32_16x16x32_bf16 v[66:69], v[176:179], v[216:219], v[66:69]
	s_barrier
	s_add_i32 s18, s26, s84
	v_lshl_add_u64 v[208:209], v[208:209], 0, s[56:57]
	s_mov_b32 m0, s18
	ds_read_b128 v[180:183], v145 offset:49152
	ds_read_b128 v[184:187], v145 offset:50176
	ds_read_b128 v[188:191], v145 offset:51200
	ds_read_b128 v[192:195], v145 offset:52224
	ds_read_b128 v[196:199], v145 offset:53248
	ds_read_b128 v[200:203], v145 offset:54272
	ds_read_b128 v[204:207], v145 offset:55296
	ds_read_b128 v[216:219], v145 offset:56320
	global_load_lds_dwordx4 v[208:209], off
	s_add_i32 m0, s18, 0x2000
	s_add_u32 s18, s70, 0x40080
	v_lshl_add_u64 v[208:209], v[220:221], 0, s[56:57]
	s_addc_u32 s19, s71, 0
	s_add_i32 s26, s27, s84
	global_load_lds_dwordx4 v[208:209], off
	s_mov_b32 m0, s26
	s_nop 0
	global_load_lds_dwordx4 v0, s[18:19]
	s_add_i32 m0, s26, 0x2000
	s_nop 0
	global_load_lds_dwordx4 v118, s[18:19]
	s_mov_b32 m0, s90
	v_lshl_add_u64 v[208:209], v[222:223], 0, s[56:57]
	global_load_lds_dwordx4 v[208:209], off
	s_mov_b32 m0, s96
	v_lshl_add_u64 v[208:209], v[224:225], 0, s[56:57]
	global_load_lds_dwordx4 v[208:209], off
	s_waitcnt vmcnt(8) lgkmcnt(0)
	s_barrier
	v_mfma_f32_16x16x32_bf16 v[62:65], v[146:149], v[180:183], v[62:65]
	v_mfma_f32_16x16x32_bf16 v[58:61], v[154:157], v[180:183], v[58:61]
	v_mfma_f32_16x16x32_bf16 v[46:49], v[146:149], v[188:191], v[46:49]
	v_mfma_f32_16x16x32_bf16 v[42:45], v[154:157], v[188:191], v[42:45]
	v_mfma_f32_16x16x32_bf16 v[30:33], v[146:149], v[196:199], v[30:33]
	v_mfma_f32_16x16x32_bf16 v[26:29], v[154:157], v[196:199], v[26:29]
	v_mfma_f32_16x16x32_bf16 v[14:17], v[146:149], v[204:207], v[14:17]
	v_mfma_f32_16x16x32_bf16 v[10:13], v[154:157], v[204:207], v[10:13]
	v_mfma_f32_16x16x32_bf16 v[62:65], v[150:153], v[184:187], v[62:65]
	v_mfma_f32_16x16x32_bf16 v[58:61], v[158:161], v[184:187], v[58:61]
	v_mfma_f32_16x16x32_bf16 v[46:49], v[150:153], v[192:195], v[46:49]
	v_mfma_f32_16x16x32_bf16 v[42:45], v[158:161], v[192:195], v[42:45]
	v_mfma_f32_16x16x32_bf16 v[30:33], v[150:153], v[200:203], v[30:33]
	v_mfma_f32_16x16x32_bf16 v[26:29], v[158:161], v[200:203], v[26:29]
	v_mfma_f32_16x16x32_bf16 v[14:17], v[150:153], v[216:219], v[14:17]
	v_mfma_f32_16x16x32_bf16 v[10:13], v[158:161], v[216:219], v[10:13]
	v_mfma_f32_16x16x32_bf16 v[54:57], v[162:165], v[180:183], v[54:57]
	v_mfma_f32_16x16x32_bf16 v[50:53], v[172:175], v[180:183], v[50:53]
	v_mfma_f32_16x16x32_bf16 v[38:41], v[162:165], v[188:191], v[38:41]
	v_mfma_f32_16x16x32_bf16 v[34:37], v[172:175], v[188:191], v[34:37]
	v_mfma_f32_16x16x32_bf16 v[22:25], v[162:165], v[196:199], v[22:25]
	v_mfma_f32_16x16x32_bf16 v[18:21], v[172:175], v[196:199], v[18:21]
	v_mfma_f32_16x16x32_bf16 v[6:9], v[162:165], v[204:207], v[6:9]
	v_mfma_f32_16x16x32_bf16 v[2:5], v[172:175], v[204:207], v[2:5]
	v_mfma_f32_16x16x32_bf16 v[54:57], v[168:171], v[184:187], v[54:57]
	v_mfma_f32_16x16x32_bf16 v[50:53], v[176:179], v[184:187], v[50:53]
	v_mfma_f32_16x16x32_bf16 v[38:41], v[168:171], v[192:195], v[38:41]
	v_mfma_f32_16x16x32_bf16 v[34:37], v[176:179], v[192:195], v[34:37]
	v_mfma_f32_16x16x32_bf16 v[22:25], v[168:171], v[200:203], v[22:25]
	v_mfma_f32_16x16x32_bf16 v[18:21], v[176:179], v[200:203], v[18:21]
	v_mfma_f32_16x16x32_bf16 v[6:9], v[168:171], v[216:219], v[6:9]
	v_mfma_f32_16x16x32_bf16 v[2:5], v[176:179], v[216:219], v[2:5]
	s_barrier
	s_add_i32 vcc_hi, vcc_hi, 2
	s_add_u32 s62, s62, 0x100
	s_addc_u32 s63, s63, 0
	s_cmp_gt_u32 vcc_hi, 13
	s_cbranch_scc0 .LBB0_587
	s_add_u32 s62, s8, 0xffffff00
	s_addc_u32 s63, s9, -1
	s_andn2_b64 vcc, exec, s[44:45]
	s_cbranch_vccnz .LBB0_590
	v_mov_b32_e32 v2, 0
	s_mov_b32 s20, s36
	s_mov_b32 s83, s46
	s_mov_b64 s[34:35], s[52:53]
	s_mov_b32 s68, s58
	v_mov_b32_e32 v3, v2
	v_mov_b32_e32 v4, v2
	v_mov_b32_e32 v5, v2
	v_mov_b32_e32 v6, v2
	v_mov_b32_e32 v7, v2
	v_mov_b32_e32 v8, v2
	v_mov_b32_e32 v9, v2
	v_mov_b32_e32 v18, v2
	v_mov_b32_e32 v19, v2
	v_mov_b32_e32 v20, v2
	v_mov_b32_e32 v21, v2
	v_mov_b32_e32 v22, v2
	v_mov_b32_e32 v23, v2
	v_mov_b32_e32 v24, v2
	v_mov_b32_e32 v25, v2
	v_mov_b32_e32 v34, v2
	v_mov_b32_e32 v35, v2
	v_mov_b32_e32 v36, v2
	v_mov_b32_e32 v37, v2
	v_mov_b32_e32 v38, v2
	v_mov_b32_e32 v39, v2
	v_mov_b32_e32 v40, v2
	v_mov_b32_e32 v41, v2
	v_mov_b32_e32 v50, v2
	v_mov_b32_e32 v51, v2
	v_mov_b32_e32 v52, v2
	v_mov_b32_e32 v53, v2
	v_mov_b32_e32 v54, v2
	v_mov_b32_e32 v55, v2
	v_mov_b32_e32 v56, v2
	v_mov_b32_e32 v57, v2
	v_mov_b32_e32 v10, v2
	v_mov_b32_e32 v11, v2
	v_mov_b32_e32 v12, v2
	v_mov_b32_e32 v13, v2
	v_mov_b32_e32 v14, v2
	v_mov_b32_e32 v15, v2
	v_mov_b32_e32 v16, v2
	v_mov_b32_e32 v17, v2
	v_mov_b32_e32 v26, v2
	v_mov_b32_e32 v27, v2
	v_mov_b32_e32 v28, v2
	v_mov_b32_e32 v29, v2
	v_mov_b32_e32 v30, v2
	v_mov_b32_e32 v31, v2
	v_mov_b32_e32 v32, v2
	v_mov_b32_e32 v33, v2
	v_mov_b32_e32 v42, v2
	v_mov_b32_e32 v43, v2
	v_mov_b32_e32 v44, v2
	v_mov_b32_e32 v45, v2
	v_mov_b32_e32 v46, v2
	v_mov_b32_e32 v47, v2
	v_mov_b32_e32 v48, v2
	v_mov_b32_e32 v49, v2
	v_mov_b32_e32 v58, v2
	v_mov_b32_e32 v59, v2
	v_mov_b32_e32 v60, v2
	v_mov_b32_e32 v61, v2
	v_mov_b32_e32 v62, v2
	v_mov_b32_e32 v63, v2
	v_mov_b32_e32 v64, v2
	v_mov_b32_e32 v65, v2
	v_mov_b32_e32 v66, v2
	v_mov_b32_e32 v67, v2
	v_mov_b32_e32 v68, v2
	v_mov_b32_e32 v69, v2
	v_mov_b32_e32 v70, v2
	v_mov_b32_e32 v71, v2
	v_mov_b32_e32 v72, v2
	v_mov_b32_e32 v73, v2
	v_mov_b32_e32 v82, v2
	v_mov_b32_e32 v83, v2
	v_mov_b32_e32 v84, v2
	v_mov_b32_e32 v85, v2
	v_mov_b32_e32 v86, v2
	v_mov_b32_e32 v87, v2
	v_mov_b32_e32 v88, v2
	v_mov_b32_e32 v89, v2
	v_mov_b32_e32 v98, v2
	v_mov_b32_e32 v99, v2
	v_mov_b32_e32 v100, v2
	v_mov_b32_e32 v101, v2
	v_mov_b32_e32 v102, v2
	v_mov_b32_e32 v103, v2
	v_mov_b32_e32 v104, v2
	v_mov_b32_e32 v105, v2
	v_mov_b32_e32 v114, v2
	v_mov_b32_e32 v115, v2
	v_mov_b32_e32 v116, v2
	v_mov_b32_e32 v117, v2
	v_mov_b32_e32 v122, v2
	v_mov_b32_e32 v123, v2
	v_mov_b32_e32 v124, v2
	v_mov_b32_e32 v125, v2
	v_mov_b32_e32 v74, v2
	v_mov_b32_e32 v75, v2
	v_mov_b32_e32 v76, v2
	v_mov_b32_e32 v77, v2
	v_mov_b32_e32 v78, v2
	v_mov_b32_e32 v79, v2
	v_mov_b32_e32 v80, v2
	v_mov_b32_e32 v81, v2
	v_mov_b32_e32 v90, v2
	v_mov_b32_e32 v91, v2
	v_mov_b32_e32 v92, v2
	v_mov_b32_e32 v93, v2
	v_mov_b32_e32 v94, v2
	v_mov_b32_e32 v95, v2
	v_mov_b32_e32 v96, v2
	v_mov_b32_e32 v97, v2
	v_mov_b32_e32 v106, v2
	v_mov_b32_e32 v107, v2
	v_mov_b32_e32 v108, v2
	v_mov_b32_e32 v109, v2
	v_mov_b32_e32 v110, v2
	v_mov_b32_e32 v111, v2
	v_mov_b32_e32 v112, v2
	v_mov_b32_e32 v113, v2
	v_mov_b32_e32 v130, v2
	v_mov_b32_e32 v131, v2
	v_mov_b32_e32 v132, v2
	v_mov_b32_e32 v133, v2
	v_mov_b32_e32 v134, v2
	v_mov_b32_e32 v135, v2
	v_mov_b32_e32 v136, v2
	v_mov_b32_e32 v137, v2
	s_andn2_b64 vcc, exec, s[42:43]
	s_cbranch_vccnz .LBB0_591
	s_branch .LBB0_592

.LBB0_684:
	s_add_u32 s52, s30, s48
	s_addc_u32 s53, s31, s49
	s_add_u32 s52, s52, 0x100
	s_addc_u32 s53, s53, 0
	s_add_u32 s95, s8, s48
	s_addc_u32 s96, s9, s49
	s_add_i32 vcc_lo, 0, 0x10000
	s_cmpk_eq_i32 s48, 0x700
	s_cselect_b32 s63, s37, s53
	s_cselect_b32 s62, s59, s52
	s_cselect_b32 s53, s35, s96
	s_cselect_b32 s52, s93, s95
	s_add_i32 s95, 0, 0x14000
	v_add_u32_e32 v158, vcc_lo, v144
	v_add_u32_e32 v167, s95, v144
	ds_read_b128 v[146:149], v158
	ds_read_b128 v[150:153], v158 offset:1024
	ds_read_b128 v[154:157], v158 offset:2048
	ds_read_b128 v[158:161], v158 offset:3072
	ds_read_b128 v[162:165], v167
	ds_read_b128 v[168:171], v167 offset:1024
	ds_read_b128 v[172:175], v167 offset:2048
	ds_read_b128 v[176:179], v167 offset:3072
	v_lshl_add_u64 v[208:209], v[142:143], 0, s[48:49]
	s_add_i32 m0, s4, 0xc000
	ds_read_b128 v[180:183], v145
	ds_read_b128 v[184:187], v145 offset:1024
	ds_read_b128 v[188:191], v145 offset:2048
	ds_read_b128 v[192:195], v145 offset:3072
	ds_read_b128 v[196:199], v145 offset:4096
	ds_read_b128 v[200:203], v145 offset:5120
	ds_read_b128 v[204:207], v145 offset:6144
	ds_read_b128 v[216:219], v145 offset:7168
	global_load_lds_dwordx4 v[208:209], off
	s_add_i32 m0, s4, 0xe000
	v_lshl_add_u64 v[208:209], v[140:141], 0, s[48:49]
	global_load_lds_dwordx4 v[208:209], off
	s_waitcnt vmcnt(8) lgkmcnt(0)
	s_barrier
	v_mfma_f32_16x16x32_bf16 v[134:137], v[146:149], v[180:183], v[134:137]
	v_mfma_f32_16x16x32_bf16 v[130:133], v[154:157], v[180:183], v[130:133]
	v_mfma_f32_16x16x32_bf16 v[110:113], v[146:149], v[188:191], v[110:113]
	v_mfma_f32_16x16x32_bf16 v[106:109], v[154:157], v[188:191], v[106:109]
	v_mfma_f32_16x16x32_bf16 v[94:97], v[146:149], v[196:199], v[94:97]
	v_mfma_f32_16x16x32_bf16 v[90:93], v[154:157], v[196:199], v[90:93]
	v_mfma_f32_16x16x32_bf16 v[78:81], v[146:149], v[204:207], v[78:81]
	v_mfma_f32_16x16x32_bf16 v[74:77], v[154:157], v[204:207], v[74:77]
	v_mfma_f32_16x16x32_bf16 v[134:137], v[150:153], v[184:187], v[134:137]
	v_mfma_f32_16x16x32_bf16 v[130:133], v[158:161], v[184:187], v[130:133]
	v_mfma_f32_16x16x32_bf16 v[110:113], v[150:153], v[192:195], v[110:113]
	v_mfma_f32_16x16x32_bf16 v[106:109], v[158:161], v[192:195], v[106:109]
	v_mfma_f32_16x16x32_bf16 v[94:97], v[150:153], v[200:203], v[94:97]
	v_mfma_f32_16x16x32_bf16 v[90:93], v[158:161], v[200:203], v[90:93]
	v_mfma_f32_16x16x32_bf16 v[78:81], v[150:153], v[216:219], v[78:81]
	v_mfma_f32_16x16x32_bf16 v[74:77], v[158:161], v[216:219], v[74:77]
	v_mfma_f32_16x16x32_bf16 v[122:125], v[162:165], v[180:183], v[122:125]
	v_mfma_f32_16x16x32_bf16 v[114:117], v[172:175], v[180:183], v[114:117]
	v_mfma_f32_16x16x32_bf16 v[102:105], v[162:165], v[188:191], v[102:105]
	v_mfma_f32_16x16x32_bf16 v[98:101], v[172:175], v[188:191], v[98:101]
	v_mfma_f32_16x16x32_bf16 v[86:89], v[162:165], v[196:199], v[86:89]
	v_mfma_f32_16x16x32_bf16 v[82:85], v[172:175], v[196:199], v[82:85]
	v_mfma_f32_16x16x32_bf16 v[70:73], v[162:165], v[204:207], v[70:73]
	v_mfma_f32_16x16x32_bf16 v[66:69], v[172:175], v[204:207], v[66:69]
	v_mfma_f32_16x16x32_bf16 v[122:125], v[168:171], v[184:187], v[122:125]
	v_mfma_f32_16x16x32_bf16 v[114:117], v[176:179], v[184:187], v[114:117]
	v_mfma_f32_16x16x32_bf16 v[102:105], v[168:171], v[192:195], v[102:105]
	v_mfma_f32_16x16x32_bf16 v[98:101], v[176:179], v[192:195], v[98:101]
	v_mfma_f32_16x16x32_bf16 v[86:89], v[168:171], v[200:203], v[86:89]
	v_mfma_f32_16x16x32_bf16 v[82:85], v[176:179], v[200:203], v[82:85]
	v_mfma_f32_16x16x32_bf16 v[70:73], v[168:171], v[216:219], v[70:73]
	v_mfma_f32_16x16x32_bf16 v[66:69], v[176:179], v[216:219], v[66:69]
	s_barrier
	s_add_i32 s96, vcc_lo, s77
	v_lshl_add_u64 v[208:209], s[52:53], 0, v[0:1]
	s_mov_b32 m0, s96
	ds_read_b128 v[180:183], v145 offset:16384
	ds_read_b128 v[184:187], v145 offset:17408
	ds_read_b128 v[188:191], v145 offset:18432
	ds_read_b128 v[192:195], v145 offset:19456
	ds_read_b128 v[196:199], v145 offset:20480
	ds_read_b128 v[200:203], v145 offset:21504
	ds_read_b128 v[204:207], v145 offset:22528
	ds_read_b128 v[216:219], v145 offset:23552
	global_load_lds_dwordx4 v0, s[52:53]
	s_add_i32 m0, s96, 0x2000
	s_add_u32 vcc_lo, s52, 0x40000
	v_lshl_add_u64 v[220:221], s[52:53], 0, v[118:119]
	s_addc_u32 vcc_hi, s53, 0
	s_add_i32 s95, s95, s77
	global_load_lds_dwordx4 v118, s[52:53]
	v_lshl_add_u64 v[222:223], vcc, 0, v[0:1]
	s_mov_b32 m0, s95
	v_lshl_add_u64 v[224:225], s[62:63], 0, v[120:121]
	global_load_lds_dwordx4 v[222:223], off
	s_add_i32 m0, s95, 0x2000
	v_lshl_add_u64 v[222:223], vcc, 0, v[118:119]
	global_load_lds_dwordx4 v[222:223], off
	s_mov_b32 m0, s4
	v_lshl_add_u64 v[222:223], s[62:63], 0, v[126:127]
	global_load_lds_dwordx4 v126, s[62:63]
	s_mov_b32 m0, s5
	s_nop 0
	global_load_lds_dwordx4 v120, s[62:63]
	s_waitcnt vmcnt(8) lgkmcnt(0)
	s_barrier
	v_mfma_f32_16x16x32_bf16 v[62:65], v[146:149], v[180:183], v[62:65]
	v_mfma_f32_16x16x32_bf16 v[58:61], v[154:157], v[180:183], v[58:61]
	v_mfma_f32_16x16x32_bf16 v[46:49], v[146:149], v[188:191], v[46:49]
	v_mfma_f32_16x16x32_bf16 v[42:45], v[154:157], v[188:191], v[42:45]
	v_mfma_f32_16x16x32_bf16 v[30:33], v[146:149], v[196:199], v[30:33]
	v_mfma_f32_16x16x32_bf16 v[26:29], v[154:157], v[196:199], v[26:29]
	v_mfma_f32_16x16x32_bf16 v[14:17], v[146:149], v[204:207], v[14:17]
	v_mfma_f32_16x16x32_bf16 v[10:13], v[154:157], v[204:207], v[10:13]
	v_mfma_f32_16x16x32_bf16 v[62:65], v[150:153], v[184:187], v[62:65]
	v_mfma_f32_16x16x32_bf16 v[58:61], v[158:161], v[184:187], v[58:61]
	v_mfma_f32_16x16x32_bf16 v[46:49], v[150:153], v[192:195], v[46:49]
	v_mfma_f32_16x16x32_bf16 v[42:45], v[158:161], v[192:195], v[42:45]
	v_mfma_f32_16x16x32_bf16 v[30:33], v[150:153], v[200:203], v[30:33]
	v_mfma_f32_16x16x32_bf16 v[26:29], v[158:161], v[200:203], v[26:29]
	v_mfma_f32_16x16x32_bf16 v[14:17], v[150:153], v[216:219], v[14:17]
	v_mfma_f32_16x16x32_bf16 v[10:13], v[158:161], v[216:219], v[10:13]
	v_mfma_f32_16x16x32_bf16 v[54:57], v[162:165], v[180:183], v[54:57]
	v_mfma_f32_16x16x32_bf16 v[50:53], v[172:175], v[180:183], v[50:53]
	v_mfma_f32_16x16x32_bf16 v[38:41], v[162:165], v[188:191], v[38:41]
	v_mfma_f32_16x16x32_bf16 v[34:37], v[172:175], v[188:191], v[34:37]
	v_mfma_f32_16x16x32_bf16 v[22:25], v[162:165], v[196:199], v[22:25]
	v_mfma_f32_16x16x32_bf16 v[18:21], v[172:175], v[196:199], v[18:21]
	v_mfma_f32_16x16x32_bf16 v[6:9], v[162:165], v[204:207], v[6:9]
	v_mfma_f32_16x16x32_bf16 v[2:5], v[172:175], v[204:207], v[2:5]
	v_mfma_f32_16x16x32_bf16 v[54:57], v[168:171], v[184:187], v[54:57]
	v_mfma_f32_16x16x32_bf16 v[50:53], v[176:179], v[184:187], v[50:53]
	v_mfma_f32_16x16x32_bf16 v[38:41], v[168:171], v[192:195], v[38:41]
	v_mfma_f32_16x16x32_bf16 v[34:37], v[176:179], v[192:195], v[34:37]
	v_mfma_f32_16x16x32_bf16 v[22:25], v[168:171], v[200:203], v[22:25]
	v_mfma_f32_16x16x32_bf16 v[18:21], v[176:179], v[200:203], v[18:21]
	v_mfma_f32_16x16x32_bf16 v[6:9], v[168:171], v[216:219], v[6:9]
	v_mfma_f32_16x16x32_bf16 v[2:5], v[176:179], v[216:219], v[2:5]
	s_barrier
	s_add_i32 s95, 0, 0x18000
	s_add_i32 s96, 0, 0x1c000
	v_add_u32_e32 v158, s95, v144
	v_add_u32_e32 v167, s96, v144
	ds_read_b128 v[146:149], v158
	ds_read_b128 v[150:153], v158 offset:1024
	ds_read_b128 v[154:157], v158 offset:2048
	ds_read_b128 v[158:161], v158 offset:3072
	ds_read_b128 v[162:165], v167
	ds_read_b128 v[168:171], v167 offset:1024
	ds_read_b128 v[172:175], v167 offset:2048
	ds_read_b128 v[176:179], v167 offset:3072
	s_add_u32 s62, s62, 0x40000
	s_addc_u32 s63, s63, 0
	s_mov_b32 m0, s33
	ds_read_b128 v[180:183], v145 offset:32768
	ds_read_b128 v[184:187], v145 offset:33792
	ds_read_b128 v[188:191], v145 offset:34816
	ds_read_b128 v[192:195], v145 offset:35840
	ds_read_b128 v[196:199], v145 offset:36864
	ds_read_b128 v[200:203], v145 offset:37888
	ds_read_b128 v[204:207], v145 offset:38912
	ds_read_b128 v[216:219], v145 offset:39936
	global_load_lds_dwordx4 v126, s[62:63]
	s_mov_b32 m0, s84
	v_lshl_add_u64 v[242:243], s[62:63], 0, v[120:121]
	global_load_lds_dwordx4 v120, s[62:63]
	s_waitcnt vmcnt(8) lgkmcnt(0)
	s_barrier
	v_mfma_f32_16x16x32_bf16 v[134:137], v[146:149], v[180:183], v[134:137]
	v_mfma_f32_16x16x32_bf16 v[130:133], v[154:157], v[180:183], v[130:133]
	v_mfma_f32_16x16x32_bf16 v[110:113], v[146:149], v[188:191], v[110:113]
	v_mfma_f32_16x16x32_bf16 v[106:109], v[154:157], v[188:191], v[106:109]
	v_mfma_f32_16x16x32_bf16 v[94:97], v[146:149], v[196:199], v[94:97]
	v_mfma_f32_16x16x32_bf16 v[90:93], v[154:157], v[196:199], v[90:93]
	v_mfma_f32_16x16x32_bf16 v[78:81], v[146:149], v[204:207], v[78:81]
	v_mfma_f32_16x16x32_bf16 v[74:77], v[154:157], v[204:207], v[74:77]
	v_mfma_f32_16x16x32_bf16 v[134:137], v[150:153], v[184:187], v[134:137]
	v_mfma_f32_16x16x32_bf16 v[130:133], v[158:161], v[184:187], v[130:133]
	v_mfma_f32_16x16x32_bf16 v[110:113], v[150:153], v[192:195], v[110:113]
	v_mfma_f32_16x16x32_bf16 v[106:109], v[158:161], v[192:195], v[106:109]
	v_mfma_f32_16x16x32_bf16 v[94:97], v[150:153], v[200:203], v[94:97]
	v_mfma_f32_16x16x32_bf16 v[90:93], v[158:161], v[200:203], v[90:93]
	v_mfma_f32_16x16x32_bf16 v[78:81], v[150:153], v[216:219], v[78:81]
	v_mfma_f32_16x16x32_bf16 v[74:77], v[158:161], v[216:219], v[74:77]
	v_mfma_f32_16x16x32_bf16 v[122:125], v[162:165], v[180:183], v[122:125]
	v_mfma_f32_16x16x32_bf16 v[114:117], v[172:175], v[180:183], v[114:117]
	v_mfma_f32_16x16x32_bf16 v[102:105], v[162:165], v[188:191], v[102:105]
	v_mfma_f32_16x16x32_bf16 v[98:101], v[172:175], v[188:191], v[98:101]
	v_mfma_f32_16x16x32_bf16 v[86:89], v[162:165], v[196:199], v[86:89]
	v_mfma_f32_16x16x32_bf16 v[82:85], v[172:175], v[196:199], v[82:85]
	v_mfma_f32_16x16x32_bf16 v[70:73], v[162:165], v[204:207], v[70:73]
	v_mfma_f32_16x16x32_bf16 v[66:69], v[172:175], v[204:207], v[66:69]
	v_mfma_f32_16x16x32_bf16 v[122:125], v[168:171], v[184:187], v[122:125]
	v_mfma_f32_16x16x32_bf16 v[114:117], v[176:179], v[184:187], v[114:117]
	v_mfma_f32_16x16x32_bf16 v[102:105], v[168:171], v[192:195], v[102:105]
	v_mfma_f32_16x16x32_bf16 v[98:101], v[176:179], v[192:195], v[98:101]
	v_mfma_f32_16x16x32_bf16 v[86:89], v[168:171], v[200:203], v[86:89]
	v_mfma_f32_16x16x32_bf16 v[82:85], v[176:179], v[200:203], v[82:85]
	v_mfma_f32_16x16x32_bf16 v[70:73], v[168:171], v[216:219], v[70:73]
	v_mfma_f32_16x16x32_bf16 v[66:69], v[176:179], v[216:219], v[66:69]
	s_barrier
	s_add_i32 s62, s95, s77
	v_lshl_add_u64 v[208:209], v[208:209], 0, s[56:57]
	s_mov_b32 m0, s62
	ds_read_b128 v[180:183], v145 offset:49152
	ds_read_b128 v[184:187], v145 offset:50176
	ds_read_b128 v[188:191], v145 offset:51200
	ds_read_b128 v[192:195], v145 offset:52224
	ds_read_b128 v[196:199], v145 offset:53248
	ds_read_b128 v[200:203], v145 offset:54272
	ds_read_b128 v[204:207], v145 offset:55296
	ds_read_b128 v[216:219], v145 offset:56320
	global_load_lds_dwordx4 v[208:209], off
	s_add_i32 m0, s62, 0x2000
	s_add_u32 s52, s52, 0x40080
	v_lshl_add_u64 v[208:209], v[220:221], 0, s[56:57]
	s_addc_u32 s53, s53, 0
	s_add_i32 s62, s96, s77
	global_load_lds_dwordx4 v[208:209], off
	s_mov_b32 m0, s62
	s_nop 0
	global_load_lds_dwordx4 v0, s[52:53]
	s_add_i32 m0, s62, 0x2000
	s_nop 0
	global_load_lds_dwordx4 v118, s[52:53]
	s_mov_b32 m0, s85
	v_lshl_add_u64 v[208:209], v[222:223], 0, s[56:57]
	global_load_lds_dwordx4 v[208:209], off
	s_mov_b32 m0, s90
	v_lshl_add_u64 v[208:209], v[224:225], 0, s[56:57]
	global_load_lds_dwordx4 v[208:209], off
	s_waitcnt vmcnt(8) lgkmcnt(0)
	s_barrier
	v_mfma_f32_16x16x32_bf16 v[62:65], v[146:149], v[180:183], v[62:65]
	v_mfma_f32_16x16x32_bf16 v[58:61], v[154:157], v[180:183], v[58:61]
	v_mfma_f32_16x16x32_bf16 v[46:49], v[146:149], v[188:191], v[46:49]
	v_mfma_f32_16x16x32_bf16 v[42:45], v[154:157], v[188:191], v[42:45]
	v_mfma_f32_16x16x32_bf16 v[30:33], v[146:149], v[196:199], v[30:33]
	v_mfma_f32_16x16x32_bf16 v[26:29], v[154:157], v[196:199], v[26:29]
	v_mfma_f32_16x16x32_bf16 v[14:17], v[146:149], v[204:207], v[14:17]
	v_mfma_f32_16x16x32_bf16 v[10:13], v[154:157], v[204:207], v[10:13]
	v_mfma_f32_16x16x32_bf16 v[62:65], v[150:153], v[184:187], v[62:65]
	v_mfma_f32_16x16x32_bf16 v[58:61], v[158:161], v[184:187], v[58:61]
	v_mfma_f32_16x16x32_bf16 v[46:49], v[150:153], v[192:195], v[46:49]
	v_mfma_f32_16x16x32_bf16 v[42:45], v[158:161], v[192:195], v[42:45]
	v_mfma_f32_16x16x32_bf16 v[30:33], v[150:153], v[200:203], v[30:33]
	v_mfma_f32_16x16x32_bf16 v[26:29], v[158:161], v[200:203], v[26:29]
	v_mfma_f32_16x16x32_bf16 v[14:17], v[150:153], v[216:219], v[14:17]
	v_mfma_f32_16x16x32_bf16 v[10:13], v[158:161], v[216:219], v[10:13]
	v_mfma_f32_16x16x32_bf16 v[54:57], v[162:165], v[180:183], v[54:57]
	v_mfma_f32_16x16x32_bf16 v[50:53], v[172:175], v[180:183], v[50:53]
	v_mfma_f32_16x16x32_bf16 v[38:41], v[162:165], v[188:191], v[38:41]
	v_mfma_f32_16x16x32_bf16 v[34:37], v[172:175], v[188:191], v[34:37]
	v_mfma_f32_16x16x32_bf16 v[22:25], v[162:165], v[196:199], v[22:25]
	v_mfma_f32_16x16x32_bf16 v[18:21], v[172:175], v[196:199], v[18:21]
	v_mfma_f32_16x16x32_bf16 v[6:9], v[162:165], v[204:207], v[6:9]
	v_mfma_f32_16x16x32_bf16 v[2:5], v[172:175], v[204:207], v[2:5]
	v_mfma_f32_16x16x32_bf16 v[54:57], v[168:171], v[184:187], v[54:57]
	v_mfma_f32_16x16x32_bf16 v[50:53], v[176:179], v[184:187], v[50:53]
	v_mfma_f32_16x16x32_bf16 v[38:41], v[168:171], v[192:195], v[38:41]
	v_mfma_f32_16x16x32_bf16 v[34:37], v[176:179], v[192:195], v[34:37]
	v_mfma_f32_16x16x32_bf16 v[22:25], v[168:171], v[200:203], v[22:25]
	v_mfma_f32_16x16x32_bf16 v[18:21], v[176:179], v[200:203], v[18:21]
	v_mfma_f32_16x16x32_bf16 v[6:9], v[168:171], v[216:219], v[6:9]
	v_mfma_f32_16x16x32_bf16 v[2:5], v[176:179], v[216:219], v[2:5]
	s_barrier
	s_add_i32 s94, s94, 2
	s_add_u32 s48, s48, 0x100
	s_addc_u32 s49, s49, 0
	s_cmp_gt_u32 s94, 13
	s_cbranch_scc0 .LBB0_684
	s_add_u32 s48, s8, 0xffffff00
	s_addc_u32 s49, s9, -1
	s_andn2_b64 vcc, exec, s[42:43]
	s_cbranch_vccnz .LBB0_687
	v_mov_b32_e32 v2, 0
	s_mov_b32 s18, s34
	s_mov_b32 s92, s36
	s_mov_b64 s[30:31], s[46:47]
	s_mov_b32 s68, s58
	v_mov_b32_e32 v3, v2
	v_mov_b32_e32 v4, v2
	v_mov_b32_e32 v5, v2
	v_mov_b32_e32 v6, v2
	v_mov_b32_e32 v7, v2
	v_mov_b32_e32 v8, v2
	v_mov_b32_e32 v9, v2
	v_mov_b32_e32 v18, v2
	v_mov_b32_e32 v19, v2
	v_mov_b32_e32 v20, v2
	v_mov_b32_e32 v21, v2
	v_mov_b32_e32 v22, v2
	v_mov_b32_e32 v23, v2
	v_mov_b32_e32 v24, v2
	v_mov_b32_e32 v25, v2
	v_mov_b32_e32 v34, v2
	v_mov_b32_e32 v35, v2
	v_mov_b32_e32 v36, v2
	v_mov_b32_e32 v37, v2
	v_mov_b32_e32 v38, v2
	v_mov_b32_e32 v39, v2
	v_mov_b32_e32 v40, v2
	v_mov_b32_e32 v41, v2
	v_mov_b32_e32 v50, v2
	v_mov_b32_e32 v51, v2
	v_mov_b32_e32 v52, v2
	v_mov_b32_e32 v53, v2
	v_mov_b32_e32 v54, v2
	v_mov_b32_e32 v55, v2
	v_mov_b32_e32 v56, v2
	v_mov_b32_e32 v57, v2
	v_mov_b32_e32 v10, v2
	v_mov_b32_e32 v11, v2
	v_mov_b32_e32 v12, v2
	v_mov_b32_e32 v13, v2
	v_mov_b32_e32 v14, v2
	v_mov_b32_e32 v15, v2
	v_mov_b32_e32 v16, v2
	v_mov_b32_e32 v17, v2
	v_mov_b32_e32 v26, v2
	v_mov_b32_e32 v27, v2
	v_mov_b32_e32 v28, v2
	v_mov_b32_e32 v29, v2
	v_mov_b32_e32 v30, v2
	v_mov_b32_e32 v31, v2
	v_mov_b32_e32 v32, v2
	v_mov_b32_e32 v33, v2
	v_mov_b32_e32 v42, v2
	v_mov_b32_e32 v43, v2
	v_mov_b32_e32 v44, v2
	v_mov_b32_e32 v45, v2
	v_mov_b32_e32 v46, v2
	v_mov_b32_e32 v47, v2
	v_mov_b32_e32 v48, v2
	v_mov_b32_e32 v49, v2
	v_mov_b32_e32 v58, v2
	v_mov_b32_e32 v59, v2
	v_mov_b32_e32 v60, v2
	v_mov_b32_e32 v61, v2
	v_mov_b32_e32 v62, v2
	v_mov_b32_e32 v63, v2
	v_mov_b32_e32 v64, v2
	v_mov_b32_e32 v65, v2
	v_mov_b32_e32 v66, v2
	v_mov_b32_e32 v67, v2
	v_mov_b32_e32 v68, v2
	v_mov_b32_e32 v69, v2
	v_mov_b32_e32 v70, v2
	v_mov_b32_e32 v71, v2
	v_mov_b32_e32 v72, v2
	v_mov_b32_e32 v73, v2
	v_mov_b32_e32 v82, v2
	v_mov_b32_e32 v83, v2
	v_mov_b32_e32 v84, v2
	v_mov_b32_e32 v85, v2
	v_mov_b32_e32 v86, v2
	v_mov_b32_e32 v87, v2
	v_mov_b32_e32 v88, v2
	v_mov_b32_e32 v89, v2
	v_mov_b32_e32 v98, v2
	v_mov_b32_e32 v99, v2
	v_mov_b32_e32 v100, v2
	v_mov_b32_e32 v101, v2
	v_mov_b32_e32 v102, v2
	v_mov_b32_e32 v103, v2
	v_mov_b32_e32 v104, v2
	v_mov_b32_e32 v105, v2
	v_mov_b32_e32 v114, v2
	v_mov_b32_e32 v115, v2
	v_mov_b32_e32 v116, v2
	v_mov_b32_e32 v117, v2
	v_mov_b32_e32 v122, v2
	v_mov_b32_e32 v123, v2
	v_mov_b32_e32 v124, v2
	v_mov_b32_e32 v125, v2
	v_mov_b32_e32 v74, v2
	v_mov_b32_e32 v75, v2
	v_mov_b32_e32 v76, v2
	v_mov_b32_e32 v77, v2
	v_mov_b32_e32 v78, v2
	v_mov_b32_e32 v79, v2
	v_mov_b32_e32 v80, v2
	v_mov_b32_e32 v81, v2
	v_mov_b32_e32 v90, v2
	v_mov_b32_e32 v91, v2
	v_mov_b32_e32 v92, v2
	v_mov_b32_e32 v93, v2
	v_mov_b32_e32 v94, v2
	v_mov_b32_e32 v95, v2
	v_mov_b32_e32 v96, v2
	v_mov_b32_e32 v97, v2
	v_mov_b32_e32 v106, v2
	v_mov_b32_e32 v107, v2
	v_mov_b32_e32 v108, v2
	v_mov_b32_e32 v109, v2
	v_mov_b32_e32 v110, v2
	v_mov_b32_e32 v111, v2
	v_mov_b32_e32 v112, v2
	v_mov_b32_e32 v113, v2
	v_mov_b32_e32 v130, v2
	v_mov_b32_e32 v131, v2
	v_mov_b32_e32 v132, v2
	v_mov_b32_e32 v133, v2
	v_mov_b32_e32 v134, v2
	v_mov_b32_e32 v135, v2
	v_mov_b32_e32 v136, v2
	v_mov_b32_e32 v137, v2
	s_branch .LBB0_688

.LBB0_836:
	s_add_u32 s28, s6, 0xfffc0080
	s_addc_u32 s29, s7, -1
	s_add_i32 s41, 0, 0x10000
	s_cmp_eq_u32 s40, 12
	s_cselect_b32 s31, s5, s29
	s_cselect_b32 s30, s8, s28
	s_cselect_b32 s29, s9, s33
	s_cselect_b32 s28, s21, s23
	s_add_i32 s53, 0, 0x14000
	ds_read_b128 v[130:133], v165
	ds_read_b128 v[134:137], v165 offset:1024
	ds_read_b128 v[138:141], v165 offset:2048
	ds_read_b128 v[142:145], v165 offset:3072
	ds_read_b128 v[146:149], v165 offset:16384
	ds_read_b128 v[150:153], v165 offset:17408
	ds_read_b128 v[154:157], v165 offset:18432
	ds_read_b128 v[168:171], v165 offset:19456
	s_add_i32 m0, s43, 0xc000
	ds_read_b128 v[172:175], v188
	ds_read_b128 v[176:179], v188 offset:1024
	ds_read_b128 v[180:183], v188 offset:2048
	ds_read_b128 v[190:193], v188 offset:3072
	ds_read_b128 v[194:197], v188 offset:4096
	ds_read_b128 v[198:201], v188 offset:5120
	ds_read_b128 v[202:205], v188 offset:6144
	global_load_lds_dwordx4 v166, s[6:7]
	s_add_i32 m0, s43, 0xe000
	ds_read_b128 v[206:209], v188 offset:7168
	global_load_lds_dwordx4 v164, s[6:7]
	s_waitcnt vmcnt(8) lgkmcnt(0)
	s_barrier
	v_mfma_f32_16x16x32_bf16 v[126:129], v[130:133], v[172:175], v[126:129]
	v_mfma_f32_16x16x32_bf16 v[122:125], v[138:141], v[172:175], v[122:125]
	v_mfma_f32_16x16x32_bf16 v[114:117], v[130:133], v[180:183], v[114:117]
	v_mfma_f32_16x16x32_bf16 v[106:109], v[138:141], v[180:183], v[106:109]
	v_mfma_f32_16x16x32_bf16 v[98:101], v[130:133], v[194:197], v[98:101]
	v_mfma_f32_16x16x32_bf16 v[90:93], v[138:141], v[194:197], v[90:93]
	v_mfma_f32_16x16x32_bf16 v[82:85], v[130:133], v[202:205], v[82:85]
	v_mfma_f32_16x16x32_bf16 v[74:77], v[138:141], v[202:205], v[74:77]
	v_mfma_f32_16x16x32_bf16 v[126:129], v[134:137], v[176:179], v[126:129]
	v_mfma_f32_16x16x32_bf16 v[122:125], v[142:145], v[176:179], v[122:125]
	v_mfma_f32_16x16x32_bf16 v[114:117], v[134:137], v[190:193], v[114:117]
	v_mfma_f32_16x16x32_bf16 v[106:109], v[142:145], v[190:193], v[106:109]
	v_mfma_f32_16x16x32_bf16 v[98:101], v[134:137], v[198:201], v[98:101]
	v_mfma_f32_16x16x32_bf16 v[90:93], v[142:145], v[198:201], v[90:93]
	v_mfma_f32_16x16x32_bf16 v[82:85], v[134:137], v[206:209], v[82:85]
	v_mfma_f32_16x16x32_bf16 v[74:77], v[142:145], v[206:209], v[74:77]
	v_mfma_f32_16x16x32_bf16 v[118:121], v[146:149], v[172:175], v[118:121]
	v_mfma_f32_16x16x32_bf16 v[110:113], v[154:157], v[172:175], v[110:113]
	v_mfma_f32_16x16x32_bf16 v[102:105], v[146:149], v[180:183], v[102:105]
	v_mfma_f32_16x16x32_bf16 v[94:97], v[154:157], v[180:183], v[94:97]
	v_mfma_f32_16x16x32_bf16 v[86:89], v[146:149], v[194:197], v[86:89]
	v_mfma_f32_16x16x32_bf16 v[78:81], v[154:157], v[194:197], v[78:81]
	v_mfma_f32_16x16x32_bf16 v[70:73], v[146:149], v[202:205], v[70:73]
	v_mfma_f32_16x16x32_bf16 v[66:69], v[154:157], v[202:205], v[66:69]
	v_mfma_f32_16x16x32_bf16 v[118:121], v[150:153], v[176:179], v[118:121]
	v_mfma_f32_16x16x32_bf16 v[110:113], v[168:171], v[176:179], v[110:113]
	v_mfma_f32_16x16x32_bf16 v[102:105], v[150:153], v[190:193], v[102:105]
	v_mfma_f32_16x16x32_bf16 v[94:97], v[168:171], v[190:193], v[94:97]
	v_mfma_f32_16x16x32_bf16 v[86:89], v[150:153], v[198:201], v[86:89]
	v_mfma_f32_16x16x32_bf16 v[78:81], v[168:171], v[198:201], v[78:81]
	v_mfma_f32_16x16x32_bf16 v[70:73], v[150:153], v[206:209], v[70:73]
	v_mfma_f32_16x16x32_bf16 v[66:69], v[168:171], v[206:209], v[66:69]
	s_barrier
	s_add_i32 s41, s41, s42
	v_lshl_add_u64 v[216:217], s[28:29], 0, v[0:1]
	s_mov_b32 m0, s41
	ds_read_b128 v[172:175], v188 offset:16384
	ds_read_b128 v[176:179], v188 offset:17408
	ds_read_b128 v[180:183], v188 offset:18432
	ds_read_b128 v[190:193], v188 offset:19456
	ds_read_b128 v[194:197], v188 offset:20480
	ds_read_b128 v[198:201], v188 offset:21504
	ds_read_b128 v[202:205], v188 offset:22528
	ds_read_b128 v[206:209], v188 offset:23552
	global_load_lds_dwordx4 v0, s[28:29]
	s_add_i32 m0, s41, 0x2000
	s_add_u32 s58, s28, 0x40000
	v_lshl_add_u64 v[218:219], s[28:29], 0, v[158:159]
	s_addc_u32 s59, s29, 0
	s_add_i32 s41, s53, s42
	global_load_lds_dwordx4 v158, s[28:29]
	s_mov_b32 m0, s41
	v_lshl_add_u64 v[222:223], s[30:31], 0, v[160:161]
	global_load_lds_dwordx4 v0, s[58:59]
	s_add_i32 m0, s41, 0x2000
	s_nop 0
	global_load_lds_dwordx4 v158, s[58:59]
	s_mov_b32 m0, s43
	v_lshl_add_u64 v[220:221], s[30:31], 0, v[162:163]
	global_load_lds_dwordx4 v162, s[30:31]
	s_mov_b32 m0, s44
	s_nop 0
	global_load_lds_dwordx4 v160, s[30:31]
	s_waitcnt vmcnt(8) lgkmcnt(0)
	s_barrier
	v_mfma_f32_16x16x32_bf16 v[62:65], v[130:133], v[172:175], v[62:65]
	v_mfma_f32_16x16x32_bf16 v[58:61], v[138:141], v[172:175], v[58:61]
	v_mfma_f32_16x16x32_bf16 v[50:53], v[130:133], v[180:183], v[50:53]
	v_mfma_f32_16x16x32_bf16 v[42:45], v[138:141], v[180:183], v[42:45]
	v_mfma_f32_16x16x32_bf16 v[34:37], v[130:133], v[194:197], v[34:37]
	v_mfma_f32_16x16x32_bf16 v[26:29], v[138:141], v[194:197], v[26:29]
	v_mfma_f32_16x16x32_bf16 v[18:21], v[130:133], v[202:205], v[18:21]
	v_mfma_f32_16x16x32_bf16 v[10:13], v[138:141], v[202:205], v[10:13]
	v_mfma_f32_16x16x32_bf16 v[62:65], v[134:137], v[176:179], v[62:65]
	v_mfma_f32_16x16x32_bf16 v[58:61], v[142:145], v[176:179], v[58:61]
	v_mfma_f32_16x16x32_bf16 v[50:53], v[134:137], v[190:193], v[50:53]
	v_mfma_f32_16x16x32_bf16 v[42:45], v[142:145], v[190:193], v[42:45]
	v_mfma_f32_16x16x32_bf16 v[34:37], v[134:137], v[198:201], v[34:37]
	v_mfma_f32_16x16x32_bf16 v[26:29], v[142:145], v[198:201], v[26:29]
	v_mfma_f32_16x16x32_bf16 v[18:21], v[134:137], v[206:209], v[18:21]
	v_mfma_f32_16x16x32_bf16 v[10:13], v[142:145], v[206:209], v[10:13]
	v_mfma_f32_16x16x32_bf16 v[54:57], v[146:149], v[172:175], v[54:57]
	v_mfma_f32_16x16x32_bf16 v[46:49], v[154:157], v[172:175], v[46:49]
	v_mfma_f32_16x16x32_bf16 v[38:41], v[146:149], v[180:183], v[38:41]
	v_mfma_f32_16x16x32_bf16 v[30:33], v[154:157], v[180:183], v[30:33]
	v_mfma_f32_16x16x32_bf16 v[22:25], v[146:149], v[194:197], v[22:25]
	v_mfma_f32_16x16x32_bf16 v[14:17], v[154:157], v[194:197], v[14:17]
	v_mfma_f32_16x16x32_bf16 v[6:9], v[146:149], v[202:205], v[6:9]
	v_mfma_f32_16x16x32_bf16 v[2:5], v[154:157], v[202:205], v[2:5]
	v_mfma_f32_16x16x32_bf16 v[54:57], v[150:153], v[176:179], v[54:57]
	v_mfma_f32_16x16x32_bf16 v[46:49], v[168:171], v[176:179], v[46:49]
	v_mfma_f32_16x16x32_bf16 v[38:41], v[150:153], v[190:193], v[38:41]
	v_mfma_f32_16x16x32_bf16 v[30:33], v[168:171], v[190:193], v[30:33]
	v_mfma_f32_16x16x32_bf16 v[22:25], v[150:153], v[198:201], v[22:25]
	v_mfma_f32_16x16x32_bf16 v[14:17], v[168:171], v[198:201], v[14:17]
	v_mfma_f32_16x16x32_bf16 v[6:9], v[150:153], v[206:209], v[6:9]
	v_mfma_f32_16x16x32_bf16 v[2:5], v[168:171], v[206:209], v[2:5]
	s_barrier
	s_add_i32 s41, 0, 0x18000
	s_add_i32 s53, 0, 0x1c000
	ds_read_b128 v[130:133], v165 offset:32768
	ds_read_b128 v[134:137], v165 offset:33792
	ds_read_b128 v[138:141], v165 offset:34816
	ds_read_b128 v[142:145], v165 offset:35840
	ds_read_b128 v[146:149], v165 offset:49152
	ds_read_b128 v[150:153], v165 offset:50176
	ds_read_b128 v[154:157], v165 offset:51200
	ds_read_b128 v[168:171], v165 offset:52224
	s_add_u32 s30, s30, 0x40000
	s_addc_u32 s31, s31, 0
	s_mov_b32 m0, s45
	ds_read_b128 v[172:175], v188 offset:32768
	ds_read_b128 v[176:179], v188 offset:33792
	ds_read_b128 v[180:183], v188 offset:34816
	ds_read_b128 v[190:193], v188 offset:35840
	ds_read_b128 v[194:197], v188 offset:36864
	ds_read_b128 v[198:201], v188 offset:37888
	ds_read_b128 v[202:205], v188 offset:38912
	global_load_lds_dwordx4 v162, s[30:31]
	s_mov_b32 m0, s46
	ds_read_b128 v[206:209], v188 offset:39936
	global_load_lds_dwordx4 v160, s[30:31]
	s_waitcnt vmcnt(8) lgkmcnt(0)
	s_barrier
	v_mfma_f32_16x16x32_bf16 v[126:129], v[130:133], v[172:175], v[126:129]
	v_mfma_f32_16x16x32_bf16 v[122:125], v[138:141], v[172:175], v[122:125]
	v_mfma_f32_16x16x32_bf16 v[114:117], v[130:133], v[180:183], v[114:117]
	v_mfma_f32_16x16x32_bf16 v[106:109], v[138:141], v[180:183], v[106:109]
	v_mfma_f32_16x16x32_bf16 v[98:101], v[130:133], v[194:197], v[98:101]
	v_mfma_f32_16x16x32_bf16 v[90:93], v[138:141], v[194:197], v[90:93]
	v_mfma_f32_16x16x32_bf16 v[82:85], v[130:133], v[202:205], v[82:85]
	v_mfma_f32_16x16x32_bf16 v[74:77], v[138:141], v[202:205], v[74:77]
	v_mfma_f32_16x16x32_bf16 v[126:129], v[134:137], v[176:179], v[126:129]
	v_mfma_f32_16x16x32_bf16 v[122:125], v[142:145], v[176:179], v[122:125]
	v_mfma_f32_16x16x32_bf16 v[114:117], v[134:137], v[190:193], v[114:117]
	v_mfma_f32_16x16x32_bf16 v[106:109], v[142:145], v[190:193], v[106:109]
	v_mfma_f32_16x16x32_bf16 v[98:101], v[134:137], v[198:201], v[98:101]
	v_mfma_f32_16x16x32_bf16 v[90:93], v[142:145], v[198:201], v[90:93]
	v_mfma_f32_16x16x32_bf16 v[82:85], v[134:137], v[206:209], v[82:85]
	v_mfma_f32_16x16x32_bf16 v[74:77], v[142:145], v[206:209], v[74:77]
	v_mfma_f32_16x16x32_bf16 v[118:121], v[146:149], v[172:175], v[118:121]
	v_mfma_f32_16x16x32_bf16 v[110:113], v[154:157], v[172:175], v[110:113]
	v_mfma_f32_16x16x32_bf16 v[102:105], v[146:149], v[180:183], v[102:105]
	v_mfma_f32_16x16x32_bf16 v[94:97], v[154:157], v[180:183], v[94:97]
	v_mfma_f32_16x16x32_bf16 v[86:89], v[146:149], v[194:197], v[86:89]
	v_mfma_f32_16x16x32_bf16 v[78:81], v[154:157], v[194:197], v[78:81]
	v_mfma_f32_16x16x32_bf16 v[70:73], v[146:149], v[202:205], v[70:73]
	v_mfma_f32_16x16x32_bf16 v[66:69], v[154:157], v[202:205], v[66:69]
	v_mfma_f32_16x16x32_bf16 v[118:121], v[150:153], v[176:179], v[118:121]
	v_mfma_f32_16x16x32_bf16 v[110:113], v[168:171], v[176:179], v[110:113]
	v_mfma_f32_16x16x32_bf16 v[102:105], v[150:153], v[190:193], v[102:105]
	v_mfma_f32_16x16x32_bf16 v[94:97], v[168:171], v[190:193], v[94:97]
	v_mfma_f32_16x16x32_bf16 v[86:89], v[150:153], v[198:201], v[86:89]
	v_mfma_f32_16x16x32_bf16 v[78:81], v[168:171], v[198:201], v[78:81]
	v_mfma_f32_16x16x32_bf16 v[70:73], v[150:153], v[206:209], v[70:73]
	v_mfma_f32_16x16x32_bf16 v[66:69], v[168:171], v[206:209], v[66:69]
	s_barrier
	s_add_i32 s30, s41, s42
	v_lshl_add_u64 v[216:217], v[216:217], 0, s[56:57]
	s_mov_b32 m0, s30
	ds_read_b128 v[172:175], v188 offset:49152
	ds_read_b128 v[176:179], v188 offset:50176
	ds_read_b128 v[180:183], v188 offset:51200
	ds_read_b128 v[190:193], v188 offset:52224
	ds_read_b128 v[194:197], v188 offset:53248
	ds_read_b128 v[198:201], v188 offset:54272
	ds_read_b128 v[202:205], v188 offset:55296
	ds_read_b128 v[206:209], v188 offset:56320
	global_load_lds_dwordx4 v[216:217], off
	s_add_i32 m0, s30, 0x2000
	s_add_u32 s28, s28, 0x40080
	v_lshl_add_u64 v[216:217], v[218:219], 0, s[56:57]
	s_addc_u32 s29, s29, 0
	s_add_i32 s30, s53, s42
	global_load_lds_dwordx4 v[216:217], off
	s_mov_b32 m0, s30
	s_nop 0
	global_load_lds_dwordx4 v0, s[28:29]
	s_add_i32 m0, s30, 0x2000
	s_nop 0
	global_load_lds_dwordx4 v158, s[28:29]
	s_mov_b32 m0, s47
	v_lshl_add_u64 v[216:217], v[220:221], 0, s[56:57]
	global_load_lds_dwordx4 v[216:217], off
	s_mov_b32 m0, s48
	v_lshl_add_u64 v[216:217], v[222:223], 0, s[56:57]
	global_load_lds_dwordx4 v[216:217], off
	s_waitcnt vmcnt(8) lgkmcnt(0)
	s_barrier
	v_mfma_f32_16x16x32_bf16 v[62:65], v[130:133], v[172:175], v[62:65]
	v_mfma_f32_16x16x32_bf16 v[58:61], v[138:141], v[172:175], v[58:61]
	v_mfma_f32_16x16x32_bf16 v[50:53], v[130:133], v[180:183], v[50:53]
	v_mfma_f32_16x16x32_bf16 v[42:45], v[138:141], v[180:183], v[42:45]
	v_mfma_f32_16x16x32_bf16 v[34:37], v[130:133], v[194:197], v[34:37]
	v_mfma_f32_16x16x32_bf16 v[26:29], v[138:141], v[194:197], v[26:29]
	v_mfma_f32_16x16x32_bf16 v[18:21], v[130:133], v[202:205], v[18:21]
	v_mfma_f32_16x16x32_bf16 v[10:13], v[138:141], v[202:205], v[10:13]
	v_mfma_f32_16x16x32_bf16 v[62:65], v[134:137], v[176:179], v[62:65]
	v_mfma_f32_16x16x32_bf16 v[58:61], v[142:145], v[176:179], v[58:61]
	v_mfma_f32_16x16x32_bf16 v[50:53], v[134:137], v[190:193], v[50:53]
	v_mfma_f32_16x16x32_bf16 v[42:45], v[142:145], v[190:193], v[42:45]
	v_mfma_f32_16x16x32_bf16 v[34:37], v[134:137], v[198:201], v[34:37]
	v_mfma_f32_16x16x32_bf16 v[26:29], v[142:145], v[198:201], v[26:29]
	v_mfma_f32_16x16x32_bf16 v[18:21], v[134:137], v[206:209], v[18:21]
	v_mfma_f32_16x16x32_bf16 v[10:13], v[142:145], v[206:209], v[10:13]
	v_mfma_f32_16x16x32_bf16 v[54:57], v[146:149], v[172:175], v[54:57]
	v_mfma_f32_16x16x32_bf16 v[46:49], v[154:157], v[172:175], v[46:49]
	v_mfma_f32_16x16x32_bf16 v[38:41], v[146:149], v[180:183], v[38:41]
	v_mfma_f32_16x16x32_bf16 v[30:33], v[154:157], v[180:183], v[30:33]
	v_mfma_f32_16x16x32_bf16 v[22:25], v[146:149], v[194:197], v[22:25]
	v_mfma_f32_16x16x32_bf16 v[14:17], v[154:157], v[194:197], v[14:17]
	v_mfma_f32_16x16x32_bf16 v[6:9], v[146:149], v[202:205], v[6:9]
	v_mfma_f32_16x16x32_bf16 v[2:5], v[154:157], v[202:205], v[2:5]
	v_mfma_f32_16x16x32_bf16 v[54:57], v[150:153], v[176:179], v[54:57]
	v_mfma_f32_16x16x32_bf16 v[46:49], v[168:171], v[176:179], v[46:49]
	v_mfma_f32_16x16x32_bf16 v[38:41], v[150:153], v[190:193], v[38:41]
	v_mfma_f32_16x16x32_bf16 v[30:33], v[168:171], v[190:193], v[30:33]
	v_mfma_f32_16x16x32_bf16 v[22:25], v[150:153], v[198:201], v[22:25]
	v_mfma_f32_16x16x32_bf16 v[14:17], v[168:171], v[198:201], v[14:17]
	v_mfma_f32_16x16x32_bf16 v[6:9], v[150:153], v[206:209], v[6:9]
	v_mfma_f32_16x16x32_bf16 v[2:5], v[168:171], v[206:209], v[2:5]
	s_barrier
	s_add_i32 s40, s40, 2
	s_add_u32 s23, s23, 0x100
	s_addc_u32 s33, s33, 0
	s_add_u32 s6, s6, 0x100
	s_addc_u32 s7, s7, 0
	s_cmp_gt_u32 s40, 13
	s_cbranch_scc0 .LBB0_836
	s_and_b64 vcc, exec, s[18:19]
	s_cbranch_vccz .LBB0_839
	s_barrier

.LBB0_1524:
	s_add_u32 s8, s34, 0x100
	s_addc_u32 s9, s35, 0
	s_add_u32 s34, s26, 0x60080
	s_addc_u32 s35, s27, 0
	v_lshl_add_u64 v[140:141], s[34:35], 0, v[128:129]
	v_lshl_add_u64 v[142:143], s[34:35], 0, v[138:139]
	s_mov_b32 s59, -2
	s_mov_b64 s[34:35], 0
	v_add_u32_e32 v241, 0x10000, v144
.LBB0_1525:
	s_add_u32 s36, s26, s34
	s_addc_u32 s37, s27, s35
	s_add_u32 s36, s36, 0x100
	s_addc_u32 s37, s37, 0
	s_add_u32 s82, s8, s34
	s_addc_u32 s83, s9, s35
	s_add_i32 s84, 0, 0x10000
	s_cmpk_eq_i32 s34, 0xb00
	s_cselect_b32 s45, s31, s37
	s_cselect_b32 s44, s30, s36
	s_cselect_b32 s37, s29, s83
	s_cselect_b32 s36, s28, s82
	s_add_i32 s85, 0, 0x14000
	ds_read_b128 v[146:149], v241
	ds_read_b128 v[150:153], v241 offset:1024
	ds_read_b128 v[154:157], v241 offset:2048
	ds_read_b128 v[158:161], v241 offset:3072
	ds_read_b128 v[162:165], v241 offset:16384
	ds_read_b128 v[168:171], v241 offset:17408
	ds_read_b128 v[172:175], v241 offset:18432
	ds_read_b128 v[176:179], v241 offset:19456
	v_lshl_add_u64 v[208:209], v[142:143], 0, s[34:35]
	s_add_i32 m0, s4, 0xc000
	ds_read_b128 v[180:183], v145
	ds_read_b128 v[184:187], v145 offset:1024
	ds_read_b128 v[188:191], v145 offset:2048
	ds_read_b128 v[192:195], v145 offset:3072
	ds_read_b128 v[196:199], v145 offset:4096
	ds_read_b128 v[200:203], v145 offset:5120
	ds_read_b128 v[204:207], v145 offset:6144
	ds_read_b128 v[216:219], v145 offset:7168
	global_load_lds_dwordx4 v[208:209], off
	s_add_i32 m0, s4, 0xe000
	v_lshl_add_u64 v[208:209], v[140:141], 0, s[34:35]
	global_load_lds_dwordx4 v[208:209], off
	s_waitcnt vmcnt(8) lgkmcnt(0)
	s_barrier
	v_mfma_f32_16x16x32_bf16 v[134:137], v[146:149], v[180:183], v[134:137]
	v_mfma_f32_16x16x32_bf16 v[130:133], v[154:157], v[180:183], v[130:133]
	v_mfma_f32_16x16x32_bf16 v[110:113], v[146:149], v[188:191], v[110:113]
	v_mfma_f32_16x16x32_bf16 v[106:109], v[154:157], v[188:191], v[106:109]
	v_mfma_f32_16x16x32_bf16 v[94:97], v[146:149], v[196:199], v[94:97]
	v_mfma_f32_16x16x32_bf16 v[90:93], v[154:157], v[196:199], v[90:93]
	v_mfma_f32_16x16x32_bf16 v[78:81], v[146:149], v[204:207], v[78:81]
	v_mfma_f32_16x16x32_bf16 v[74:77], v[154:157], v[204:207], v[74:77]
	v_mfma_f32_16x16x32_bf16 v[134:137], v[150:153], v[184:187], v[134:137]
	v_mfma_f32_16x16x32_bf16 v[130:133], v[158:161], v[184:187], v[130:133]
	v_mfma_f32_16x16x32_bf16 v[110:113], v[150:153], v[192:195], v[110:113]
	v_mfma_f32_16x16x32_bf16 v[106:109], v[158:161], v[192:195], v[106:109]
	v_mfma_f32_16x16x32_bf16 v[94:97], v[150:153], v[200:203], v[94:97]
	v_mfma_f32_16x16x32_bf16 v[90:93], v[158:161], v[200:203], v[90:93]
	v_mfma_f32_16x16x32_bf16 v[78:81], v[150:153], v[216:219], v[78:81]
	v_mfma_f32_16x16x32_bf16 v[74:77], v[158:161], v[216:219], v[74:77]
	v_mfma_f32_16x16x32_bf16 v[122:125], v[162:165], v[180:183], v[122:125]
	v_mfma_f32_16x16x32_bf16 v[114:117], v[172:175], v[180:183], v[114:117]
	v_mfma_f32_16x16x32_bf16 v[102:105], v[162:165], v[188:191], v[102:105]
	v_mfma_f32_16x16x32_bf16 v[98:101], v[172:175], v[188:191], v[98:101]
	v_mfma_f32_16x16x32_bf16 v[86:89], v[162:165], v[196:199], v[86:89]
	v_mfma_f32_16x16x32_bf16 v[82:85], v[172:175], v[196:199], v[82:85]
	v_mfma_f32_16x16x32_bf16 v[70:73], v[162:165], v[204:207], v[70:73]
	v_mfma_f32_16x16x32_bf16 v[66:69], v[172:175], v[204:207], v[66:69]
	v_mfma_f32_16x16x32_bf16 v[122:125], v[168:171], v[184:187], v[122:125]
	v_mfma_f32_16x16x32_bf16 v[114:117], v[176:179], v[184:187], v[114:117]
	v_mfma_f32_16x16x32_bf16 v[102:105], v[168:171], v[192:195], v[102:105]
	v_mfma_f32_16x16x32_bf16 v[98:101], v[176:179], v[192:195], v[98:101]
	v_mfma_f32_16x16x32_bf16 v[86:89], v[168:171], v[200:203], v[86:89]
	v_mfma_f32_16x16x32_bf16 v[82:85], v[176:179], v[200:203], v[82:85]
	v_mfma_f32_16x16x32_bf16 v[70:73], v[168:171], v[216:219], v[70:73]
	v_mfma_f32_16x16x32_bf16 v[66:69], v[176:179], v[216:219], v[66:69]
	s_barrier
	s_add_i32 s82, s84, s70
	v_lshl_add_u64 v[208:209], s[36:37], 0, v[0:1]
	s_mov_b32 m0, s82
	ds_read_b128 v[180:183], v145 offset:16384
	ds_read_b128 v[184:187], v145 offset:17408
	ds_read_b128 v[188:191], v145 offset:18432
	ds_read_b128 v[192:195], v145 offset:19456
	ds_read_b128 v[196:199], v145 offset:20480
	ds_read_b128 v[200:203], v145 offset:21504
	ds_read_b128 v[204:207], v145 offset:22528
	ds_read_b128 v[216:219], v145 offset:23552
	global_load_lds_dwordx4 v0, s[36:37]
	s_add_i32 m0, s82, 0x2000
	s_add_u32 s82, s36, 0x60000
	v_lshl_add_u64 v[220:221], s[36:37], 0, v[118:119]
	s_addc_u32 s83, s37, 0
	s_add_i32 s84, s85, s70
	global_load_lds_dwordx4 v118, s[36:37]
	s_mov_b32 m0, s84
	v_lshl_add_u64 v[224:225], s[44:45], 0, v[120:121]
	global_load_lds_dwordx4 v0, s[82:83]
	s_add_i32 m0, s84, 0x2000
	s_nop 0
	global_load_lds_dwordx4 v118, s[82:83]
	s_mov_b32 m0, s4
	v_lshl_add_u64 v[222:223], s[44:45], 0, v[126:127]
	global_load_lds_dwordx4 v126, s[44:45]
	s_mov_b32 m0, s33
	s_nop 0
	global_load_lds_dwordx4 v120, s[44:45]
	s_waitcnt vmcnt(8) lgkmcnt(0)
	s_barrier
	v_mfma_f32_16x16x32_bf16 v[62:65], v[146:149], v[180:183], v[62:65]
	v_mfma_f32_16x16x32_bf16 v[58:61], v[154:157], v[180:183], v[58:61]
	v_mfma_f32_16x16x32_bf16 v[46:49], v[146:149], v[188:191], v[46:49]
	v_mfma_f32_16x16x32_bf16 v[42:45], v[154:157], v[188:191], v[42:45]
	v_mfma_f32_16x16x32_bf16 v[30:33], v[146:149], v[196:199], v[30:33]
	v_mfma_f32_16x16x32_bf16 v[26:29], v[154:157], v[196:199], v[26:29]
	v_mfma_f32_16x16x32_bf16 v[14:17], v[146:149], v[204:207], v[14:17]
	v_mfma_f32_16x16x32_bf16 v[10:13], v[154:157], v[204:207], v[10:13]
	v_mfma_f32_16x16x32_bf16 v[62:65], v[150:153], v[184:187], v[62:65]
	v_mfma_f32_16x16x32_bf16 v[58:61], v[158:161], v[184:187], v[58:61]
	v_mfma_f32_16x16x32_bf16 v[46:49], v[150:153], v[192:195], v[46:49]
	v_mfma_f32_16x16x32_bf16 v[42:45], v[158:161], v[192:195], v[42:45]
	v_mfma_f32_16x16x32_bf16 v[30:33], v[150:153], v[200:203], v[30:33]
	v_mfma_f32_16x16x32_bf16 v[26:29], v[158:161], v[200:203], v[26:29]
	v_mfma_f32_16x16x32_bf16 v[14:17], v[150:153], v[216:219], v[14:17]
	v_mfma_f32_16x16x32_bf16 v[10:13], v[158:161], v[216:219], v[10:13]
	v_mfma_f32_16x16x32_bf16 v[54:57], v[162:165], v[180:183], v[54:57]
	v_mfma_f32_16x16x32_bf16 v[50:53], v[172:175], v[180:183], v[50:53]
	v_mfma_f32_16x16x32_bf16 v[38:41], v[162:165], v[188:191], v[38:41]
	v_mfma_f32_16x16x32_bf16 v[34:37], v[172:175], v[188:191], v[34:37]
	v_mfma_f32_16x16x32_bf16 v[22:25], v[162:165], v[196:199], v[22:25]
	v_mfma_f32_16x16x32_bf16 v[18:21], v[172:175], v[196:199], v[18:21]
	v_mfma_f32_16x16x32_bf16 v[6:9], v[162:165], v[204:207], v[6:9]
	v_mfma_f32_16x16x32_bf16 v[2:5], v[172:175], v[204:207], v[2:5]
	v_mfma_f32_16x16x32_bf16 v[54:57], v[168:171], v[184:187], v[54:57]
	v_mfma_f32_16x16x32_bf16 v[50:53], v[176:179], v[184:187], v[50:53]
	v_mfma_f32_16x16x32_bf16 v[38:41], v[168:171], v[192:195], v[38:41]
	v_mfma_f32_16x16x32_bf16 v[34:37], v[176:179], v[192:195], v[34:37]
	v_mfma_f32_16x16x32_bf16 v[22:25], v[168:171], v[200:203], v[22:25]
	v_mfma_f32_16x16x32_bf16 v[18:21], v[176:179], v[200:203], v[18:21]
	v_mfma_f32_16x16x32_bf16 v[6:9], v[168:171], v[216:219], v[6:9]
	v_mfma_f32_16x16x32_bf16 v[2:5], v[176:179], v[216:219], v[2:5]
	s_barrier
	s_add_i32 s82, 0, 0x18000
	s_add_i32 s83, 0, 0x1c000
	ds_read_b128 v[146:149], v241 offset:32768
	ds_read_b128 v[150:153], v241 offset:33792
	ds_read_b128 v[154:157], v241 offset:34816
	ds_read_b128 v[158:161], v241 offset:35840
	ds_read_b128 v[162:165], v241 offset:49152
	ds_read_b128 v[168:171], v241 offset:50176
	ds_read_b128 v[172:175], v241 offset:51200
	ds_read_b128 v[176:179], v241 offset:52224
	s_add_u32 s44, s44, 0x60000
	s_addc_u32 s45, s45, 0
	s_mov_b32 m0, s71
	ds_read_b128 v[180:183], v145 offset:32768
	ds_read_b128 v[184:187], v145 offset:33792
	ds_read_b128 v[188:191], v145 offset:34816
	ds_read_b128 v[192:195], v145 offset:35840
	ds_read_b128 v[196:199], v145 offset:36864
	ds_read_b128 v[200:203], v145 offset:37888
	ds_read_b128 v[204:207], v145 offset:38912
	ds_read_b128 v[216:219], v145 offset:39936
	global_load_lds_dwordx4 v126, s[44:45]
	s_mov_b32 m0, s76
	v_lshl_add_u64 v[242:243], s[44:45], 0, v[120:121]
	global_load_lds_dwordx4 v120, s[44:45]
	s_waitcnt vmcnt(8) lgkmcnt(0)
	s_barrier
	v_mfma_f32_16x16x32_bf16 v[134:137], v[146:149], v[180:183], v[134:137]
	v_mfma_f32_16x16x32_bf16 v[130:133], v[154:157], v[180:183], v[130:133]
	v_mfma_f32_16x16x32_bf16 v[110:113], v[146:149], v[188:191], v[110:113]
	v_mfma_f32_16x16x32_bf16 v[106:109], v[154:157], v[188:191], v[106:109]
	v_mfma_f32_16x16x32_bf16 v[94:97], v[146:149], v[196:199], v[94:97]
	v_mfma_f32_16x16x32_bf16 v[90:93], v[154:157], v[196:199], v[90:93]
	v_mfma_f32_16x16x32_bf16 v[78:81], v[146:149], v[204:207], v[78:81]
	v_mfma_f32_16x16x32_bf16 v[74:77], v[154:157], v[204:207], v[74:77]
	v_mfma_f32_16x16x32_bf16 v[134:137], v[150:153], v[184:187], v[134:137]
	v_mfma_f32_16x16x32_bf16 v[130:133], v[158:161], v[184:187], v[130:133]
	v_mfma_f32_16x16x32_bf16 v[110:113], v[150:153], v[192:195], v[110:113]
	v_mfma_f32_16x16x32_bf16 v[106:109], v[158:161], v[192:195], v[106:109]
	v_mfma_f32_16x16x32_bf16 v[94:97], v[150:153], v[200:203], v[94:97]
	v_mfma_f32_16x16x32_bf16 v[90:93], v[158:161], v[200:203], v[90:93]
	v_mfma_f32_16x16x32_bf16 v[78:81], v[150:153], v[216:219], v[78:81]
	v_mfma_f32_16x16x32_bf16 v[74:77], v[158:161], v[216:219], v[74:77]
	v_mfma_f32_16x16x32_bf16 v[122:125], v[162:165], v[180:183], v[122:125]
	v_mfma_f32_16x16x32_bf16 v[114:117], v[172:175], v[180:183], v[114:117]
	v_mfma_f32_16x16x32_bf16 v[102:105], v[162:165], v[188:191], v[102:105]
	v_mfma_f32_16x16x32_bf16 v[98:101], v[172:175], v[188:191], v[98:101]
	v_mfma_f32_16x16x32_bf16 v[86:89], v[162:165], v[196:199], v[86:89]
	v_mfma_f32_16x16x32_bf16 v[82:85], v[172:175], v[196:199], v[82:85]
	v_mfma_f32_16x16x32_bf16 v[70:73], v[162:165], v[204:207], v[70:73]
	v_mfma_f32_16x16x32_bf16 v[66:69], v[172:175], v[204:207], v[66:69]
	v_mfma_f32_16x16x32_bf16 v[122:125], v[168:171], v[184:187], v[122:125]
	v_mfma_f32_16x16x32_bf16 v[114:117], v[176:179], v[184:187], v[114:117]
	v_mfma_f32_16x16x32_bf16 v[102:105], v[168:171], v[192:195], v[102:105]
	v_mfma_f32_16x16x32_bf16 v[98:101], v[176:179], v[192:195], v[98:101]
	v_mfma_f32_16x16x32_bf16 v[86:89], v[168:171], v[200:203], v[86:89]
	v_mfma_f32_16x16x32_bf16 v[82:85], v[176:179], v[200:203], v[82:85]
	v_mfma_f32_16x16x32_bf16 v[70:73], v[168:171], v[216:219], v[70:73]
	v_mfma_f32_16x16x32_bf16 v[66:69], v[176:179], v[216:219], v[66:69]
	s_barrier
	s_add_i32 s44, s82, s70
	v_lshl_add_u64 v[208:209], v[208:209], 0, s[56:57]
	s_mov_b32 m0, s44
	ds_read_b128 v[180:183], v145 offset:49152
	ds_read_b128 v[184:187], v145 offset:50176
	ds_read_b128 v[188:191], v145 offset:51200
	ds_read_b128 v[192:195], v145 offset:52224
	ds_read_b128 v[196:199], v145 offset:53248
	ds_read_b128 v[200:203], v145 offset:54272
	ds_read_b128 v[204:207], v145 offset:55296
	ds_read_b128 v[216:219], v145 offset:56320
	global_load_lds_dwordx4 v[208:209], off
	s_add_i32 m0, s44, 0x2000
	s_add_u32 s36, s36, 0x60080
	v_lshl_add_u64 v[208:209], v[220:221], 0, s[56:57]
	s_addc_u32 s37, s37, 0
	s_add_i32 s44, s83, s70
	global_load_lds_dwordx4 v[208:209], off
	s_mov_b32 m0, s44
	s_nop 0
	global_load_lds_dwordx4 v0, s[36:37]
	s_add_i32 m0, s44, 0x2000
	s_nop 0
	global_load_lds_dwordx4 v118, s[36:37]
	s_mov_b32 m0, s77
	v_lshl_add_u64 v[208:209], v[222:223], 0, s[56:57]
	global_load_lds_dwordx4 v[208:209], off
	s_mov_b32 m0, s79
	v_lshl_add_u64 v[208:209], v[224:225], 0, s[56:57]
	global_load_lds_dwordx4 v[208:209], off
	s_waitcnt vmcnt(8) lgkmcnt(0)
	s_barrier
	v_mfma_f32_16x16x32_bf16 v[62:65], v[146:149], v[180:183], v[62:65]
	v_mfma_f32_16x16x32_bf16 v[58:61], v[154:157], v[180:183], v[58:61]
	v_mfma_f32_16x16x32_bf16 v[46:49], v[146:149], v[188:191], v[46:49]
	v_mfma_f32_16x16x32_bf16 v[42:45], v[154:157], v[188:191], v[42:45]
	v_mfma_f32_16x16x32_bf16 v[30:33], v[146:149], v[196:199], v[30:33]
	v_mfma_f32_16x16x32_bf16 v[26:29], v[154:157], v[196:199], v[26:29]
	v_mfma_f32_16x16x32_bf16 v[14:17], v[146:149], v[204:207], v[14:17]
	v_mfma_f32_16x16x32_bf16 v[10:13], v[154:157], v[204:207], v[10:13]
	v_mfma_f32_16x16x32_bf16 v[62:65], v[150:153], v[184:187], v[62:65]
	v_mfma_f32_16x16x32_bf16 v[58:61], v[158:161], v[184:187], v[58:61]
	v_mfma_f32_16x16x32_bf16 v[46:49], v[150:153], v[192:195], v[46:49]
	v_mfma_f32_16x16x32_bf16 v[42:45], v[158:161], v[192:195], v[42:45]
	v_mfma_f32_16x16x32_bf16 v[30:33], v[150:153], v[200:203], v[30:33]
	v_mfma_f32_16x16x32_bf16 v[26:29], v[158:161], v[200:203], v[26:29]
	v_mfma_f32_16x16x32_bf16 v[14:17], v[150:153], v[216:219], v[14:17]
	v_mfma_f32_16x16x32_bf16 v[10:13], v[158:161], v[216:219], v[10:13]
	v_mfma_f32_16x16x32_bf16 v[54:57], v[162:165], v[180:183], v[54:57]
	v_mfma_f32_16x16x32_bf16 v[50:53], v[172:175], v[180:183], v[50:53]
	v_mfma_f32_16x16x32_bf16 v[38:41], v[162:165], v[188:191], v[38:41]
	v_mfma_f32_16x16x32_bf16 v[34:37], v[172:175], v[188:191], v[34:37]
	v_mfma_f32_16x16x32_bf16 v[22:25], v[162:165], v[196:199], v[22:25]
	v_mfma_f32_16x16x32_bf16 v[18:21], v[172:175], v[196:199], v[18:21]
	v_mfma_f32_16x16x32_bf16 v[6:9], v[162:165], v[204:207], v[6:9]
	v_mfma_f32_16x16x32_bf16 v[2:5], v[172:175], v[204:207], v[2:5]
	v_mfma_f32_16x16x32_bf16 v[54:57], v[168:171], v[184:187], v[54:57]
	v_mfma_f32_16x16x32_bf16 v[50:53], v[176:179], v[184:187], v[50:53]
	v_mfma_f32_16x16x32_bf16 v[38:41], v[168:171], v[192:195], v[38:41]
	v_mfma_f32_16x16x32_bf16 v[34:37], v[176:179], v[192:195], v[34:37]
	v_mfma_f32_16x16x32_bf16 v[22:25], v[168:171], v[200:203], v[22:25]
	v_mfma_f32_16x16x32_bf16 v[18:21], v[176:179], v[200:203], v[18:21]
	v_mfma_f32_16x16x32_bf16 v[6:9], v[168:171], v[216:219], v[6:9]
	v_mfma_f32_16x16x32_bf16 v[2:5], v[176:179], v[216:219], v[2:5]
	s_barrier
	s_add_i32 s59, s59, 2
	s_add_u32 s34, s34, 0x100
	s_addc_u32 s35, s35, 0
	s_cmp_gt_u32 s59, 21
	s_cbranch_scc0 .LBB0_1525
	s_add_u32 s34, s8, 0xffffff00
	s_addc_u32 s35, s9, -1
	s_and_b64 vcc, exec, s[42:43]
	s_cbranch_vccnz .LBB0_1528
	v_mov_b32_e32 v2, 0
	s_mov_b32 s16, s80
	s_mov_b32 s47, s81
	s_mov_b64 s[26:27], s[30:31]
	s_mov_b32 s68, s58
	v_mov_b32_e32 v3, v2
	v_mov_b32_e32 v4, v2
	v_mov_b32_e32 v5, v2
	v_mov_b32_e32 v6, v2
	v_mov_b32_e32 v7, v2
	v_mov_b32_e32 v8, v2
	v_mov_b32_e32 v9, v2
	v_mov_b32_e32 v18, v2
	v_mov_b32_e32 v19, v2
	v_mov_b32_e32 v20, v2
	v_mov_b32_e32 v21, v2
	v_mov_b32_e32 v22, v2
	v_mov_b32_e32 v23, v2
	v_mov_b32_e32 v24, v2
	v_mov_b32_e32 v25, v2
	v_mov_b32_e32 v34, v2
	v_mov_b32_e32 v35, v2
	v_mov_b32_e32 v36, v2
	v_mov_b32_e32 v37, v2
	v_mov_b32_e32 v38, v2
	v_mov_b32_e32 v39, v2
	v_mov_b32_e32 v40, v2
	v_mov_b32_e32 v41, v2
	v_mov_b32_e32 v50, v2
	v_mov_b32_e32 v51, v2
	v_mov_b32_e32 v52, v2
	v_mov_b32_e32 v53, v2
	v_mov_b32_e32 v54, v2
	v_mov_b32_e32 v55, v2
	v_mov_b32_e32 v56, v2
	v_mov_b32_e32 v57, v2
	v_mov_b32_e32 v10, v2
	v_mov_b32_e32 v11, v2
	v_mov_b32_e32 v12, v2
	v_mov_b32_e32 v13, v2
	v_mov_b32_e32 v14, v2
	v_mov_b32_e32 v15, v2
	v_mov_b32_e32 v16, v2
	v_mov_b32_e32 v17, v2
	v_mov_b32_e32 v26, v2
	v_mov_b32_e32 v27, v2
	v_mov_b32_e32 v28, v2
	v_mov_b32_e32 v29, v2
	v_mov_b32_e32 v30, v2
	v_mov_b32_e32 v31, v2
	v_mov_b32_e32 v32, v2
	v_mov_b32_e32 v33, v2
	v_mov_b32_e32 v42, v2
	v_mov_b32_e32 v43, v2
	v_mov_b32_e32 v44, v2
	v_mov_b32_e32 v45, v2
	v_mov_b32_e32 v46, v2
	v_mov_b32_e32 v47, v2
	v_mov_b32_e32 v48, v2
	v_mov_b32_e32 v49, v2
	v_mov_b32_e32 v58, v2
	v_mov_b32_e32 v59, v2
	v_mov_b32_e32 v60, v2
	v_mov_b32_e32 v61, v2
	v_mov_b32_e32 v62, v2
	v_mov_b32_e32 v63, v2
	v_mov_b32_e32 v64, v2
	v_mov_b32_e32 v65, v2
	v_mov_b32_e32 v66, v2
	v_mov_b32_e32 v67, v2
	v_mov_b32_e32 v68, v2
	v_mov_b32_e32 v69, v2
	v_mov_b32_e32 v70, v2
	v_mov_b32_e32 v71, v2
	v_mov_b32_e32 v72, v2
	v_mov_b32_e32 v73, v2
	v_mov_b32_e32 v82, v2
	v_mov_b32_e32 v83, v2
	v_mov_b32_e32 v84, v2
	v_mov_b32_e32 v85, v2
	v_mov_b32_e32 v86, v2
	v_mov_b32_e32 v87, v2
	v_mov_b32_e32 v88, v2
	v_mov_b32_e32 v89, v2
	v_mov_b32_e32 v98, v2
	v_mov_b32_e32 v99, v2
	v_mov_b32_e32 v100, v2
	v_mov_b32_e32 v101, v2
	v_mov_b32_e32 v102, v2
	v_mov_b32_e32 v103, v2
	v_mov_b32_e32 v104, v2
	v_mov_b32_e32 v105, v2
	v_mov_b32_e32 v114, v2
	v_mov_b32_e32 v115, v2
	v_mov_b32_e32 v116, v2
	v_mov_b32_e32 v117, v2
	v_mov_b32_e32 v122, v2
	v_mov_b32_e32 v123, v2
	v_mov_b32_e32 v124, v2
	v_mov_b32_e32 v125, v2
	v_mov_b32_e32 v74, v2
	v_mov_b32_e32 v75, v2
	v_mov_b32_e32 v76, v2
	v_mov_b32_e32 v77, v2
	v_mov_b32_e32 v78, v2
	v_mov_b32_e32 v79, v2
	v_mov_b32_e32 v80, v2
	v_mov_b32_e32 v81, v2
	v_mov_b32_e32 v90, v2
	v_mov_b32_e32 v91, v2
	v_mov_b32_e32 v92, v2
	v_mov_b32_e32 v93, v2
	v_mov_b32_e32 v94, v2
	v_mov_b32_e32 v95, v2
	v_mov_b32_e32 v96, v2
	v_mov_b32_e32 v97, v2
	v_mov_b32_e32 v106, v2
	v_mov_b32_e32 v107, v2
	v_mov_b32_e32 v108, v2
	v_mov_b32_e32 v109, v2
	v_mov_b32_e32 v110, v2
	v_mov_b32_e32 v111, v2
	v_mov_b32_e32 v112, v2
	v_mov_b32_e32 v113, v2
	v_mov_b32_e32 v130, v2
	v_mov_b32_e32 v131, v2
	v_mov_b32_e32 v132, v2
	v_mov_b32_e32 v133, v2
	v_mov_b32_e32 v134, v2
	v_mov_b32_e32 v135, v2
	v_mov_b32_e32 v136, v2
	v_mov_b32_e32 v137, v2
	s_andn2_b64 vcc, exec, s[40:41]
	s_cbranch_vccnz .LBB0_1529
	s_branch .LBB0_1531

.LBB0_1623:
	s_add_u32 s36, s26, s34
	s_addc_u32 s37, s27, s35
	s_add_u32 s36, s36, 0x100
	s_addc_u32 s37, s37, 0
	s_add_u32 s80, s8, s34
	s_addc_u32 s81, s9, s35
	s_add_i32 s82, 0, 0x10000
	s_cmpk_eq_i32 s34, 0xb00
	s_cselect_b32 s43, s31, s37
	s_cselect_b32 s42, s30, s36
	s_cselect_b32 s37, s29, s81
	s_cselect_b32 s36, s28, s80
	s_add_i32 s83, 0, 0x14000
	ds_read_b128 v[146:149], v241
	ds_read_b128 v[150:153], v241 offset:1024
	ds_read_b128 v[154:157], v241 offset:2048
	ds_read_b128 v[158:161], v241 offset:3072
	ds_read_b128 v[162:165], v241 offset:16384
	ds_read_b128 v[168:171], v241 offset:17408
	ds_read_b128 v[172:175], v241 offset:18432
	ds_read_b128 v[176:179], v241 offset:19456
	v_lshl_add_u64 v[208:209], v[142:143], 0, s[34:35]
	s_add_i32 m0, s4, 0xc000
	ds_read_b128 v[180:183], v145
	ds_read_b128 v[184:187], v145 offset:1024
	ds_read_b128 v[188:191], v145 offset:2048
	ds_read_b128 v[192:195], v145 offset:3072
	ds_read_b128 v[196:199], v145 offset:4096
	ds_read_b128 v[200:203], v145 offset:5120
	ds_read_b128 v[204:207], v145 offset:6144
	ds_read_b128 v[216:219], v145 offset:7168
	global_load_lds_dwordx4 v[208:209], off
	s_add_i32 m0, s4, 0xe000
	v_lshl_add_u64 v[208:209], v[140:141], 0, s[34:35]
	global_load_lds_dwordx4 v[208:209], off
	s_waitcnt vmcnt(8) lgkmcnt(0)
	s_barrier
	v_mfma_f32_16x16x32_bf16 v[134:137], v[146:149], v[180:183], v[134:137]
	v_mfma_f32_16x16x32_bf16 v[130:133], v[154:157], v[180:183], v[130:133]
	v_mfma_f32_16x16x32_bf16 v[110:113], v[146:149], v[188:191], v[110:113]
	v_mfma_f32_16x16x32_bf16 v[106:109], v[154:157], v[188:191], v[106:109]
	v_mfma_f32_16x16x32_bf16 v[94:97], v[146:149], v[196:199], v[94:97]
	v_mfma_f32_16x16x32_bf16 v[90:93], v[154:157], v[196:199], v[90:93]
	v_mfma_f32_16x16x32_bf16 v[78:81], v[146:149], v[204:207], v[78:81]
	v_mfma_f32_16x16x32_bf16 v[74:77], v[154:157], v[204:207], v[74:77]
	v_mfma_f32_16x16x32_bf16 v[134:137], v[150:153], v[184:187], v[134:137]
	v_mfma_f32_16x16x32_bf16 v[130:133], v[158:161], v[184:187], v[130:133]
	v_mfma_f32_16x16x32_bf16 v[110:113], v[150:153], v[192:195], v[110:113]
	v_mfma_f32_16x16x32_bf16 v[106:109], v[158:161], v[192:195], v[106:109]
	v_mfma_f32_16x16x32_bf16 v[94:97], v[150:153], v[200:203], v[94:97]
	v_mfma_f32_16x16x32_bf16 v[90:93], v[158:161], v[200:203], v[90:93]
	v_mfma_f32_16x16x32_bf16 v[78:81], v[150:153], v[216:219], v[78:81]
	v_mfma_f32_16x16x32_bf16 v[74:77], v[158:161], v[216:219], v[74:77]
	v_mfma_f32_16x16x32_bf16 v[122:125], v[162:165], v[180:183], v[122:125]
	v_mfma_f32_16x16x32_bf16 v[114:117], v[172:175], v[180:183], v[114:117]
	v_mfma_f32_16x16x32_bf16 v[102:105], v[162:165], v[188:191], v[102:105]
	v_mfma_f32_16x16x32_bf16 v[98:101], v[172:175], v[188:191], v[98:101]
	v_mfma_f32_16x16x32_bf16 v[86:89], v[162:165], v[196:199], v[86:89]
	v_mfma_f32_16x16x32_bf16 v[82:85], v[172:175], v[196:199], v[82:85]
	v_mfma_f32_16x16x32_bf16 v[70:73], v[162:165], v[204:207], v[70:73]
	v_mfma_f32_16x16x32_bf16 v[66:69], v[172:175], v[204:207], v[66:69]
	v_mfma_f32_16x16x32_bf16 v[122:125], v[168:171], v[184:187], v[122:125]
	v_mfma_f32_16x16x32_bf16 v[114:117], v[176:179], v[184:187], v[114:117]
	v_mfma_f32_16x16x32_bf16 v[102:105], v[168:171], v[192:195], v[102:105]
	v_mfma_f32_16x16x32_bf16 v[98:101], v[176:179], v[192:195], v[98:101]
	v_mfma_f32_16x16x32_bf16 v[86:89], v[168:171], v[200:203], v[86:89]
	v_mfma_f32_16x16x32_bf16 v[82:85], v[176:179], v[200:203], v[82:85]
	v_mfma_f32_16x16x32_bf16 v[70:73], v[168:171], v[216:219], v[70:73]
	v_mfma_f32_16x16x32_bf16 v[66:69], v[176:179], v[216:219], v[66:69]
	s_barrier
	s_add_i32 s80, s82, s53
	v_lshl_add_u64 v[208:209], s[36:37], 0, v[0:1]
	s_mov_b32 m0, s80
	ds_read_b128 v[180:183], v145 offset:16384
	ds_read_b128 v[184:187], v145 offset:17408
	ds_read_b128 v[188:191], v145 offset:18432
	ds_read_b128 v[192:195], v145 offset:19456
	ds_read_b128 v[196:199], v145 offset:20480
	ds_read_b128 v[200:203], v145 offset:21504
	ds_read_b128 v[204:207], v145 offset:22528
	ds_read_b128 v[216:219], v145 offset:23552
	global_load_lds_dwordx4 v0, s[36:37]
	s_add_i32 m0, s80, 0x2000
	s_add_u32 s80, s36, 0x60000
	v_lshl_add_u64 v[220:221], s[36:37], 0, v[118:119]
	s_addc_u32 s81, s37, 0
	s_add_i32 s82, s83, s53
	global_load_lds_dwordx4 v118, s[36:37]
	s_mov_b32 m0, s82
	v_lshl_add_u64 v[224:225], s[42:43], 0, v[120:121]
	global_load_lds_dwordx4 v0, s[80:81]
	s_add_i32 m0, s82, 0x2000
	s_nop 0
	global_load_lds_dwordx4 v118, s[80:81]
	s_mov_b32 m0, s4
	v_lshl_add_u64 v[222:223], s[42:43], 0, v[126:127]
	global_load_lds_dwordx4 v126, s[42:43]
	s_mov_b32 m0, s33
	s_nop 0
	global_load_lds_dwordx4 v120, s[42:43]
	s_waitcnt vmcnt(8) lgkmcnt(0)
	s_barrier
	v_mfma_f32_16x16x32_bf16 v[62:65], v[146:149], v[180:183], v[62:65]
	v_mfma_f32_16x16x32_bf16 v[58:61], v[154:157], v[180:183], v[58:61]
	v_mfma_f32_16x16x32_bf16 v[46:49], v[146:149], v[188:191], v[46:49]
	v_mfma_f32_16x16x32_bf16 v[42:45], v[154:157], v[188:191], v[42:45]
	v_mfma_f32_16x16x32_bf16 v[30:33], v[146:149], v[196:199], v[30:33]
	v_mfma_f32_16x16x32_bf16 v[26:29], v[154:157], v[196:199], v[26:29]
	v_mfma_f32_16x16x32_bf16 v[14:17], v[146:149], v[204:207], v[14:17]
	v_mfma_f32_16x16x32_bf16 v[10:13], v[154:157], v[204:207], v[10:13]
	v_mfma_f32_16x16x32_bf16 v[62:65], v[150:153], v[184:187], v[62:65]
	v_mfma_f32_16x16x32_bf16 v[58:61], v[158:161], v[184:187], v[58:61]
	v_mfma_f32_16x16x32_bf16 v[46:49], v[150:153], v[192:195], v[46:49]
	v_mfma_f32_16x16x32_bf16 v[42:45], v[158:161], v[192:195], v[42:45]
	v_mfma_f32_16x16x32_bf16 v[30:33], v[150:153], v[200:203], v[30:33]
	v_mfma_f32_16x16x32_bf16 v[26:29], v[158:161], v[200:203], v[26:29]
	v_mfma_f32_16x16x32_bf16 v[14:17], v[150:153], v[216:219], v[14:17]
	v_mfma_f32_16x16x32_bf16 v[10:13], v[158:161], v[216:219], v[10:13]
	v_mfma_f32_16x16x32_bf16 v[54:57], v[162:165], v[180:183], v[54:57]
	v_mfma_f32_16x16x32_bf16 v[50:53], v[172:175], v[180:183], v[50:53]
	v_mfma_f32_16x16x32_bf16 v[38:41], v[162:165], v[188:191], v[38:41]
	v_mfma_f32_16x16x32_bf16 v[34:37], v[172:175], v[188:191], v[34:37]
	v_mfma_f32_16x16x32_bf16 v[22:25], v[162:165], v[196:199], v[22:25]
	v_mfma_f32_16x16x32_bf16 v[18:21], v[172:175], v[196:199], v[18:21]
	v_mfma_f32_16x16x32_bf16 v[6:9], v[162:165], v[204:207], v[6:9]
	v_mfma_f32_16x16x32_bf16 v[2:5], v[172:175], v[204:207], v[2:5]
	v_mfma_f32_16x16x32_bf16 v[54:57], v[168:171], v[184:187], v[54:57]
	v_mfma_f32_16x16x32_bf16 v[50:53], v[176:179], v[184:187], v[50:53]
	v_mfma_f32_16x16x32_bf16 v[38:41], v[168:171], v[192:195], v[38:41]
	v_mfma_f32_16x16x32_bf16 v[34:37], v[176:179], v[192:195], v[34:37]
	v_mfma_f32_16x16x32_bf16 v[22:25], v[168:171], v[200:203], v[22:25]
	v_mfma_f32_16x16x32_bf16 v[18:21], v[176:179], v[200:203], v[18:21]
	v_mfma_f32_16x16x32_bf16 v[6:9], v[168:171], v[216:219], v[6:9]
	v_mfma_f32_16x16x32_bf16 v[2:5], v[176:179], v[216:219], v[2:5]
	s_barrier
	s_add_i32 s80, 0, 0x18000
	s_add_i32 s81, 0, 0x1c000
	ds_read_b128 v[146:149], v241 offset:32768
	ds_read_b128 v[150:153], v241 offset:33792
	ds_read_b128 v[154:157], v241 offset:34816
	ds_read_b128 v[158:161], v241 offset:35840
	ds_read_b128 v[162:165], v241 offset:49152
	ds_read_b128 v[168:171], v241 offset:50176
	ds_read_b128 v[172:175], v241 offset:51200
	ds_read_b128 v[176:179], v241 offset:52224
	s_add_u32 s42, s42, 0x60000
	s_addc_u32 s43, s43, 0
	s_mov_b32 m0, s62
	ds_read_b128 v[180:183], v145 offset:32768
	ds_read_b128 v[184:187], v145 offset:33792
	ds_read_b128 v[188:191], v145 offset:34816
	ds_read_b128 v[192:195], v145 offset:35840
	ds_read_b128 v[196:199], v145 offset:36864
	ds_read_b128 v[200:203], v145 offset:37888
	ds_read_b128 v[204:207], v145 offset:38912
	ds_read_b128 v[216:219], v145 offset:39936
	global_load_lds_dwordx4 v126, s[42:43]
	s_mov_b32 m0, s63
	v_lshl_add_u64 v[242:243], s[42:43], 0, v[120:121]
	global_load_lds_dwordx4 v120, s[42:43]
	s_waitcnt vmcnt(8) lgkmcnt(0)
	s_barrier
	v_mfma_f32_16x16x32_bf16 v[134:137], v[146:149], v[180:183], v[134:137]
	v_mfma_f32_16x16x32_bf16 v[130:133], v[154:157], v[180:183], v[130:133]
	v_mfma_f32_16x16x32_bf16 v[110:113], v[146:149], v[188:191], v[110:113]
	v_mfma_f32_16x16x32_bf16 v[106:109], v[154:157], v[188:191], v[106:109]
	v_mfma_f32_16x16x32_bf16 v[94:97], v[146:149], v[196:199], v[94:97]
	v_mfma_f32_16x16x32_bf16 v[90:93], v[154:157], v[196:199], v[90:93]
	v_mfma_f32_16x16x32_bf16 v[78:81], v[146:149], v[204:207], v[78:81]
	v_mfma_f32_16x16x32_bf16 v[74:77], v[154:157], v[204:207], v[74:77]
	v_mfma_f32_16x16x32_bf16 v[134:137], v[150:153], v[184:187], v[134:137]
	v_mfma_f32_16x16x32_bf16 v[130:133], v[158:161], v[184:187], v[130:133]
	v_mfma_f32_16x16x32_bf16 v[110:113], v[150:153], v[192:195], v[110:113]
	v_mfma_f32_16x16x32_bf16 v[106:109], v[158:161], v[192:195], v[106:109]
	v_mfma_f32_16x16x32_bf16 v[94:97], v[150:153], v[200:203], v[94:97]
	v_mfma_f32_16x16x32_bf16 v[90:93], v[158:161], v[200:203], v[90:93]
	v_mfma_f32_16x16x32_bf16 v[78:81], v[150:153], v[216:219], v[78:81]
	v_mfma_f32_16x16x32_bf16 v[74:77], v[158:161], v[216:219], v[74:77]
	v_mfma_f32_16x16x32_bf16 v[122:125], v[162:165], v[180:183], v[122:125]
	v_mfma_f32_16x16x32_bf16 v[114:117], v[172:175], v[180:183], v[114:117]
	v_mfma_f32_16x16x32_bf16 v[102:105], v[162:165], v[188:191], v[102:105]
	v_mfma_f32_16x16x32_bf16 v[98:101], v[172:175], v[188:191], v[98:101]
	v_mfma_f32_16x16x32_bf16 v[86:89], v[162:165], v[196:199], v[86:89]
	v_mfma_f32_16x16x32_bf16 v[82:85], v[172:175], v[196:199], v[82:85]
	v_mfma_f32_16x16x32_bf16 v[70:73], v[162:165], v[204:207], v[70:73]
	v_mfma_f32_16x16x32_bf16 v[66:69], v[172:175], v[204:207], v[66:69]
	v_mfma_f32_16x16x32_bf16 v[122:125], v[168:171], v[184:187], v[122:125]
	v_mfma_f32_16x16x32_bf16 v[114:117], v[176:179], v[184:187], v[114:117]
	v_mfma_f32_16x16x32_bf16 v[102:105], v[168:171], v[192:195], v[102:105]
	v_mfma_f32_16x16x32_bf16 v[98:101], v[176:179], v[192:195], v[98:101]
	v_mfma_f32_16x16x32_bf16 v[86:89], v[168:171], v[200:203], v[86:89]
	v_mfma_f32_16x16x32_bf16 v[82:85], v[176:179], v[200:203], v[82:85]
	v_mfma_f32_16x16x32_bf16 v[70:73], v[168:171], v[216:219], v[70:73]
	v_mfma_f32_16x16x32_bf16 v[66:69], v[176:179], v[216:219], v[66:69]
	s_barrier
	s_add_i32 s42, s80, s53
	v_lshl_add_u64 v[208:209], v[208:209], 0, s[56:57]
	s_mov_b32 m0, s42
	ds_read_b128 v[180:183], v145 offset:49152
	ds_read_b128 v[184:187], v145 offset:50176
	ds_read_b128 v[188:191], v145 offset:51200
	ds_read_b128 v[192:195], v145 offset:52224
	ds_read_b128 v[196:199], v145 offset:53248
	ds_read_b128 v[200:203], v145 offset:54272
	ds_read_b128 v[204:207], v145 offset:55296
	ds_read_b128 v[216:219], v145 offset:56320
	global_load_lds_dwordx4 v[208:209], off
	s_add_i32 m0, s42, 0x2000
	s_add_u32 s36, s36, 0x60080
	v_lshl_add_u64 v[208:209], v[220:221], 0, s[56:57]
	s_addc_u32 s37, s37, 0
	s_add_i32 s42, s81, s53
	global_load_lds_dwordx4 v[208:209], off
	s_mov_b32 m0, s42
	s_nop 0
	global_load_lds_dwordx4 v0, s[36:37]
	s_add_i32 m0, s42, 0x2000
	s_nop 0
	global_load_lds_dwordx4 v118, s[36:37]
	s_mov_b32 m0, s70
	v_lshl_add_u64 v[208:209], v[222:223], 0, s[56:57]
	global_load_lds_dwordx4 v[208:209], off
	s_mov_b32 m0, s71
	v_lshl_add_u64 v[208:209], v[224:225], 0, s[56:57]
	global_load_lds_dwordx4 v[208:209], off
	s_waitcnt vmcnt(8) lgkmcnt(0)
	s_barrier
	v_mfma_f32_16x16x32_bf16 v[62:65], v[146:149], v[180:183], v[62:65]
	v_mfma_f32_16x16x32_bf16 v[58:61], v[154:157], v[180:183], v[58:61]
	v_mfma_f32_16x16x32_bf16 v[46:49], v[146:149], v[188:191], v[46:49]
	v_mfma_f32_16x16x32_bf16 v[42:45], v[154:157], v[188:191], v[42:45]
	v_mfma_f32_16x16x32_bf16 v[30:33], v[146:149], v[196:199], v[30:33]
	v_mfma_f32_16x16x32_bf16 v[26:29], v[154:157], v[196:199], v[26:29]
	v_mfma_f32_16x16x32_bf16 v[14:17], v[146:149], v[204:207], v[14:17]
	v_mfma_f32_16x16x32_bf16 v[10:13], v[154:157], v[204:207], v[10:13]
	v_mfma_f32_16x16x32_bf16 v[62:65], v[150:153], v[184:187], v[62:65]
	v_mfma_f32_16x16x32_bf16 v[58:61], v[158:161], v[184:187], v[58:61]
	v_mfma_f32_16x16x32_bf16 v[46:49], v[150:153], v[192:195], v[46:49]
	v_mfma_f32_16x16x32_bf16 v[42:45], v[158:161], v[192:195], v[42:45]
	v_mfma_f32_16x16x32_bf16 v[30:33], v[150:153], v[200:203], v[30:33]
	v_mfma_f32_16x16x32_bf16 v[26:29], v[158:161], v[200:203], v[26:29]
	v_mfma_f32_16x16x32_bf16 v[14:17], v[150:153], v[216:219], v[14:17]
	v_mfma_f32_16x16x32_bf16 v[10:13], v[158:161], v[216:219], v[10:13]
	v_mfma_f32_16x16x32_bf16 v[54:57], v[162:165], v[180:183], v[54:57]
	v_mfma_f32_16x16x32_bf16 v[50:53], v[172:175], v[180:183], v[50:53]
	v_mfma_f32_16x16x32_bf16 v[38:41], v[162:165], v[188:191], v[38:41]
	v_mfma_f32_16x16x32_bf16 v[34:37], v[172:175], v[188:191], v[34:37]
	v_mfma_f32_16x16x32_bf16 v[22:25], v[162:165], v[196:199], v[22:25]
	v_mfma_f32_16x16x32_bf16 v[18:21], v[172:175], v[196:199], v[18:21]
	v_mfma_f32_16x16x32_bf16 v[6:9], v[162:165], v[204:207], v[6:9]
	v_mfma_f32_16x16x32_bf16 v[2:5], v[172:175], v[204:207], v[2:5]
	v_mfma_f32_16x16x32_bf16 v[54:57], v[168:171], v[184:187], v[54:57]
	v_mfma_f32_16x16x32_bf16 v[50:53], v[176:179], v[184:187], v[50:53]
	v_mfma_f32_16x16x32_bf16 v[38:41], v[168:171], v[192:195], v[38:41]
	v_mfma_f32_16x16x32_bf16 v[34:37], v[176:179], v[192:195], v[34:37]
	v_mfma_f32_16x16x32_bf16 v[22:25], v[168:171], v[200:203], v[22:25]
	v_mfma_f32_16x16x32_bf16 v[18:21], v[176:179], v[200:203], v[18:21]
	v_mfma_f32_16x16x32_bf16 v[6:9], v[168:171], v[216:219], v[6:9]
	v_mfma_f32_16x16x32_bf16 v[2:5], v[176:179], v[216:219], v[2:5]
	s_barrier
	s_add_i32 s59, s59, 2
	s_add_u32 s34, s34, 0x100
	s_addc_u32 s35, s35, 0
	s_cmp_gt_u32 s59, 21
	s_cbranch_scc0 .LBB0_1623
	s_add_u32 s34, s8, 0xffffff00
	s_addc_u32 s35, s9, -1
	s_and_b64 vcc, exec, s[40:41]
	s_cbranch_vccnz .LBB0_1626
	v_mov_b32_e32 v2, 0
	s_mov_b32 s16, s77
	s_mov_b32 s76, s79
	s_mov_b64 s[26:27], s[30:31]
	s_mov_b32 s68, s58
	v_mov_b32_e32 v3, v2
	v_mov_b32_e32 v4, v2
	v_mov_b32_e32 v5, v2
	v_mov_b32_e32 v6, v2
	v_mov_b32_e32 v7, v2
	v_mov_b32_e32 v8, v2
	v_mov_b32_e32 v9, v2
	v_mov_b32_e32 v18, v2
	v_mov_b32_e32 v19, v2
	v_mov_b32_e32 v20, v2
	v_mov_b32_e32 v21, v2
	v_mov_b32_e32 v22, v2
	v_mov_b32_e32 v23, v2
	v_mov_b32_e32 v24, v2
	v_mov_b32_e32 v25, v2
	v_mov_b32_e32 v34, v2
	v_mov_b32_e32 v35, v2
	v_mov_b32_e32 v36, v2
	v_mov_b32_e32 v37, v2
	v_mov_b32_e32 v38, v2
	v_mov_b32_e32 v39, v2
	v_mov_b32_e32 v40, v2
	v_mov_b32_e32 v41, v2
	v_mov_b32_e32 v50, v2
	v_mov_b32_e32 v51, v2
	v_mov_b32_e32 v52, v2
	v_mov_b32_e32 v53, v2
	v_mov_b32_e32 v54, v2
	v_mov_b32_e32 v55, v2
	v_mov_b32_e32 v56, v2
	v_mov_b32_e32 v57, v2
	v_mov_b32_e32 v10, v2
	v_mov_b32_e32 v11, v2
	v_mov_b32_e32 v12, v2
	v_mov_b32_e32 v13, v2
	v_mov_b32_e32 v14, v2
	v_mov_b32_e32 v15, v2
	v_mov_b32_e32 v16, v2
	v_mov_b32_e32 v17, v2
	v_mov_b32_e32 v26, v2
	v_mov_b32_e32 v27, v2
	v_mov_b32_e32 v28, v2
	v_mov_b32_e32 v29, v2
	v_mov_b32_e32 v30, v2
	v_mov_b32_e32 v31, v2
	v_mov_b32_e32 v32, v2
	v_mov_b32_e32 v33, v2
	v_mov_b32_e32 v42, v2
	v_mov_b32_e32 v43, v2
	v_mov_b32_e32 v44, v2
	v_mov_b32_e32 v45, v2
	v_mov_b32_e32 v46, v2
	v_mov_b32_e32 v47, v2
	v_mov_b32_e32 v48, v2
	v_mov_b32_e32 v49, v2
	v_mov_b32_e32 v58, v2
	v_mov_b32_e32 v59, v2
	v_mov_b32_e32 v60, v2
	v_mov_b32_e32 v61, v2
	v_mov_b32_e32 v62, v2
	v_mov_b32_e32 v63, v2
	v_mov_b32_e32 v64, v2
	v_mov_b32_e32 v65, v2
	v_mov_b32_e32 v66, v2
	v_mov_b32_e32 v67, v2
	v_mov_b32_e32 v68, v2
	v_mov_b32_e32 v69, v2
	v_mov_b32_e32 v70, v2
	v_mov_b32_e32 v71, v2
	v_mov_b32_e32 v72, v2
	v_mov_b32_e32 v73, v2
	v_mov_b32_e32 v82, v2
	v_mov_b32_e32 v83, v2
	v_mov_b32_e32 v84, v2
	v_mov_b32_e32 v85, v2
	v_mov_b32_e32 v86, v2
	v_mov_b32_e32 v87, v2
	v_mov_b32_e32 v88, v2
	v_mov_b32_e32 v89, v2
	v_mov_b32_e32 v98, v2
	v_mov_b32_e32 v99, v2
	v_mov_b32_e32 v100, v2
	v_mov_b32_e32 v101, v2
	v_mov_b32_e32 v102, v2
	v_mov_b32_e32 v103, v2
	v_mov_b32_e32 v104, v2
	v_mov_b32_e32 v105, v2
	v_mov_b32_e32 v114, v2
	v_mov_b32_e32 v115, v2
	v_mov_b32_e32 v116, v2
	v_mov_b32_e32 v117, v2
	v_mov_b32_e32 v122, v2
	v_mov_b32_e32 v123, v2
	v_mov_b32_e32 v124, v2
	v_mov_b32_e32 v125, v2
	v_mov_b32_e32 v74, v2
	v_mov_b32_e32 v75, v2
	v_mov_b32_e32 v76, v2
	v_mov_b32_e32 v77, v2
	v_mov_b32_e32 v78, v2
	v_mov_b32_e32 v79, v2
	v_mov_b32_e32 v80, v2
	v_mov_b32_e32 v81, v2
	v_mov_b32_e32 v90, v2
	v_mov_b32_e32 v91, v2
	v_mov_b32_e32 v92, v2
	v_mov_b32_e32 v93, v2
	v_mov_b32_e32 v94, v2
	v_mov_b32_e32 v95, v2
	v_mov_b32_e32 v96, v2
	v_mov_b32_e32 v97, v2
	v_mov_b32_e32 v106, v2
	v_mov_b32_e32 v107, v2
	v_mov_b32_e32 v108, v2
	v_mov_b32_e32 v109, v2
	v_mov_b32_e32 v110, v2
	v_mov_b32_e32 v111, v2
	v_mov_b32_e32 v112, v2
	v_mov_b32_e32 v113, v2
	v_mov_b32_e32 v130, v2
	v_mov_b32_e32 v131, v2
	v_mov_b32_e32 v132, v2
	v_mov_b32_e32 v133, v2
	v_mov_b32_e32 v134, v2
	v_mov_b32_e32 v135, v2
	v_mov_b32_e32 v136, v2
	v_mov_b32_e32 v137, v2
	s_andn2_b64 vcc, exec, s[38:39]
	s_cbranch_vccnz .LBB0_1627
	s_branch .LBB0_1628

.LBB0_1782:
	s_ashr_i32 s23, s22, 31
	s_lshl_b64 s[8:9], s[22:23], 19
	s_add_u32 s24, s34, s8
	s_addc_u32 s25, s35, s9
	s_and_b64 s[8:9], s[38:39], exec
	s_cselect_b32 s8, s25, s7
	s_cselect_b32 s9, s24, s6
	s_ashr_i32 s21, s20, 31
	s_lshl_b64 s[26:27], s[20:21], 19
	s_add_u32 s26, s10, s26
	s_addc_u32 s27, s11, s27
	s_and_b64 s[30:31], s[38:39], exec
	s_cselect_b32 s21, s27, s29
	s_cselect_b32 s23, s26, s28
	s_add_u32 s33, s28, 0x100
	s_addc_u32 s40, s29, 0
	s_add_u32 s6, s6, 0x40080
	v_mov_b32_e32 v2, 0
	s_addc_u32 s7, s7, 0
	s_mov_b32 s41, -2
	v_mov_b32_e32 v3, v2
	v_mov_b32_e32 v4, v2
	v_mov_b32_e32 v5, v2
	v_mov_b32_e32 v6, v2
	v_mov_b32_e32 v7, v2
	v_mov_b32_e32 v8, v2
	v_mov_b32_e32 v9, v2
	v_mov_b32_e32 v14, v2
	v_mov_b32_e32 v15, v2
	v_mov_b32_e32 v16, v2
	v_mov_b32_e32 v17, v2
	v_mov_b32_e32 v22, v2
	v_mov_b32_e32 v23, v2
	v_mov_b32_e32 v24, v2
	v_mov_b32_e32 v25, v2
	v_mov_b32_e32 v30, v2
	v_mov_b32_e32 v31, v2
	v_mov_b32_e32 v32, v2
	v_mov_b32_e32 v33, v2
	v_mov_b32_e32 v38, v2
	v_mov_b32_e32 v39, v2
	v_mov_b32_e32 v40, v2
	v_mov_b32_e32 v41, v2
	v_mov_b32_e32 v46, v2
	v_mov_b32_e32 v47, v2
	v_mov_b32_e32 v48, v2
	v_mov_b32_e32 v49, v2
	v_mov_b32_e32 v54, v2
	v_mov_b32_e32 v55, v2
	v_mov_b32_e32 v56, v2
	v_mov_b32_e32 v57, v2
	v_mov_b32_e32 v10, v2
	v_mov_b32_e32 v11, v2
	v_mov_b32_e32 v12, v2
	v_mov_b32_e32 v13, v2
	v_mov_b32_e32 v18, v2
	v_mov_b32_e32 v19, v2
	v_mov_b32_e32 v20, v2
	v_mov_b32_e32 v21, v2
	v_mov_b32_e32 v26, v2
	v_mov_b32_e32 v27, v2
	v_mov_b32_e32 v28, v2
	v_mov_b32_e32 v29, v2
	v_mov_b32_e32 v34, v2
	v_mov_b32_e32 v35, v2
	v_mov_b32_e32 v36, v2
	v_mov_b32_e32 v37, v2
	v_mov_b32_e32 v42, v2
	v_mov_b32_e32 v43, v2
	v_mov_b32_e32 v44, v2
	v_mov_b32_e32 v45, v2
	v_mov_b32_e32 v50, v2
	v_mov_b32_e32 v51, v2
	v_mov_b32_e32 v52, v2
	v_mov_b32_e32 v53, v2
	v_mov_b32_e32 v58, v2
	v_mov_b32_e32 v59, v2
	v_mov_b32_e32 v60, v2
	v_mov_b32_e32 v61, v2
	v_mov_b32_e32 v62, v2
	v_mov_b32_e32 v63, v2
	v_mov_b32_e32 v64, v2
	v_mov_b32_e32 v65, v2
	v_mov_b32_e32 v66, v2
	v_mov_b32_e32 v67, v2
	v_mov_b32_e32 v68, v2
	v_mov_b32_e32 v69, v2
	v_mov_b32_e32 v70, v2
	v_mov_b32_e32 v71, v2
	v_mov_b32_e32 v72, v2
	v_mov_b32_e32 v73, v2
	v_mov_b32_e32 v78, v2
	v_mov_b32_e32 v79, v2
	v_mov_b32_e32 v80, v2
	v_mov_b32_e32 v81, v2
	v_mov_b32_e32 v86, v2
	v_mov_b32_e32 v87, v2
	v_mov_b32_e32 v88, v2
	v_mov_b32_e32 v89, v2
	v_mov_b32_e32 v94, v2
	v_mov_b32_e32 v95, v2
	v_mov_b32_e32 v96, v2
	v_mov_b32_e32 v97, v2
	v_mov_b32_e32 v102, v2
	v_mov_b32_e32 v103, v2
	v_mov_b32_e32 v104, v2
	v_mov_b32_e32 v105, v2
	v_mov_b32_e32 v110, v2
	v_mov_b32_e32 v111, v2
	v_mov_b32_e32 v112, v2
	v_mov_b32_e32 v113, v2
	v_mov_b32_e32 v118, v2
	v_mov_b32_e32 v119, v2
	v_mov_b32_e32 v120, v2
	v_mov_b32_e32 v121, v2
	v_mov_b32_e32 v74, v2
	v_mov_b32_e32 v75, v2
	v_mov_b32_e32 v76, v2
	v_mov_b32_e32 v77, v2
	v_mov_b32_e32 v82, v2
	v_mov_b32_e32 v83, v2
	v_mov_b32_e32 v84, v2
	v_mov_b32_e32 v85, v2
	v_mov_b32_e32 v90, v2
	v_mov_b32_e32 v91, v2
	v_mov_b32_e32 v92, v2
	v_mov_b32_e32 v93, v2
	v_mov_b32_e32 v98, v2
	v_mov_b32_e32 v99, v2
	v_mov_b32_e32 v100, v2
	v_mov_b32_e32 v101, v2
	v_mov_b32_e32 v106, v2
	v_mov_b32_e32 v107, v2
	v_mov_b32_e32 v108, v2
	v_mov_b32_e32 v109, v2
	v_mov_b32_e32 v114, v2
	v_mov_b32_e32 v115, v2
	v_mov_b32_e32 v116, v2
	v_mov_b32_e32 v117, v2
	v_mov_b32_e32 v122, v2
	v_mov_b32_e32 v123, v2
	v_mov_b32_e32 v124, v2
	v_mov_b32_e32 v125, v2
	v_mov_b32_e32 v126, v2
	v_mov_b32_e32 v127, v2
	v_mov_b32_e32 v128, v2
	v_mov_b32_e32 v129, v2
	s_waitcnt vmcnt(0)
	v_add_u32_e32 v165, 0x10000, v181
.LBB0_1783:
	s_add_u32 s28, s6, 0xfffc0080
	s_addc_u32 s29, s7, -1
	s_add_i32 s53, 0, 0x10000
	s_cmp_eq_u32 s41, 12
	s_cselect_b32 s31, s8, s29
	s_cselect_b32 s30, s9, s28
	s_cselect_b32 s29, s21, s40
	s_cselect_b32 s28, s23, s33
	s_add_i32 s62, 0, 0x14000
	ds_read_b128 v[130:133], v165
	ds_read_b128 v[134:137], v165 offset:1024
	ds_read_b128 v[138:141], v165 offset:2048
	ds_read_b128 v[142:145], v165 offset:3072
	ds_read_b128 v[146:149], v165 offset:16384
	ds_read_b128 v[150:153], v165 offset:17408
	ds_read_b128 v[154:157], v165 offset:18432
	ds_read_b128 v[168:171], v165 offset:19456
	s_add_i32 m0, s37, 0xc000
	ds_read_b128 v[172:175], v183
	ds_read_b128 v[184:187], v183 offset:1024
	ds_read_b128 v[188:191], v183 offset:2048
	ds_read_b128 v[192:195], v183 offset:3072
	ds_read_b128 v[196:199], v183 offset:4096
	ds_read_b128 v[200:203], v183 offset:5120
	ds_read_b128 v[204:207], v183 offset:6144
	global_load_lds_dwordx4 v166, s[6:7]
	s_add_i32 m0, s37, 0xe000
	ds_read_b128 v[216:219], v183 offset:7168
	global_load_lds_dwordx4 v164, s[6:7]
	s_waitcnt vmcnt(8) lgkmcnt(0)
	s_barrier
	v_mfma_f32_16x16x32_bf16 v[126:129], v[130:133], v[172:175], v[126:129]
	v_mfma_f32_16x16x32_bf16 v[122:125], v[138:141], v[172:175], v[122:125]
	v_mfma_f32_16x16x32_bf16 v[114:117], v[130:133], v[188:191], v[114:117]
	v_mfma_f32_16x16x32_bf16 v[106:109], v[138:141], v[188:191], v[106:109]
	v_mfma_f32_16x16x32_bf16 v[98:101], v[130:133], v[196:199], v[98:101]
	v_mfma_f32_16x16x32_bf16 v[90:93], v[138:141], v[196:199], v[90:93]
	v_mfma_f32_16x16x32_bf16 v[82:85], v[130:133], v[204:207], v[82:85]
	v_mfma_f32_16x16x32_bf16 v[74:77], v[138:141], v[204:207], v[74:77]
	v_mfma_f32_16x16x32_bf16 v[126:129], v[134:137], v[184:187], v[126:129]
	v_mfma_f32_16x16x32_bf16 v[122:125], v[142:145], v[184:187], v[122:125]
	v_mfma_f32_16x16x32_bf16 v[114:117], v[134:137], v[192:195], v[114:117]
	v_mfma_f32_16x16x32_bf16 v[106:109], v[142:145], v[192:195], v[106:109]
	v_mfma_f32_16x16x32_bf16 v[98:101], v[134:137], v[200:203], v[98:101]
	v_mfma_f32_16x16x32_bf16 v[90:93], v[142:145], v[200:203], v[90:93]
	v_mfma_f32_16x16x32_bf16 v[82:85], v[134:137], v[216:219], v[82:85]
	v_mfma_f32_16x16x32_bf16 v[74:77], v[142:145], v[216:219], v[74:77]
	v_mfma_f32_16x16x32_bf16 v[118:121], v[146:149], v[172:175], v[118:121]
	v_mfma_f32_16x16x32_bf16 v[110:113], v[154:157], v[172:175], v[110:113]
	v_mfma_f32_16x16x32_bf16 v[102:105], v[146:149], v[188:191], v[102:105]
	v_mfma_f32_16x16x32_bf16 v[94:97], v[154:157], v[188:191], v[94:97]
	v_mfma_f32_16x16x32_bf16 v[86:89], v[146:149], v[196:199], v[86:89]
	v_mfma_f32_16x16x32_bf16 v[78:81], v[154:157], v[196:199], v[78:81]
	v_mfma_f32_16x16x32_bf16 v[70:73], v[146:149], v[204:207], v[70:73]
	v_mfma_f32_16x16x32_bf16 v[66:69], v[154:157], v[204:207], v[66:69]
	v_mfma_f32_16x16x32_bf16 v[118:121], v[150:153], v[184:187], v[118:121]
	v_mfma_f32_16x16x32_bf16 v[110:113], v[168:171], v[184:187], v[110:113]
	v_mfma_f32_16x16x32_bf16 v[102:105], v[150:153], v[192:195], v[102:105]
	v_mfma_f32_16x16x32_bf16 v[94:97], v[168:171], v[192:195], v[94:97]
	v_mfma_f32_16x16x32_bf16 v[86:89], v[150:153], v[200:203], v[86:89]
	v_mfma_f32_16x16x32_bf16 v[78:81], v[168:171], v[200:203], v[78:81]
	v_mfma_f32_16x16x32_bf16 v[70:73], v[150:153], v[216:219], v[70:73]
	v_mfma_f32_16x16x32_bf16 v[66:69], v[168:171], v[216:219], v[66:69]
	s_barrier
	s_add_i32 s53, s53, s36
	v_lshl_add_u64 v[176:177], s[28:29], 0, v[162:163]
	s_mov_b32 m0, s53
	ds_read_b128 v[172:175], v183 offset:16384
	ds_read_b128 v[184:187], v183 offset:17408
	ds_read_b128 v[188:191], v183 offset:18432
	ds_read_b128 v[192:195], v183 offset:19456
	ds_read_b128 v[196:199], v183 offset:20480
	ds_read_b128 v[200:203], v183 offset:21504
	ds_read_b128 v[204:207], v183 offset:22528
	ds_read_b128 v[216:219], v183 offset:23552
	global_load_lds_dwordx4 v162, s[28:29]
	s_add_i32 m0, s53, 0x2000
	s_add_u32 s58, s28, 0x40000
	v_lshl_add_u64 v[208:209], s[28:29], 0, v[158:159]
	s_addc_u32 s59, s29, 0
	s_add_i32 s53, s62, s36
	global_load_lds_dwordx4 v158, s[28:29]
	s_mov_b32 m0, s53
	v_lshl_add_u64 v[222:223], s[30:31], 0, v[160:161]
	global_load_lds_dwordx4 v162, s[58:59]
	s_add_i32 m0, s53, 0x2000
	s_nop 0
	global_load_lds_dwordx4 v158, s[58:59]
	s_mov_b32 m0, s37
	v_lshl_add_u64 v[220:221], s[30:31], 0, v[0:1]
	global_load_lds_dwordx4 v0, s[30:31]
	s_mov_b32 m0, s44
	s_nop 0
	global_load_lds_dwordx4 v160, s[30:31]
	s_waitcnt vmcnt(8) lgkmcnt(0)
	s_barrier
	v_mfma_f32_16x16x32_bf16 v[62:65], v[130:133], v[172:175], v[62:65]
	v_mfma_f32_16x16x32_bf16 v[58:61], v[138:141], v[172:175], v[58:61]
	v_mfma_f32_16x16x32_bf16 v[50:53], v[130:133], v[188:191], v[50:53]
	v_mfma_f32_16x16x32_bf16 v[42:45], v[138:141], v[188:191], v[42:45]
	v_mfma_f32_16x16x32_bf16 v[34:37], v[130:133], v[196:199], v[34:37]
	v_mfma_f32_16x16x32_bf16 v[26:29], v[138:141], v[196:199], v[26:29]
	v_mfma_f32_16x16x32_bf16 v[18:21], v[130:133], v[204:207], v[18:21]
	v_mfma_f32_16x16x32_bf16 v[10:13], v[138:141], v[204:207], v[10:13]
	v_mfma_f32_16x16x32_bf16 v[62:65], v[134:137], v[184:187], v[62:65]
	v_mfma_f32_16x16x32_bf16 v[58:61], v[142:145], v[184:187], v[58:61]
	v_mfma_f32_16x16x32_bf16 v[50:53], v[134:137], v[192:195], v[50:53]
	v_mfma_f32_16x16x32_bf16 v[42:45], v[142:145], v[192:195], v[42:45]
	v_mfma_f32_16x16x32_bf16 v[34:37], v[134:137], v[200:203], v[34:37]
	v_mfma_f32_16x16x32_bf16 v[26:29], v[142:145], v[200:203], v[26:29]
	v_mfma_f32_16x16x32_bf16 v[18:21], v[134:137], v[216:219], v[18:21]
	v_mfma_f32_16x16x32_bf16 v[10:13], v[142:145], v[216:219], v[10:13]
	v_mfma_f32_16x16x32_bf16 v[54:57], v[146:149], v[172:175], v[54:57]
	v_mfma_f32_16x16x32_bf16 v[46:49], v[154:157], v[172:175], v[46:49]
	v_mfma_f32_16x16x32_bf16 v[38:41], v[146:149], v[188:191], v[38:41]
	v_mfma_f32_16x16x32_bf16 v[30:33], v[154:157], v[188:191], v[30:33]
	v_mfma_f32_16x16x32_bf16 v[22:25], v[146:149], v[196:199], v[22:25]
	v_mfma_f32_16x16x32_bf16 v[14:17], v[154:157], v[196:199], v[14:17]
	v_mfma_f32_16x16x32_bf16 v[6:9], v[146:149], v[204:207], v[6:9]
	v_mfma_f32_16x16x32_bf16 v[2:5], v[154:157], v[204:207], v[2:5]
	v_mfma_f32_16x16x32_bf16 v[54:57], v[150:153], v[184:187], v[54:57]
	v_mfma_f32_16x16x32_bf16 v[46:49], v[168:171], v[184:187], v[46:49]
	v_mfma_f32_16x16x32_bf16 v[38:41], v[150:153], v[192:195], v[38:41]
	v_mfma_f32_16x16x32_bf16 v[30:33], v[168:171], v[192:195], v[30:33]
	v_mfma_f32_16x16x32_bf16 v[22:25], v[150:153], v[200:203], v[22:25]
	v_mfma_f32_16x16x32_bf16 v[14:17], v[168:171], v[200:203], v[14:17]
	v_mfma_f32_16x16x32_bf16 v[6:9], v[150:153], v[216:219], v[6:9]
	v_mfma_f32_16x16x32_bf16 v[2:5], v[168:171], v[216:219], v[2:5]
	s_barrier
	s_add_i32 s53, 0, 0x18000
	s_add_i32 s58, 0, 0x1c000
	ds_read_b128 v[130:133], v165 offset:32768
	ds_read_b128 v[134:137], v165 offset:33792
	ds_read_b128 v[138:141], v165 offset:34816
	ds_read_b128 v[142:145], v165 offset:35840
	ds_read_b128 v[146:149], v165 offset:49152
	ds_read_b128 v[150:153], v165 offset:50176
	ds_read_b128 v[154:157], v165 offset:51200
	ds_read_b128 v[168:171], v165 offset:52224
	s_add_u32 s30, s30, 0x40000
	s_addc_u32 s31, s31, 0
	s_mov_b32 m0, s45
	ds_read_b128 v[172:175], v183 offset:32768
	ds_read_b128 v[184:187], v183 offset:33792
	ds_read_b128 v[188:191], v183 offset:34816
	ds_read_b128 v[192:195], v183 offset:35840
	ds_read_b128 v[196:199], v183 offset:36864
	ds_read_b128 v[200:203], v183 offset:37888
	ds_read_b128 v[204:207], v183 offset:38912
	ds_read_b128 v[216:219], v183 offset:39936
	global_load_lds_dwordx4 v0, s[30:31]
	s_mov_b32 m0, s46
	v_lshl_add_u64 v[224:225], s[30:31], 0, v[160:161]
	global_load_lds_dwordx4 v160, s[30:31]
	s_waitcnt vmcnt(8) lgkmcnt(0)
	s_barrier
	v_mfma_f32_16x16x32_bf16 v[126:129], v[130:133], v[172:175], v[126:129]
	v_mfma_f32_16x16x32_bf16 v[122:125], v[138:141], v[172:175], v[122:125]
	v_mfma_f32_16x16x32_bf16 v[114:117], v[130:133], v[188:191], v[114:117]
	v_mfma_f32_16x16x32_bf16 v[106:109], v[138:141], v[188:191], v[106:109]
	v_mfma_f32_16x16x32_bf16 v[98:101], v[130:133], v[196:199], v[98:101]
	v_mfma_f32_16x16x32_bf16 v[90:93], v[138:141], v[196:199], v[90:93]
	v_mfma_f32_16x16x32_bf16 v[82:85], v[130:133], v[204:207], v[82:85]
	v_mfma_f32_16x16x32_bf16 v[74:77], v[138:141], v[204:207], v[74:77]
	v_mfma_f32_16x16x32_bf16 v[126:129], v[134:137], v[184:187], v[126:129]
	v_mfma_f32_16x16x32_bf16 v[122:125], v[142:145], v[184:187], v[122:125]
	v_mfma_f32_16x16x32_bf16 v[114:117], v[134:137], v[192:195], v[114:117]
	v_mfma_f32_16x16x32_bf16 v[106:109], v[142:145], v[192:195], v[106:109]
	v_mfma_f32_16x16x32_bf16 v[98:101], v[134:137], v[200:203], v[98:101]
	v_mfma_f32_16x16x32_bf16 v[90:93], v[142:145], v[200:203], v[90:93]
	v_mfma_f32_16x16x32_bf16 v[82:85], v[134:137], v[216:219], v[82:85]
	v_mfma_f32_16x16x32_bf16 v[74:77], v[142:145], v[216:219], v[74:77]
	v_mfma_f32_16x16x32_bf16 v[118:121], v[146:149], v[172:175], v[118:121]
	v_mfma_f32_16x16x32_bf16 v[110:113], v[154:157], v[172:175], v[110:113]
	v_mfma_f32_16x16x32_bf16 v[102:105], v[146:149], v[188:191], v[102:105]
	v_mfma_f32_16x16x32_bf16 v[94:97], v[154:157], v[188:191], v[94:97]
	v_mfma_f32_16x16x32_bf16 v[86:89], v[146:149], v[196:199], v[86:89]
	v_mfma_f32_16x16x32_bf16 v[78:81], v[154:157], v[196:199], v[78:81]
	v_mfma_f32_16x16x32_bf16 v[70:73], v[146:149], v[204:207], v[70:73]
	v_mfma_f32_16x16x32_bf16 v[66:69], v[154:157], v[204:207], v[66:69]
	v_mfma_f32_16x16x32_bf16 v[118:121], v[150:153], v[184:187], v[118:121]
	v_mfma_f32_16x16x32_bf16 v[110:113], v[168:171], v[184:187], v[110:113]
	v_mfma_f32_16x16x32_bf16 v[102:105], v[150:153], v[192:195], v[102:105]
	v_mfma_f32_16x16x32_bf16 v[94:97], v[168:171], v[192:195], v[94:97]
	v_mfma_f32_16x16x32_bf16 v[86:89], v[150:153], v[200:203], v[86:89]
	v_mfma_f32_16x16x32_bf16 v[78:81], v[168:171], v[200:203], v[78:81]
	v_mfma_f32_16x16x32_bf16 v[70:73], v[150:153], v[216:219], v[70:73]
	v_mfma_f32_16x16x32_bf16 v[66:69], v[168:171], v[216:219], v[66:69]
	s_barrier
	s_add_i32 s30, s53, s36
	v_lshl_add_u64 v[176:177], v[176:177], 0, s[56:57]
	s_mov_b32 m0, s30
	ds_read_b128 v[172:175], v183 offset:49152
	ds_read_b128 v[184:187], v183 offset:50176
	ds_read_b128 v[188:191], v183 offset:51200
	ds_read_b128 v[192:195], v183 offset:52224
	ds_read_b128 v[196:199], v183 offset:53248
	ds_read_b128 v[200:203], v183 offset:54272
	ds_read_b128 v[204:207], v183 offset:55296
	ds_read_b128 v[216:219], v183 offset:56320
	global_load_lds_dwordx4 v[176:177], off
	s_add_i32 m0, s30, 0x2000
	s_add_u32 s28, s28, 0x40080
	v_lshl_add_u64 v[176:177], v[208:209], 0, s[56:57]
	s_addc_u32 s29, s29, 0
	s_add_i32 s30, s58, s36
	global_load_lds_dwordx4 v[176:177], off
	s_mov_b32 m0, s30
	s_nop 0
	global_load_lds_dwordx4 v162, s[28:29]
	s_add_i32 m0, s30, 0x2000
	s_nop 0
	global_load_lds_dwordx4 v158, s[28:29]
	s_mov_b32 m0, s47
	v_lshl_add_u64 v[176:177], v[220:221], 0, s[56:57]
	global_load_lds_dwordx4 v[176:177], off
	s_mov_b32 m0, s48
	v_lshl_add_u64 v[176:177], v[222:223], 0, s[56:57]
	global_load_lds_dwordx4 v[176:177], off
	s_waitcnt vmcnt(8) lgkmcnt(0)
	s_barrier
	v_mfma_f32_16x16x32_bf16 v[62:65], v[130:133], v[172:175], v[62:65]
	v_mfma_f32_16x16x32_bf16 v[58:61], v[138:141], v[172:175], v[58:61]
	v_mfma_f32_16x16x32_bf16 v[50:53], v[130:133], v[188:191], v[50:53]
	v_mfma_f32_16x16x32_bf16 v[42:45], v[138:141], v[188:191], v[42:45]
	v_mfma_f32_16x16x32_bf16 v[34:37], v[130:133], v[196:199], v[34:37]
	v_mfma_f32_16x16x32_bf16 v[26:29], v[138:141], v[196:199], v[26:29]
	v_mfma_f32_16x16x32_bf16 v[18:21], v[130:133], v[204:207], v[18:21]
	v_mfma_f32_16x16x32_bf16 v[10:13], v[138:141], v[204:207], v[10:13]
	v_mfma_f32_16x16x32_bf16 v[62:65], v[134:137], v[184:187], v[62:65]
	v_mfma_f32_16x16x32_bf16 v[58:61], v[142:145], v[184:187], v[58:61]
	v_mfma_f32_16x16x32_bf16 v[50:53], v[134:137], v[192:195], v[50:53]
	v_mfma_f32_16x16x32_bf16 v[42:45], v[142:145], v[192:195], v[42:45]
	v_mfma_f32_16x16x32_bf16 v[34:37], v[134:137], v[200:203], v[34:37]
	v_mfma_f32_16x16x32_bf16 v[26:29], v[142:145], v[200:203], v[26:29]
	v_mfma_f32_16x16x32_bf16 v[18:21], v[134:137], v[216:219], v[18:21]
	v_mfma_f32_16x16x32_bf16 v[10:13], v[142:145], v[216:219], v[10:13]
	v_mfma_f32_16x16x32_bf16 v[54:57], v[146:149], v[172:175], v[54:57]
	v_mfma_f32_16x16x32_bf16 v[46:49], v[154:157], v[172:175], v[46:49]
	v_mfma_f32_16x16x32_bf16 v[38:41], v[146:149], v[188:191], v[38:41]
	v_mfma_f32_16x16x32_bf16 v[30:33], v[154:157], v[188:191], v[30:33]
	v_mfma_f32_16x16x32_bf16 v[22:25], v[146:149], v[196:199], v[22:25]
	v_mfma_f32_16x16x32_bf16 v[14:17], v[154:157], v[196:199], v[14:17]
	v_mfma_f32_16x16x32_bf16 v[6:9], v[146:149], v[204:207], v[6:9]
	v_mfma_f32_16x16x32_bf16 v[2:5], v[154:157], v[204:207], v[2:5]
	v_mfma_f32_16x16x32_bf16 v[54:57], v[150:153], v[184:187], v[54:57]
	v_mfma_f32_16x16x32_bf16 v[46:49], v[168:171], v[184:187], v[46:49]
	v_mfma_f32_16x16x32_bf16 v[38:41], v[150:153], v[192:195], v[38:41]
	v_mfma_f32_16x16x32_bf16 v[30:33], v[168:171], v[192:195], v[30:33]
	v_mfma_f32_16x16x32_bf16 v[22:25], v[150:153], v[200:203], v[22:25]
	v_mfma_f32_16x16x32_bf16 v[14:17], v[168:171], v[200:203], v[14:17]
	v_mfma_f32_16x16x32_bf16 v[6:9], v[150:153], v[216:219], v[6:9]
	v_mfma_f32_16x16x32_bf16 v[2:5], v[168:171], v[216:219], v[2:5]
	s_barrier
	s_add_i32 s41, s41, 2
	s_add_u32 s33, s33, 0x100
	s_addc_u32 s40, s40, 0
	s_add_u32 s6, s6, 0x100
	s_addc_u32 s7, s7, 0
	s_cmp_gt_u32 s41, 13
	s_cbranch_scc0 .LBB0_1783
	s_and_b64 vcc, exec, s[18:19]
	s_cbranch_vccz .LBB0_1786
	s_barrier

.LBB0_1798:
	s_ashr_i32 s17, s16, 31
	s_lshl_b64 s[8:9], s[16:17], 19
	s_add_u32 s20, s30, s8
	s_addc_u32 s21, s31, s9
	s_and_b64 s[8:9], s[18:19], exec
	s_cselect_b32 s8, s21, s27
	s_cselect_b32 s9, s20, s26
	s_ashr_i32 s15, s14, 31
	s_lshl_b64 s[22:23], s[14:15], 19
	s_add_u32 s22, s5, s22
	s_addc_u32 s23, s34, s23
	s_and_b64 s[28:29], s[18:19], exec
	s_cselect_b32 s15, s23, s25
	s_cselect_b32 s17, s22, s24
	s_add_u32 s45, s24, 0x100
	s_addc_u32 s46, s25, 0
	s_add_u32 s24, s26, 0x40080
	v_mov_b32_e32 v2, 0
	s_addc_u32 s25, s27, 0
	s_mov_b32 s47, -2
	v_mov_b32_e32 v3, v2
	v_mov_b32_e32 v4, v2
	v_mov_b32_e32 v5, v2
	v_mov_b32_e32 v6, v2
	v_mov_b32_e32 v7, v2
	v_mov_b32_e32 v8, v2
	v_mov_b32_e32 v9, v2
	v_mov_b32_e32 v10, v2
	v_mov_b32_e32 v11, v2
	v_mov_b32_e32 v12, v2
	v_mov_b32_e32 v13, v2
	v_mov_b32_e32 v18, v2
	v_mov_b32_e32 v19, v2
	v_mov_b32_e32 v20, v2
	v_mov_b32_e32 v21, v2
	v_mov_b32_e32 v26, v2
	v_mov_b32_e32 v27, v2
	v_mov_b32_e32 v28, v2
	v_mov_b32_e32 v29, v2
	v_mov_b32_e32 v34, v2
	v_mov_b32_e32 v35, v2
	v_mov_b32_e32 v36, v2
	v_mov_b32_e32 v37, v2
	v_mov_b32_e32 v42, v2
	v_mov_b32_e32 v43, v2
	v_mov_b32_e32 v44, v2
	v_mov_b32_e32 v45, v2
	v_mov_b32_e32 v50, v2
	v_mov_b32_e32 v51, v2
	v_mov_b32_e32 v52, v2
	v_mov_b32_e32 v53, v2
	v_mov_b32_e32 v14, v2
	v_mov_b32_e32 v15, v2
	v_mov_b32_e32 v16, v2
	v_mov_b32_e32 v17, v2
	v_mov_b32_e32 v22, v2
	v_mov_b32_e32 v23, v2
	v_mov_b32_e32 v24, v2
	v_mov_b32_e32 v25, v2
	v_mov_b32_e32 v30, v2
	v_mov_b32_e32 v31, v2
	v_mov_b32_e32 v32, v2
	v_mov_b32_e32 v33, v2
	v_mov_b32_e32 v38, v2
	v_mov_b32_e32 v39, v2
	v_mov_b32_e32 v40, v2
	v_mov_b32_e32 v41, v2
	v_mov_b32_e32 v46, v2
	v_mov_b32_e32 v47, v2
	v_mov_b32_e32 v48, v2
	v_mov_b32_e32 v49, v2
	v_mov_b32_e32 v54, v2
	v_mov_b32_e32 v55, v2
	v_mov_b32_e32 v56, v2
	v_mov_b32_e32 v57, v2
	v_mov_b32_e32 v58, v2
	v_mov_b32_e32 v59, v2
	v_mov_b32_e32 v60, v2
	v_mov_b32_e32 v61, v2
	v_mov_b32_e32 v62, v2
	v_mov_b32_e32 v63, v2
	v_mov_b32_e32 v64, v2
	v_mov_b32_e32 v65, v2
	v_mov_b32_e32 v66, v2
	v_mov_b32_e32 v67, v2
	v_mov_b32_e32 v68, v2
	v_mov_b32_e32 v69, v2
	v_mov_b32_e32 v70, v2
	v_mov_b32_e32 v71, v2
	v_mov_b32_e32 v72, v2
	v_mov_b32_e32 v73, v2
	v_mov_b32_e32 v74, v2
	v_mov_b32_e32 v75, v2
	v_mov_b32_e32 v76, v2
	v_mov_b32_e32 v77, v2
	v_mov_b32_e32 v82, v2
	v_mov_b32_e32 v83, v2
	v_mov_b32_e32 v84, v2
	v_mov_b32_e32 v85, v2
	v_mov_b32_e32 v90, v2
	v_mov_b32_e32 v91, v2
	v_mov_b32_e32 v92, v2
	v_mov_b32_e32 v93, v2
	v_mov_b32_e32 v98, v2
	v_mov_b32_e32 v99, v2
	v_mov_b32_e32 v100, v2
	v_mov_b32_e32 v101, v2
	v_mov_b32_e32 v106, v2
	v_mov_b32_e32 v107, v2
	v_mov_b32_e32 v108, v2
	v_mov_b32_e32 v109, v2
	v_mov_b32_e32 v114, v2
	v_mov_b32_e32 v115, v2
	v_mov_b32_e32 v116, v2
	v_mov_b32_e32 v117, v2
	v_mov_b32_e32 v78, v2
	v_mov_b32_e32 v79, v2
	v_mov_b32_e32 v80, v2
	v_mov_b32_e32 v81, v2
	v_mov_b32_e32 v86, v2
	v_mov_b32_e32 v87, v2
	v_mov_b32_e32 v88, v2
	v_mov_b32_e32 v89, v2
	v_mov_b32_e32 v94, v2
	v_mov_b32_e32 v95, v2
	v_mov_b32_e32 v96, v2
	v_mov_b32_e32 v97, v2
	v_mov_b32_e32 v102, v2
	v_mov_b32_e32 v103, v2
	v_mov_b32_e32 v104, v2
	v_mov_b32_e32 v105, v2
	v_mov_b32_e32 v110, v2
	v_mov_b32_e32 v111, v2
	v_mov_b32_e32 v112, v2
	v_mov_b32_e32 v113, v2
	v_mov_b32_e32 v118, v2
	v_mov_b32_e32 v119, v2
	v_mov_b32_e32 v120, v2
	v_mov_b32_e32 v121, v2
	v_mov_b32_e32 v122, v2
	v_mov_b32_e32 v123, v2
	v_mov_b32_e32 v124, v2
	v_mov_b32_e32 v125, v2
	v_mov_b32_e32 v126, v2
	v_mov_b32_e32 v127, v2
	v_mov_b32_e32 v128, v2
	v_mov_b32_e32 v129, v2
	v_add_u32_e32 v139, 0x10000, v144
.LBB0_1799:
	s_add_u32 s26, s24, 0xfffc0080
	s_addc_u32 s27, s25, -1
	s_add_i32 s48, 0, 0x10000
	s_cmp_eq_u32 s47, 12
	s_cselect_b32 s29, s8, s27
	s_cselect_b32 s28, s9, s26
	s_cselect_b32 s27, s15, s46
	s_cselect_b32 s26, s17, s45
	s_add_i32 s52, 0, 0x14000
	ds_read_b128 v[148:151], v139
	ds_read_b128 v[152:155], v139 offset:1024
	ds_read_b128 v[156:159], v139 offset:2048
	ds_read_b128 v[160:163], v139 offset:3072
	ds_read_b128 v[164:167], v139 offset:16384
	ds_read_b128 v[168:171], v139 offset:17408
	ds_read_b128 v[172:175], v139 offset:18432
	ds_read_b128 v[180:183], v139 offset:19456
	s_add_i32 m0, s36, 0xc000
	ds_read_b128 v[184:187], v146
	ds_read_b128 v[188:191], v146 offset:1024
	ds_read_b128 v[192:195], v146 offset:2048
	ds_read_b128 v[196:199], v146 offset:3072
	ds_read_b128 v[200:203], v146 offset:4096
	ds_read_b128 v[204:207], v146 offset:5120
	ds_read_b128 v[216:219], v146 offset:6144
	global_load_lds_dwordx4 v140, s[24:25]
	s_add_i32 m0, s36, 0xe000
	ds_read_b128 v[220:223], v146 offset:7168
	global_load_lds_dwordx4 v138, s[24:25]
	s_waitcnt vmcnt(8) lgkmcnt(0)
	s_barrier
	v_mfma_f32_16x16x32_bf16 v[126:129], v[148:151], v[184:187], v[126:129]
	v_mfma_f32_16x16x32_bf16 v[122:125], v[156:159], v[184:187], v[122:125]
	v_mfma_f32_16x16x32_bf16 v[118:121], v[148:151], v[192:195], v[118:121]
	v_mfma_f32_16x16x32_bf16 v[110:113], v[156:159], v[192:195], v[110:113]
	v_mfma_f32_16x16x32_bf16 v[102:105], v[148:151], v[200:203], v[102:105]
	v_mfma_f32_16x16x32_bf16 v[94:97], v[156:159], v[200:203], v[94:97]
	v_mfma_f32_16x16x32_bf16 v[86:89], v[148:151], v[216:219], v[86:89]
	v_mfma_f32_16x16x32_bf16 v[78:81], v[156:159], v[216:219], v[78:81]
	v_mfma_f32_16x16x32_bf16 v[126:129], v[152:155], v[188:191], v[126:129]
	v_mfma_f32_16x16x32_bf16 v[122:125], v[160:163], v[188:191], v[122:125]
	v_mfma_f32_16x16x32_bf16 v[118:121], v[152:155], v[196:199], v[118:121]
	v_mfma_f32_16x16x32_bf16 v[110:113], v[160:163], v[196:199], v[110:113]
	v_mfma_f32_16x16x32_bf16 v[102:105], v[152:155], v[204:207], v[102:105]
	v_mfma_f32_16x16x32_bf16 v[94:97], v[160:163], v[204:207], v[94:97]
	v_mfma_f32_16x16x32_bf16 v[86:89], v[152:155], v[220:223], v[86:89]
	v_mfma_f32_16x16x32_bf16 v[78:81], v[160:163], v[220:223], v[78:81]
	v_mfma_f32_16x16x32_bf16 v[114:117], v[164:167], v[184:187], v[114:117]
	v_mfma_f32_16x16x32_bf16 v[106:109], v[172:175], v[184:187], v[106:109]
	v_mfma_f32_16x16x32_bf16 v[98:101], v[164:167], v[192:195], v[98:101]
	v_mfma_f32_16x16x32_bf16 v[90:93], v[172:175], v[192:195], v[90:93]
	v_mfma_f32_16x16x32_bf16 v[82:85], v[164:167], v[200:203], v[82:85]
	v_mfma_f32_16x16x32_bf16 v[74:77], v[172:175], v[200:203], v[74:77]
	v_mfma_f32_16x16x32_bf16 v[70:73], v[164:167], v[216:219], v[70:73]
	v_mfma_f32_16x16x32_bf16 v[66:69], v[172:175], v[216:219], v[66:69]
	v_mfma_f32_16x16x32_bf16 v[114:117], v[168:171], v[188:191], v[114:117]
	v_mfma_f32_16x16x32_bf16 v[106:109], v[180:183], v[188:191], v[106:109]
	v_mfma_f32_16x16x32_bf16 v[98:101], v[168:171], v[196:199], v[98:101]
	v_mfma_f32_16x16x32_bf16 v[90:93], v[180:183], v[196:199], v[90:93]
	v_mfma_f32_16x16x32_bf16 v[82:85], v[168:171], v[204:207], v[82:85]
	v_mfma_f32_16x16x32_bf16 v[74:77], v[180:183], v[204:207], v[74:77]
	v_mfma_f32_16x16x32_bf16 v[70:73], v[168:171], v[220:223], v[70:73]
	v_mfma_f32_16x16x32_bf16 v[66:69], v[180:183], v[220:223], v[66:69]
	s_barrier
	s_add_i32 s48, s48, s35
	v_lshl_add_u64 v[142:143], s[26:27], 0, v[134:135]
	s_mov_b32 m0, s48
	ds_read_b128 v[184:187], v146 offset:16384
	ds_read_b128 v[188:191], v146 offset:17408
	ds_read_b128 v[192:195], v146 offset:18432
	ds_read_b128 v[196:199], v146 offset:19456
	ds_read_b128 v[200:203], v146 offset:20480
	ds_read_b128 v[204:207], v146 offset:21504
	ds_read_b128 v[216:219], v146 offset:22528
	ds_read_b128 v[220:223], v146 offset:23552
	global_load_lds_dwordx4 v134, s[26:27]
	s_add_i32 m0, s48, 0x2000
	s_add_u32 s48, s26, 0x40000
	v_lshl_add_u64 v[176:177], s[26:27], 0, v[130:131]
	s_addc_u32 s49, s27, 0
	s_add_i32 s52, s52, s35
	global_load_lds_dwordx4 v130, s[26:27]
	s_mov_b32 m0, s52
	v_lshl_add_u64 v[224:225], s[28:29], 0, v[132:133]
	global_load_lds_dwordx4 v134, s[48:49]
	s_add_i32 m0, s52, 0x2000
	s_nop 0
	global_load_lds_dwordx4 v130, s[48:49]
	s_mov_b32 m0, s36
	v_lshl_add_u64 v[208:209], s[28:29], 0, v[136:137]
	global_load_lds_dwordx4 v136, s[28:29]
	s_mov_b32 m0, s37
	s_nop 0
	global_load_lds_dwordx4 v132, s[28:29]
	s_waitcnt vmcnt(8) lgkmcnt(0)
	s_barrier
	v_mfma_f32_16x16x32_bf16 v[62:65], v[148:151], v[184:187], v[62:65]
	v_mfma_f32_16x16x32_bf16 v[58:61], v[156:159], v[184:187], v[58:61]
	v_mfma_f32_16x16x32_bf16 v[54:57], v[148:151], v[192:195], v[54:57]
	v_mfma_f32_16x16x32_bf16 v[46:49], v[156:159], v[192:195], v[46:49]
	v_mfma_f32_16x16x32_bf16 v[38:41], v[148:151], v[200:203], v[38:41]
	v_mfma_f32_16x16x32_bf16 v[30:33], v[156:159], v[200:203], v[30:33]
	v_mfma_f32_16x16x32_bf16 v[22:25], v[148:151], v[216:219], v[22:25]
	v_mfma_f32_16x16x32_bf16 v[14:17], v[156:159], v[216:219], v[14:17]
	v_mfma_f32_16x16x32_bf16 v[62:65], v[152:155], v[188:191], v[62:65]
	v_mfma_f32_16x16x32_bf16 v[58:61], v[160:163], v[188:191], v[58:61]
	v_mfma_f32_16x16x32_bf16 v[54:57], v[152:155], v[196:199], v[54:57]
	v_mfma_f32_16x16x32_bf16 v[46:49], v[160:163], v[196:199], v[46:49]
	v_mfma_f32_16x16x32_bf16 v[38:41], v[152:155], v[204:207], v[38:41]
	v_mfma_f32_16x16x32_bf16 v[30:33], v[160:163], v[204:207], v[30:33]
	v_mfma_f32_16x16x32_bf16 v[22:25], v[152:155], v[220:223], v[22:25]
	v_mfma_f32_16x16x32_bf16 v[14:17], v[160:163], v[220:223], v[14:17]
	v_mfma_f32_16x16x32_bf16 v[50:53], v[164:167], v[184:187], v[50:53]
	v_mfma_f32_16x16x32_bf16 v[42:45], v[172:175], v[184:187], v[42:45]
	v_mfma_f32_16x16x32_bf16 v[34:37], v[164:167], v[192:195], v[34:37]
	v_mfma_f32_16x16x32_bf16 v[26:29], v[172:175], v[192:195], v[26:29]
	v_mfma_f32_16x16x32_bf16 v[18:21], v[164:167], v[200:203], v[18:21]
	v_mfma_f32_16x16x32_bf16 v[10:13], v[172:175], v[200:203], v[10:13]
	v_mfma_f32_16x16x32_bf16 v[6:9], v[164:167], v[216:219], v[6:9]
	v_mfma_f32_16x16x32_bf16 v[2:5], v[172:175], v[216:219], v[2:5]
	v_mfma_f32_16x16x32_bf16 v[50:53], v[168:171], v[188:191], v[50:53]
	v_mfma_f32_16x16x32_bf16 v[42:45], v[180:183], v[188:191], v[42:45]
	v_mfma_f32_16x16x32_bf16 v[34:37], v[168:171], v[196:199], v[34:37]
	v_mfma_f32_16x16x32_bf16 v[26:29], v[180:183], v[196:199], v[26:29]
	v_mfma_f32_16x16x32_bf16 v[18:21], v[168:171], v[204:207], v[18:21]
	v_mfma_f32_16x16x32_bf16 v[10:13], v[180:183], v[204:207], v[10:13]
	v_mfma_f32_16x16x32_bf16 v[6:9], v[168:171], v[220:223], v[6:9]
	v_mfma_f32_16x16x32_bf16 v[2:5], v[180:183], v[220:223], v[2:5]
	s_barrier
	s_add_i32 s48, 0, 0x18000
	s_add_i32 s49, 0, 0x1c000
	ds_read_b128 v[148:151], v139 offset:32768
	ds_read_b128 v[152:155], v139 offset:33792
	ds_read_b128 v[156:159], v139 offset:34816
	ds_read_b128 v[160:163], v139 offset:35840
	ds_read_b128 v[164:167], v139 offset:49152
	ds_read_b128 v[168:171], v139 offset:50176
	ds_read_b128 v[172:175], v139 offset:51200
	ds_read_b128 v[180:183], v139 offset:52224
	s_add_u32 s28, s28, 0x40000
	s_addc_u32 s29, s29, 0
	s_mov_b32 m0, s4
	ds_read_b128 v[184:187], v146 offset:32768
	ds_read_b128 v[188:191], v146 offset:33792
	ds_read_b128 v[192:195], v146 offset:34816
	ds_read_b128 v[196:199], v146 offset:35840
	ds_read_b128 v[200:203], v146 offset:36864
	ds_read_b128 v[204:207], v146 offset:37888
	ds_read_b128 v[216:219], v146 offset:38912
	global_load_lds_dwordx4 v136, s[28:29]
	s_mov_b32 m0, s33
	ds_read_b128 v[220:223], v146 offset:39936
	global_load_lds_dwordx4 v132, s[28:29]
	s_waitcnt vmcnt(8) lgkmcnt(0)
	s_barrier
	v_mfma_f32_16x16x32_bf16 v[126:129], v[148:151], v[184:187], v[126:129]
	v_mfma_f32_16x16x32_bf16 v[122:125], v[156:159], v[184:187], v[122:125]
	v_mfma_f32_16x16x32_bf16 v[118:121], v[148:151], v[192:195], v[118:121]
	v_mfma_f32_16x16x32_bf16 v[110:113], v[156:159], v[192:195], v[110:113]
	v_mfma_f32_16x16x32_bf16 v[102:105], v[148:151], v[200:203], v[102:105]
	v_mfma_f32_16x16x32_bf16 v[94:97], v[156:159], v[200:203], v[94:97]
	v_mfma_f32_16x16x32_bf16 v[86:89], v[148:151], v[216:219], v[86:89]
	v_mfma_f32_16x16x32_bf16 v[78:81], v[156:159], v[216:219], v[78:81]
	v_mfma_f32_16x16x32_bf16 v[126:129], v[152:155], v[188:191], v[126:129]
	v_mfma_f32_16x16x32_bf16 v[122:125], v[160:163], v[188:191], v[122:125]
	v_mfma_f32_16x16x32_bf16 v[118:121], v[152:155], v[196:199], v[118:121]
	v_mfma_f32_16x16x32_bf16 v[110:113], v[160:163], v[196:199], v[110:113]
	v_mfma_f32_16x16x32_bf16 v[102:105], v[152:155], v[204:207], v[102:105]
	v_mfma_f32_16x16x32_bf16 v[94:97], v[160:163], v[204:207], v[94:97]
	v_mfma_f32_16x16x32_bf16 v[86:89], v[152:155], v[220:223], v[86:89]
	v_mfma_f32_16x16x32_bf16 v[78:81], v[160:163], v[220:223], v[78:81]
	v_mfma_f32_16x16x32_bf16 v[114:117], v[164:167], v[184:187], v[114:117]
	v_mfma_f32_16x16x32_bf16 v[106:109], v[172:175], v[184:187], v[106:109]
	v_mfma_f32_16x16x32_bf16 v[98:101], v[164:167], v[192:195], v[98:101]
	v_mfma_f32_16x16x32_bf16 v[90:93], v[172:175], v[192:195], v[90:93]
	v_mfma_f32_16x16x32_bf16 v[82:85], v[164:167], v[200:203], v[82:85]
	v_mfma_f32_16x16x32_bf16 v[74:77], v[172:175], v[200:203], v[74:77]
	v_mfma_f32_16x16x32_bf16 v[70:73], v[164:167], v[216:219], v[70:73]
	v_mfma_f32_16x16x32_bf16 v[66:69], v[172:175], v[216:219], v[66:69]
	v_mfma_f32_16x16x32_bf16 v[114:117], v[168:171], v[188:191], v[114:117]
	v_mfma_f32_16x16x32_bf16 v[106:109], v[180:183], v[188:191], v[106:109]
	v_mfma_f32_16x16x32_bf16 v[98:101], v[168:171], v[196:199], v[98:101]
	v_mfma_f32_16x16x32_bf16 v[90:93], v[180:183], v[196:199], v[90:93]
	v_mfma_f32_16x16x32_bf16 v[82:85], v[168:171], v[204:207], v[82:85]
	v_mfma_f32_16x16x32_bf16 v[74:77], v[180:183], v[204:207], v[74:77]
	v_mfma_f32_16x16x32_bf16 v[70:73], v[168:171], v[220:223], v[70:73]
	v_mfma_f32_16x16x32_bf16 v[66:69], v[180:183], v[220:223], v[66:69]
	s_barrier
	s_add_i32 s28, s48, s35
	v_lshl_add_u64 v[142:143], v[142:143], 0, s[56:57]
	s_mov_b32 m0, s28
	ds_read_b128 v[184:187], v146 offset:49152
	ds_read_b128 v[188:191], v146 offset:50176
	ds_read_b128 v[192:195], v146 offset:51200
	ds_read_b128 v[196:199], v146 offset:52224
	ds_read_b128 v[200:203], v146 offset:53248
	ds_read_b128 v[204:207], v146 offset:54272
	ds_read_b128 v[216:219], v146 offset:55296
	ds_read_b128 v[220:223], v146 offset:56320
	global_load_lds_dwordx4 v[142:143], off
	s_add_i32 m0, s28, 0x2000
	s_add_u32 s26, s26, 0x40080
	v_lshl_add_u64 v[142:143], v[176:177], 0, s[56:57]
	s_addc_u32 s27, s27, 0
	s_add_i32 s28, s49, s35
	global_load_lds_dwordx4 v[142:143], off
	s_mov_b32 m0, s28
	s_nop 0
	global_load_lds_dwordx4 v134, s[26:27]
	s_add_i32 m0, s28, 0x2000
	s_nop 0
	global_load_lds_dwordx4 v130, s[26:27]
	s_mov_b32 m0, s38
	v_lshl_add_u64 v[142:143], v[208:209], 0, s[56:57]
	global_load_lds_dwordx4 v[142:143], off
	s_mov_b32 m0, s39
	v_lshl_add_u64 v[142:143], v[224:225], 0, s[56:57]
	global_load_lds_dwordx4 v[142:143], off
	s_waitcnt vmcnt(8) lgkmcnt(0)
	s_barrier
	v_mfma_f32_16x16x32_bf16 v[62:65], v[148:151], v[184:187], v[62:65]
	v_mfma_f32_16x16x32_bf16 v[58:61], v[156:159], v[184:187], v[58:61]
	v_mfma_f32_16x16x32_bf16 v[54:57], v[148:151], v[192:195], v[54:57]
	v_mfma_f32_16x16x32_bf16 v[46:49], v[156:159], v[192:195], v[46:49]
	v_mfma_f32_16x16x32_bf16 v[38:41], v[148:151], v[200:203], v[38:41]
	v_mfma_f32_16x16x32_bf16 v[30:33], v[156:159], v[200:203], v[30:33]
	v_mfma_f32_16x16x32_bf16 v[22:25], v[148:151], v[216:219], v[22:25]
	v_mfma_f32_16x16x32_bf16 v[14:17], v[156:159], v[216:219], v[14:17]
	v_mfma_f32_16x16x32_bf16 v[62:65], v[152:155], v[188:191], v[62:65]
	v_mfma_f32_16x16x32_bf16 v[58:61], v[160:163], v[188:191], v[58:61]
	v_mfma_f32_16x16x32_bf16 v[54:57], v[152:155], v[196:199], v[54:57]
	v_mfma_f32_16x16x32_bf16 v[46:49], v[160:163], v[196:199], v[46:49]
	v_mfma_f32_16x16x32_bf16 v[38:41], v[152:155], v[204:207], v[38:41]
	v_mfma_f32_16x16x32_bf16 v[30:33], v[160:163], v[204:207], v[30:33]
	v_mfma_f32_16x16x32_bf16 v[22:25], v[152:155], v[220:223], v[22:25]
	v_mfma_f32_16x16x32_bf16 v[14:17], v[160:163], v[220:223], v[14:17]
	v_mfma_f32_16x16x32_bf16 v[50:53], v[164:167], v[184:187], v[50:53]
	v_mfma_f32_16x16x32_bf16 v[42:45], v[172:175], v[184:187], v[42:45]
	v_mfma_f32_16x16x32_bf16 v[34:37], v[164:167], v[192:195], v[34:37]
	v_mfma_f32_16x16x32_bf16 v[26:29], v[172:175], v[192:195], v[26:29]
	v_mfma_f32_16x16x32_bf16 v[18:21], v[164:167], v[200:203], v[18:21]
	v_mfma_f32_16x16x32_bf16 v[10:13], v[172:175], v[200:203], v[10:13]
	v_mfma_f32_16x16x32_bf16 v[6:9], v[164:167], v[216:219], v[6:9]
	v_mfma_f32_16x16x32_bf16 v[2:5], v[172:175], v[216:219], v[2:5]
	v_mfma_f32_16x16x32_bf16 v[50:53], v[168:171], v[188:191], v[50:53]
	v_mfma_f32_16x16x32_bf16 v[42:45], v[180:183], v[188:191], v[42:45]
	v_mfma_f32_16x16x32_bf16 v[34:37], v[168:171], v[196:199], v[34:37]
	v_mfma_f32_16x16x32_bf16 v[26:29], v[180:183], v[196:199], v[26:29]
	v_mfma_f32_16x16x32_bf16 v[18:21], v[168:171], v[204:207], v[18:21]
	v_mfma_f32_16x16x32_bf16 v[10:13], v[180:183], v[204:207], v[10:13]
	v_mfma_f32_16x16x32_bf16 v[6:9], v[168:171], v[220:223], v[6:9]
	v_mfma_f32_16x16x32_bf16 v[2:5], v[180:183], v[220:223], v[2:5]
	s_barrier
	s_add_i32 s47, s47, 2
	s_add_u32 s45, s45, 0x100
	s_addc_u32 s46, s46, 0
	s_add_u32 s24, s24, 0x100
	s_addc_u32 s25, s25, 0
	s_cmp_gt_u32 s47, 13
	s_cbranch_scc0 .LBB0_1799
	s_and_b64 vcc, exec, s[12:13]
	s_cbranch_vccz .LBB0_1802
	s_barrier

.LBB0_2367:
	s_add_u32 s10, s34, s38
	s_addc_u32 s11, s35, 0
	s_add_u32 s39, s10, 0x100
	s_addc_u32 s76, s11, 0
	s_and_b64 s[70:71], s[62:63], exec
	s_cselect_b32 s77, s45, s76
	s_cselect_b32 s76, s59, s39
	s_add_u32 s38, s30, s38
	s_addc_u32 s39, s31, 0
	s_add_u32 s70, s38, 0x100
	s_addc_u32 s71, s39, 0
	s_add_i32 s91, 0, 0x10000
	s_and_b64 s[38:39], s[62:63], exec
	s_cselect_b32 s79, s37, s71
	s_cselect_b32 s78, s82, s70
	s_add_i32 s38, 0, 0x14000
	s_add_u32 s10, s10, 0x10080
	s_addc_u32 s11, s11, 0
	s_add_i32 s8, s91, s95
	s_add_i32 m0, s65, 0xc000
	s_add_i32 s14, s65, 0xe000
	s_add_i32 s9, s8, 0x2000
	s_add_u32 s80, s78, 0x10000
	s_addc_u32 s81, s79, 0
	s_add_i32 s50, s38, s95
	v_add_u32_e32 v152, s91, v138
	v_add_u32_e32 v164, s38, v138
	s_add_i32 s74, s50, 0x2000
	s_add_i32 vcc_hi, 0, 0x18000
	s_add_i32 s39, 0, 0x1c000
	ds_read_b128 v[140:143], v152
	ds_read_b128 v[144:147], v152 offset:1024
	ds_read_b128 v[148:151], v152 offset:2048
	ds_read_b128 v[152:155], v152 offset:3072
	ds_read_b128 v[156:159], v164
	ds_read_b128 v[160:163], v164 offset:1024
	ds_read_b128 v[168:171], v164 offset:2048
	ds_read_b128 v[172:175], v164 offset:3072
	s_add_u32 s70, s76, 0x10000
	s_addc_u32 s71, s77, 0
	s_add_i32 vcc_lo, vcc_hi, s95
	s_add_i32 s64, vcc_lo, 0x2000
	s_add_u32 s62, s78, 0x10080
	s_addc_u32 s63, s79, 0
	s_add_i32 s91, s39, s95
	s_add_i32 s38, s91, 0x2000
	ds_read_b128 v[176:179], v139
	ds_read_b128 v[180:183], v139 offset:1024
	ds_read_b128 v[184:187], v139 offset:2048
	ds_read_b128 v[188:191], v139 offset:3072
	ds_read_b128 v[192:195], v139 offset:4096
	ds_read_b128 v[196:199], v139 offset:5120
	ds_read_b128 v[200:203], v139 offset:6144
	global_load_lds_dwordx4 v128, s[10:11]
	s_mov_b32 m0, s14
	ds_read_b128 v[204:207], v139 offset:7168
	global_load_lds_dwordx4 v124, s[10:11]
	s_waitcnt vmcnt(8)
	s_waitcnt lgkmcnt(0)
	s_barrier
	s_waitcnt lgkmcnt(0)
	v_mfma_f32_16x16x32_bf16 v[134:137], v[140:143], v[176:179], v[134:137]
	v_mfma_f32_16x16x32_bf16 v[130:133], v[148:151], v[176:179], v[130:133]
	v_mfma_f32_16x16x32_bf16 v[110:113], v[140:143], v[184:187], v[110:113]
	v_mfma_f32_16x16x32_bf16 v[106:109], v[148:151], v[184:187], v[106:109]
	v_mfma_f32_16x16x32_bf16 v[94:97], v[140:143], v[192:195], v[94:97]
	v_mfma_f32_16x16x32_bf16 v[90:93], v[148:151], v[192:195], v[90:93]
	v_mfma_f32_16x16x32_bf16 v[78:81], v[140:143], v[200:203], v[78:81]
	v_mfma_f32_16x16x32_bf16 v[74:77], v[148:151], v[200:203], v[74:77]
	v_mfma_f32_16x16x32_bf16 v[134:137], v[144:147], v[180:183], v[134:137]
	v_mfma_f32_16x16x32_bf16 v[130:133], v[152:155], v[180:183], v[130:133]
	v_mfma_f32_16x16x32_bf16 v[110:113], v[144:147], v[188:191], v[110:113]
	v_mfma_f32_16x16x32_bf16 v[106:109], v[152:155], v[188:191], v[106:109]
	v_mfma_f32_16x16x32_bf16 v[94:97], v[144:147], v[196:199], v[94:97]
	v_mfma_f32_16x16x32_bf16 v[90:93], v[152:155], v[196:199], v[90:93]
	v_mfma_f32_16x16x32_bf16 v[78:81], v[144:147], v[204:207], v[78:81]
	v_mfma_f32_16x16x32_bf16 v[74:77], v[152:155], v[204:207], v[74:77]
	v_mfma_f32_16x16x32_bf16 v[118:121], v[156:159], v[176:179], v[118:121]
	v_mfma_f32_16x16x32_bf16 v[114:117], v[168:171], v[176:179], v[114:117]
	v_mfma_f32_16x16x32_bf16 v[102:105], v[156:159], v[184:187], v[102:105]
	v_mfma_f32_16x16x32_bf16 v[98:101], v[168:171], v[184:187], v[98:101]
	v_mfma_f32_16x16x32_bf16 v[86:89], v[156:159], v[192:195], v[86:89]
	v_mfma_f32_16x16x32_bf16 v[82:85], v[168:171], v[192:195], v[82:85]
	v_mfma_f32_16x16x32_bf16 v[70:73], v[156:159], v[200:203], v[70:73]
	v_mfma_f32_16x16x32_bf16 v[66:69], v[168:171], v[200:203], v[66:69]
	v_mfma_f32_16x16x32_bf16 v[118:121], v[160:163], v[180:183], v[118:121]
	v_mfma_f32_16x16x32_bf16 v[114:117], v[172:175], v[180:183], v[114:117]
	v_mfma_f32_16x16x32_bf16 v[102:105], v[160:163], v[188:191], v[102:105]
	v_mfma_f32_16x16x32_bf16 v[98:101], v[172:175], v[188:191], v[98:101]
	v_mfma_f32_16x16x32_bf16 v[86:89], v[160:163], v[196:199], v[86:89]
	v_mfma_f32_16x16x32_bf16 v[82:85], v[172:175], v[196:199], v[82:85]
	v_mfma_f32_16x16x32_bf16 v[70:73], v[160:163], v[204:207], v[70:73]
	v_mfma_f32_16x16x32_bf16 v[66:69], v[172:175], v[204:207], v[66:69]
	s_barrier
	s_mov_b32 m0, s8
	v_lshl_add_u64 v[164:165], s[78:79], 0, v[126:127]
	ds_read_b128 v[176:179], v139 offset:16384
	ds_read_b128 v[180:183], v139 offset:17408
	ds_read_b128 v[184:187], v139 offset:18432
	ds_read_b128 v[188:191], v139 offset:19456
	ds_read_b128 v[192:195], v139 offset:20480
	ds_read_b128 v[196:199], v139 offset:21504
	ds_read_b128 v[200:203], v139 offset:22528
	ds_read_b128 v[204:207], v139 offset:23552
	global_load_lds_dwordx4 v126, s[78:79]
	v_lshl_add_u64 v[208:209], s[78:79], 0, v[122:123]
	s_mov_b32 m0, s9
	s_nop 0
	global_load_lds_dwordx4 v122, s[78:79]
	s_mov_b32 m0, s50
	v_lshl_add_u64 v[218:219], s[76:77], 0, v[124:125]
	global_load_lds_dwordx4 v126, s[80:81]
	s_mov_b32 m0, s74
	s_nop 0
	global_load_lds_dwordx4 v122, s[80:81]
	s_mov_b32 m0, s65
	v_lshl_add_u64 v[216:217], s[76:77], 0, v[128:129]
	global_load_lds_dwordx4 v128, s[76:77]
	s_mov_b32 m0, s15
	s_nop 0
	global_load_lds_dwordx4 v124, s[76:77]
	s_waitcnt vmcnt(8)
	s_waitcnt lgkmcnt(0)
	s_barrier
	s_waitcnt lgkmcnt(0)
	v_mfma_f32_16x16x32_bf16 v[62:65], v[140:143], v[176:179], v[62:65]
	v_mfma_f32_16x16x32_bf16 v[58:61], v[148:151], v[176:179], v[58:61]
	v_mfma_f32_16x16x32_bf16 v[46:49], v[140:143], v[184:187], v[46:49]
	v_mfma_f32_16x16x32_bf16 v[42:45], v[148:151], v[184:187], v[42:45]
	v_mfma_f32_16x16x32_bf16 v[30:33], v[140:143], v[192:195], v[30:33]
	v_mfma_f32_16x16x32_bf16 v[26:29], v[148:151], v[192:195], v[26:29]
	v_mfma_f32_16x16x32_bf16 v[14:17], v[140:143], v[200:203], v[14:17]
	v_mfma_f32_16x16x32_bf16 v[10:13], v[148:151], v[200:203], v[10:13]
	v_mfma_f32_16x16x32_bf16 v[62:65], v[144:147], v[180:183], v[62:65]
	v_mfma_f32_16x16x32_bf16 v[58:61], v[152:155], v[180:183], v[58:61]
	v_mfma_f32_16x16x32_bf16 v[46:49], v[144:147], v[188:191], v[46:49]
	v_mfma_f32_16x16x32_bf16 v[42:45], v[152:155], v[188:191], v[42:45]
	v_mfma_f32_16x16x32_bf16 v[30:33], v[144:147], v[196:199], v[30:33]
	v_mfma_f32_16x16x32_bf16 v[26:29], v[152:155], v[196:199], v[26:29]
	v_mfma_f32_16x16x32_bf16 v[14:17], v[144:147], v[204:207], v[14:17]
	v_mfma_f32_16x16x32_bf16 v[10:13], v[152:155], v[204:207], v[10:13]
	v_mfma_f32_16x16x32_bf16 v[54:57], v[156:159], v[176:179], v[54:57]
	v_mfma_f32_16x16x32_bf16 v[50:53], v[168:171], v[176:179], v[50:53]
	v_mfma_f32_16x16x32_bf16 v[38:41], v[156:159], v[184:187], v[38:41]
	v_mfma_f32_16x16x32_bf16 v[34:37], v[168:171], v[184:187], v[34:37]
	v_mfma_f32_16x16x32_bf16 v[22:25], v[156:159], v[192:195], v[22:25]
	v_mfma_f32_16x16x32_bf16 v[18:21], v[168:171], v[192:195], v[18:21]
	v_mfma_f32_16x16x32_bf16 v[6:9], v[156:159], v[200:203], v[6:9]
	v_mfma_f32_16x16x32_bf16 v[2:5], v[168:171], v[200:203], v[2:5]
	v_mfma_f32_16x16x32_bf16 v[54:57], v[160:163], v[180:183], v[54:57]
	v_mfma_f32_16x16x32_bf16 v[50:53], v[172:175], v[180:183], v[50:53]
	v_mfma_f32_16x16x32_bf16 v[38:41], v[160:163], v[188:191], v[38:41]
	v_mfma_f32_16x16x32_bf16 v[34:37], v[172:175], v[188:191], v[34:37]
	v_mfma_f32_16x16x32_bf16 v[22:25], v[160:163], v[196:199], v[22:25]
	v_mfma_f32_16x16x32_bf16 v[18:21], v[172:175], v[196:199], v[18:21]
	v_mfma_f32_16x16x32_bf16 v[6:9], v[160:163], v[204:207], v[6:9]
	v_mfma_f32_16x16x32_bf16 v[2:5], v[172:175], v[204:207], v[2:5]
	s_barrier
	v_add_u32_e32 v152, vcc_hi, v138
	v_add_u32_e32 v167, s39, v138
	ds_read_b128 v[140:143], v152
	ds_read_b128 v[144:147], v152 offset:1024
	ds_read_b128 v[148:151], v152 offset:2048
	ds_read_b128 v[152:155], v152 offset:3072
	ds_read_b128 v[156:159], v167
	ds_read_b128 v[160:163], v167 offset:1024
	ds_read_b128 v[168:171], v167 offset:2048
	ds_read_b128 v[172:175], v167 offset:3072
	s_mov_b32 m0, s84
	ds_read_b128 v[176:179], v139 offset:32768
	ds_read_b128 v[180:183], v139 offset:33792
	ds_read_b128 v[184:187], v139 offset:34816
	ds_read_b128 v[188:191], v139 offset:35840
	ds_read_b128 v[192:195], v139 offset:36864
	ds_read_b128 v[196:199], v139 offset:37888
	ds_read_b128 v[200:203], v139 offset:38912
	ds_read_b128 v[204:207], v139 offset:39936
	global_load_lds_dwordx4 v128, s[70:71]
	s_mov_b32 m0, s90
	v_lshl_add_u64 v[220:221], s[70:71], 0, v[124:125]
	global_load_lds_dwordx4 v124, s[70:71]
	s_waitcnt vmcnt(8)
	s_waitcnt lgkmcnt(0)
	s_barrier
	s_waitcnt lgkmcnt(0)
	v_mfma_f32_16x16x32_bf16 v[134:137], v[140:143], v[176:179], v[134:137]
	v_mfma_f32_16x16x32_bf16 v[130:133], v[148:151], v[176:179], v[130:133]
	v_mfma_f32_16x16x32_bf16 v[110:113], v[140:143], v[184:187], v[110:113]
	v_mfma_f32_16x16x32_bf16 v[106:109], v[148:151], v[184:187], v[106:109]
	v_mfma_f32_16x16x32_bf16 v[94:97], v[140:143], v[192:195], v[94:97]
	v_mfma_f32_16x16x32_bf16 v[90:93], v[148:151], v[192:195], v[90:93]
	v_mfma_f32_16x16x32_bf16 v[78:81], v[140:143], v[200:203], v[78:81]
	v_mfma_f32_16x16x32_bf16 v[74:77], v[148:151], v[200:203], v[74:77]
	v_mfma_f32_16x16x32_bf16 v[134:137], v[144:147], v[180:183], v[134:137]
	v_mfma_f32_16x16x32_bf16 v[130:133], v[152:155], v[180:183], v[130:133]
	v_mfma_f32_16x16x32_bf16 v[110:113], v[144:147], v[188:191], v[110:113]
	v_mfma_f32_16x16x32_bf16 v[106:109], v[152:155], v[188:191], v[106:109]
	v_mfma_f32_16x16x32_bf16 v[94:97], v[144:147], v[196:199], v[94:97]
	v_mfma_f32_16x16x32_bf16 v[90:93], v[152:155], v[196:199], v[90:93]
	v_mfma_f32_16x16x32_bf16 v[78:81], v[144:147], v[204:207], v[78:81]
	v_mfma_f32_16x16x32_bf16 v[74:77], v[152:155], v[204:207], v[74:77]
	v_mfma_f32_16x16x32_bf16 v[118:121], v[156:159], v[176:179], v[118:121]
	v_mfma_f32_16x16x32_bf16 v[114:117], v[168:171], v[176:179], v[114:117]
	v_mfma_f32_16x16x32_bf16 v[102:105], v[156:159], v[184:187], v[102:105]
	v_mfma_f32_16x16x32_bf16 v[98:101], v[168:171], v[184:187], v[98:101]
	v_mfma_f32_16x16x32_bf16 v[86:89], v[156:159], v[192:195], v[86:89]
	v_mfma_f32_16x16x32_bf16 v[82:85], v[168:171], v[192:195], v[82:85]
	v_mfma_f32_16x16x32_bf16 v[70:73], v[156:159], v[200:203], v[70:73]
	v_mfma_f32_16x16x32_bf16 v[66:69], v[168:171], v[200:203], v[66:69]
	v_mfma_f32_16x16x32_bf16 v[118:121], v[160:163], v[180:183], v[118:121]
	v_mfma_f32_16x16x32_bf16 v[114:117], v[172:175], v[180:183], v[114:117]
	v_mfma_f32_16x16x32_bf16 v[102:105], v[160:163], v[188:191], v[102:105]
	v_mfma_f32_16x16x32_bf16 v[98:101], v[172:175], v[188:191], v[98:101]
	v_mfma_f32_16x16x32_bf16 v[86:89], v[160:163], v[196:199], v[86:89]
	v_mfma_f32_16x16x32_bf16 v[82:85], v[172:175], v[196:199], v[82:85]
	v_mfma_f32_16x16x32_bf16 v[70:73], v[160:163], v[204:207], v[70:73]
	v_mfma_f32_16x16x32_bf16 v[66:69], v[172:175], v[204:207], v[66:69]
	s_barrier
	s_mov_b32 m0, vcc_lo
	v_lshl_add_u64 v[164:165], v[164:165], 0, s[56:57]
	ds_read_b128 v[176:179], v139 offset:49152
	ds_read_b128 v[180:183], v139 offset:50176
	ds_read_b128 v[184:187], v139 offset:51200
	ds_read_b128 v[188:191], v139 offset:52224
	ds_read_b128 v[192:195], v139 offset:53248
	ds_read_b128 v[196:199], v139 offset:54272
	ds_read_b128 v[200:203], v139 offset:55296
	ds_read_b128 v[204:207], v139 offset:56320
	global_load_lds_dwordx4 v[164:165], off
	s_mov_b32 m0, s64
	v_lshl_add_u64 v[164:165], v[208:209], 0, s[56:57]
	global_load_lds_dwordx4 v[164:165], off
	s_mov_b32 m0, s91
	s_nop 0
	global_load_lds_dwordx4 v126, s[62:63]
	s_mov_b32 m0, s38
	s_nop 0
	global_load_lds_dwordx4 v122, s[62:63]
	s_mov_b32 m0, s68
	v_lshl_add_u64 v[164:165], v[216:217], 0, s[56:57]
	global_load_lds_dwordx4 v[164:165], off
	s_mov_b32 m0, s22
	v_lshl_add_u64 v[164:165], v[218:219], 0, s[56:57]
	global_load_lds_dwordx4 v[164:165], off
	s_waitcnt vmcnt(8)
	s_waitcnt lgkmcnt(0)
	s_barrier
	s_waitcnt lgkmcnt(0)
	v_mfma_f32_16x16x32_bf16 v[62:65], v[140:143], v[176:179], v[62:65]
	v_mfma_f32_16x16x32_bf16 v[58:61], v[148:151], v[176:179], v[58:61]
	v_mfma_f32_16x16x32_bf16 v[46:49], v[140:143], v[184:187], v[46:49]
	v_mfma_f32_16x16x32_bf16 v[42:45], v[148:151], v[184:187], v[42:45]
	v_mfma_f32_16x16x32_bf16 v[30:33], v[140:143], v[192:195], v[30:33]
	v_mfma_f32_16x16x32_bf16 v[26:29], v[148:151], v[192:195], v[26:29]
	v_mfma_f32_16x16x32_bf16 v[14:17], v[140:143], v[200:203], v[14:17]
	v_mfma_f32_16x16x32_bf16 v[10:13], v[148:151], v[200:203], v[10:13]
	v_mfma_f32_16x16x32_bf16 v[62:65], v[144:147], v[180:183], v[62:65]
	v_mfma_f32_16x16x32_bf16 v[58:61], v[152:155], v[180:183], v[58:61]
	v_mfma_f32_16x16x32_bf16 v[46:49], v[144:147], v[188:191], v[46:49]
	v_mfma_f32_16x16x32_bf16 v[42:45], v[152:155], v[188:191], v[42:45]
	v_mfma_f32_16x16x32_bf16 v[30:33], v[144:147], v[196:199], v[30:33]
	v_mfma_f32_16x16x32_bf16 v[26:29], v[152:155], v[196:199], v[26:29]
	v_mfma_f32_16x16x32_bf16 v[14:17], v[144:147], v[204:207], v[14:17]
	v_mfma_f32_16x16x32_bf16 v[10:13], v[152:155], v[204:207], v[10:13]
	v_mfma_f32_16x16x32_bf16 v[54:57], v[156:159], v[176:179], v[54:57]
	v_mfma_f32_16x16x32_bf16 v[50:53], v[168:171], v[176:179], v[50:53]
	v_mfma_f32_16x16x32_bf16 v[38:41], v[156:159], v[184:187], v[38:41]
	v_mfma_f32_16x16x32_bf16 v[34:37], v[168:171], v[184:187], v[34:37]
	v_mfma_f32_16x16x32_bf16 v[22:25], v[156:159], v[192:195], v[22:25]
	v_mfma_f32_16x16x32_bf16 v[18:21], v[168:171], v[192:195], v[18:21]
	v_mfma_f32_16x16x32_bf16 v[6:9], v[156:159], v[200:203], v[6:9]
	v_mfma_f32_16x16x32_bf16 v[2:5], v[168:171], v[200:203], v[2:5]
	v_mfma_f32_16x16x32_bf16 v[54:57], v[160:163], v[180:183], v[54:57]
	v_mfma_f32_16x16x32_bf16 v[50:53], v[172:175], v[180:183], v[50:53]
	v_mfma_f32_16x16x32_bf16 v[38:41], v[160:163], v[188:191], v[38:41]
	v_mfma_f32_16x16x32_bf16 v[34:37], v[172:175], v[188:191], v[34:37]
	v_mfma_f32_16x16x32_bf16 v[22:25], v[160:163], v[196:199], v[22:25]
	v_mfma_f32_16x16x32_bf16 v[18:21], v[172:175], v[196:199], v[18:21]
	v_mfma_f32_16x16x32_bf16 v[6:9], v[160:163], v[204:207], v[6:9]
	v_mfma_f32_16x16x32_bf16 v[2:5], v[172:175], v[204:207], v[2:5]
	s_barrier
	s_movk_i32 s38, 0x100
	s_andn2_b64 vcc, exec, s[52:53]
	s_mov_b64 s[62:63], -1
	s_mov_b64 s[52:53], 0
	s_cbranch_vccz .LBB0_2367
	s_andn2_b64 vcc, exec, s[42:43]
	s_cbranch_vccnz .LBB0_2359
	v_mov_b32_e32 v2, 0
	s_mov_b32 s16, s36
	s_mov_b32 s94, s44
	s_mov_b64 s[30:31], s[48:49]
	s_mov_b64 s[34:35], s[46:47]
	s_mov_b32 s58, s23
	v_mov_b32_e32 v3, v2
	v_mov_b32_e32 v4, v2
	v_mov_b32_e32 v5, v2
	v_mov_b32_e32 v6, v2
	v_mov_b32_e32 v7, v2
	v_mov_b32_e32 v8, v2
	v_mov_b32_e32 v9, v2
	v_mov_b32_e32 v18, v2
	v_mov_b32_e32 v19, v2
	v_mov_b32_e32 v20, v2
	v_mov_b32_e32 v21, v2
	v_mov_b32_e32 v22, v2
	v_mov_b32_e32 v23, v2
	v_mov_b32_e32 v24, v2
	v_mov_b32_e32 v25, v2
	v_mov_b32_e32 v34, v2
	v_mov_b32_e32 v35, v2
	v_mov_b32_e32 v36, v2
	v_mov_b32_e32 v37, v2
	v_mov_b32_e32 v38, v2
	v_mov_b32_e32 v39, v2
	v_mov_b32_e32 v40, v2
	v_mov_b32_e32 v41, v2
	v_mov_b32_e32 v50, v2
	v_mov_b32_e32 v51, v2
	v_mov_b32_e32 v52, v2
	v_mov_b32_e32 v53, v2
	v_mov_b32_e32 v54, v2
	v_mov_b32_e32 v55, v2
	v_mov_b32_e32 v56, v2
	v_mov_b32_e32 v57, v2
	v_mov_b32_e32 v10, v2
	v_mov_b32_e32 v11, v2
	v_mov_b32_e32 v12, v2
	v_mov_b32_e32 v13, v2
	v_mov_b32_e32 v14, v2
	v_mov_b32_e32 v15, v2
	v_mov_b32_e32 v16, v2
	v_mov_b32_e32 v17, v2
	v_mov_b32_e32 v26, v2
	v_mov_b32_e32 v27, v2
	v_mov_b32_e32 v28, v2
	v_mov_b32_e32 v29, v2
	v_mov_b32_e32 v30, v2
	v_mov_b32_e32 v31, v2
	v_mov_b32_e32 v32, v2
	v_mov_b32_e32 v33, v2
	v_mov_b32_e32 v42, v2
	v_mov_b32_e32 v43, v2
	v_mov_b32_e32 v44, v2
	v_mov_b32_e32 v45, v2
	v_mov_b32_e32 v46, v2
	v_mov_b32_e32 v47, v2
	v_mov_b32_e32 v48, v2
	v_mov_b32_e32 v49, v2
	v_mov_b32_e32 v58, v2
	v_mov_b32_e32 v59, v2
	v_mov_b32_e32 v60, v2
	v_mov_b32_e32 v61, v2
	v_mov_b32_e32 v62, v2
	v_mov_b32_e32 v63, v2
	v_mov_b32_e32 v64, v2
	v_mov_b32_e32 v65, v2
	v_mov_b32_e32 v66, v2
	v_mov_b32_e32 v67, v2
	v_mov_b32_e32 v68, v2
	v_mov_b32_e32 v69, v2
	v_mov_b32_e32 v70, v2
	v_mov_b32_e32 v71, v2
	v_mov_b32_e32 v72, v2
	v_mov_b32_e32 v73, v2
	v_mov_b32_e32 v82, v2
	v_mov_b32_e32 v83, v2
	v_mov_b32_e32 v84, v2
	v_mov_b32_e32 v85, v2
	v_mov_b32_e32 v86, v2
	v_mov_b32_e32 v87, v2
	v_mov_b32_e32 v88, v2
	v_mov_b32_e32 v89, v2
	v_mov_b32_e32 v98, v2
	v_mov_b32_e32 v99, v2
	v_mov_b32_e32 v100, v2
	v_mov_b32_e32 v101, v2
	v_mov_b32_e32 v102, v2
	v_mov_b32_e32 v103, v2
	v_mov_b32_e32 v104, v2
	v_mov_b32_e32 v105, v2
	v_mov_b32_e32 v114, v2
	v_mov_b32_e32 v115, v2
	v_mov_b32_e32 v116, v2
	v_mov_b32_e32 v117, v2
	v_mov_b32_e32 v118, v2
	v_mov_b32_e32 v119, v2
	v_mov_b32_e32 v120, v2
	v_mov_b32_e32 v121, v2
	v_mov_b32_e32 v74, v2
	v_mov_b32_e32 v75, v2
	v_mov_b32_e32 v76, v2
	v_mov_b32_e32 v77, v2
	v_mov_b32_e32 v78, v2
	v_mov_b32_e32 v79, v2
	v_mov_b32_e32 v80, v2
	v_mov_b32_e32 v81, v2
	v_mov_b32_e32 v90, v2
	v_mov_b32_e32 v91, v2
	v_mov_b32_e32 v92, v2
	v_mov_b32_e32 v93, v2
	v_mov_b32_e32 v94, v2
	v_mov_b32_e32 v95, v2
	v_mov_b32_e32 v96, v2
	v_mov_b32_e32 v97, v2
	v_mov_b32_e32 v106, v2
	v_mov_b32_e32 v107, v2
	v_mov_b32_e32 v108, v2
	v_mov_b32_e32 v109, v2
	v_mov_b32_e32 v110, v2
	v_mov_b32_e32 v111, v2
	v_mov_b32_e32 v112, v2
	v_mov_b32_e32 v113, v2
	v_mov_b32_e32 v130, v2
	v_mov_b32_e32 v131, v2
	v_mov_b32_e32 v132, v2
	v_mov_b32_e32 v133, v2
	v_mov_b32_e32 v134, v2
	v_mov_b32_e32 v135, v2
	v_mov_b32_e32 v136, v2
	v_mov_b32_e32 v137, v2
	s_branch .LBB0_2359

.LBB0_2467:
	s_add_u32 s8, s30, s12
	s_addc_u32 s9, s31, 0
	s_add_u32 s13, s8, 0x100
	s_addc_u32 s50, s9, 0
	s_and_b64 s[10:11], s[48:49], exec
	s_cselect_b32 s63, s37, s50
	s_cselect_b32 s62, s59, s13
	s_add_u32 s10, s28, s12
	s_addc_u32 s11, s29, 0
	s_add_u32 s12, s10, 0x100
	s_addc_u32 s13, s11, 0
	s_add_i32 s50, 0, 0x10000
	s_and_b64 s[10:11], s[48:49], exec
	s_cselect_b32 s71, s35, s13
	s_cselect_b32 s70, s96, s12
	s_add_i32 s12, 0, 0x14000
	s_add_u32 s10, s8, 0x10080
	s_addc_u32 s11, s9, 0
	s_add_i32 s9, s50, s81
	s_add_i32 m0, s82, 0xc000
	s_add_i32 s8, s82, 0xe000
	s_add_i32 s64, s9, 0x2000
	s_add_u32 s76, s70, 0x10000
	s_addc_u32 s77, s71, 0
	s_add_i32 s65, s12, s81
	v_add_u32_e32 v152, s50, v138
	v_add_u32_e32 v168, s12, v138
	s_add_i32 s74, s65, 0x2000
	s_add_i32 s91, 0, 0x18000
	s_add_i32 s13, 0, 0x1c000
	ds_read_b128 v[140:143], v152
	ds_read_b128 v[144:147], v152 offset:1024
	ds_read_b128 v[148:151], v152 offset:2048
	ds_read_b128 v[152:155], v152 offset:3072
	ds_read_b128 v[156:159], v168
	ds_read_b128 v[160:163], v168 offset:1024
	ds_read_b128 v[164:167], v168 offset:2048
	ds_read_b128 v[168:171], v168 offset:3072
	s_add_u32 s52, s62, 0x10000
	s_addc_u32 s53, s63, 0
	s_add_i32 vcc_hi, s91, s81
	s_add_i32 vcc_lo, vcc_hi, 0x2000
	s_add_u32 s48, s70, 0x10080
	s_addc_u32 s49, s71, 0
	s_add_i32 s50, s13, s81
	s_add_i32 s12, s50, 0x2000
	ds_read_b128 v[172:175], v139
	ds_read_b128 v[176:179], v139 offset:1024
	ds_read_b128 v[180:183], v139 offset:2048
	ds_read_b128 v[184:187], v139 offset:3072
	ds_read_b128 v[188:191], v139 offset:4096
	ds_read_b128 v[192:195], v139 offset:5120
	ds_read_b128 v[196:199], v139 offset:6144
	global_load_lds_dwordx4 v128, s[10:11]
	s_mov_b32 m0, s8
	ds_read_b128 v[200:203], v139 offset:7168
	global_load_lds_dwordx4 v124, s[10:11]
	s_waitcnt vmcnt(8)
	s_waitcnt lgkmcnt(0)
	s_barrier
	s_waitcnt lgkmcnt(0)
	v_mfma_f32_16x16x32_bf16 v[134:137], v[140:143], v[172:175], v[134:137]
	v_mfma_f32_16x16x32_bf16 v[130:133], v[148:151], v[172:175], v[130:133]
	v_mfma_f32_16x16x32_bf16 v[110:113], v[140:143], v[180:183], v[110:113]
	v_mfma_f32_16x16x32_bf16 v[106:109], v[148:151], v[180:183], v[106:109]
	v_mfma_f32_16x16x32_bf16 v[94:97], v[140:143], v[188:191], v[94:97]
	v_mfma_f32_16x16x32_bf16 v[90:93], v[148:151], v[188:191], v[90:93]
	v_mfma_f32_16x16x32_bf16 v[78:81], v[140:143], v[196:199], v[78:81]
	v_mfma_f32_16x16x32_bf16 v[74:77], v[148:151], v[196:199], v[74:77]
	v_mfma_f32_16x16x32_bf16 v[134:137], v[144:147], v[176:179], v[134:137]
	v_mfma_f32_16x16x32_bf16 v[130:133], v[152:155], v[176:179], v[130:133]
	v_mfma_f32_16x16x32_bf16 v[110:113], v[144:147], v[184:187], v[110:113]
	v_mfma_f32_16x16x32_bf16 v[106:109], v[152:155], v[184:187], v[106:109]
	v_mfma_f32_16x16x32_bf16 v[94:97], v[144:147], v[192:195], v[94:97]
	v_mfma_f32_16x16x32_bf16 v[90:93], v[152:155], v[192:195], v[90:93]
	v_mfma_f32_16x16x32_bf16 v[78:81], v[144:147], v[200:203], v[78:81]
	v_mfma_f32_16x16x32_bf16 v[74:77], v[152:155], v[200:203], v[74:77]
	v_mfma_f32_16x16x32_bf16 v[118:121], v[156:159], v[172:175], v[118:121]
	v_mfma_f32_16x16x32_bf16 v[114:117], v[164:167], v[172:175], v[114:117]
	v_mfma_f32_16x16x32_bf16 v[102:105], v[156:159], v[180:183], v[102:105]
	v_mfma_f32_16x16x32_bf16 v[98:101], v[164:167], v[180:183], v[98:101]
	v_mfma_f32_16x16x32_bf16 v[86:89], v[156:159], v[188:191], v[86:89]
	v_mfma_f32_16x16x32_bf16 v[82:85], v[164:167], v[188:191], v[82:85]
	v_mfma_f32_16x16x32_bf16 v[70:73], v[156:159], v[196:199], v[70:73]
	v_mfma_f32_16x16x32_bf16 v[66:69], v[164:167], v[196:199], v[66:69]
	v_mfma_f32_16x16x32_bf16 v[118:121], v[160:163], v[176:179], v[118:121]
	v_mfma_f32_16x16x32_bf16 v[114:117], v[168:171], v[176:179], v[114:117]
	v_mfma_f32_16x16x32_bf16 v[102:105], v[160:163], v[184:187], v[102:105]
	v_mfma_f32_16x16x32_bf16 v[98:101], v[168:171], v[184:187], v[98:101]
	v_mfma_f32_16x16x32_bf16 v[86:89], v[160:163], v[192:195], v[86:89]
	v_mfma_f32_16x16x32_bf16 v[82:85], v[168:171], v[192:195], v[82:85]
	v_mfma_f32_16x16x32_bf16 v[70:73], v[160:163], v[200:203], v[70:73]
	v_mfma_f32_16x16x32_bf16 v[66:69], v[168:171], v[200:203], v[66:69]
	s_barrier
	s_mov_b32 m0, s9
	v_lshl_add_u64 v[204:205], s[70:71], 0, v[126:127]
	ds_read_b128 v[172:175], v139 offset:16384
	ds_read_b128 v[176:179], v139 offset:17408
	ds_read_b128 v[180:183], v139 offset:18432
	ds_read_b128 v[184:187], v139 offset:19456
	ds_read_b128 v[188:191], v139 offset:20480
	ds_read_b128 v[192:195], v139 offset:21504
	ds_read_b128 v[196:199], v139 offset:22528
	ds_read_b128 v[200:203], v139 offset:23552
	global_load_lds_dwordx4 v126, s[70:71]
	v_lshl_add_u64 v[206:207], s[70:71], 0, v[122:123]
	s_mov_b32 m0, s64
	s_nop 0
	global_load_lds_dwordx4 v122, s[70:71]
	s_mov_b32 m0, s65
	v_lshl_add_u64 v[216:217], s[62:63], 0, v[124:125]
	global_load_lds_dwordx4 v126, s[76:77]
	s_mov_b32 m0, s74
	s_nop 0
	global_load_lds_dwordx4 v122, s[76:77]
	s_mov_b32 m0, s82
	v_lshl_add_u64 v[208:209], s[62:63], 0, v[128:129]
	global_load_lds_dwordx4 v128, s[62:63]
	s_mov_b32 m0, s92
	s_nop 0
	global_load_lds_dwordx4 v124, s[62:63]
	s_waitcnt vmcnt(8)
	s_waitcnt lgkmcnt(0)
	s_barrier
	s_waitcnt lgkmcnt(0)
	v_mfma_f32_16x16x32_bf16 v[62:65], v[140:143], v[172:175], v[62:65]
	v_mfma_f32_16x16x32_bf16 v[58:61], v[148:151], v[172:175], v[58:61]
	v_mfma_f32_16x16x32_bf16 v[46:49], v[140:143], v[180:183], v[46:49]
	v_mfma_f32_16x16x32_bf16 v[42:45], v[148:151], v[180:183], v[42:45]
	v_mfma_f32_16x16x32_bf16 v[30:33], v[140:143], v[188:191], v[30:33]
	v_mfma_f32_16x16x32_bf16 v[26:29], v[148:151], v[188:191], v[26:29]
	v_mfma_f32_16x16x32_bf16 v[14:17], v[140:143], v[196:199], v[14:17]
	v_mfma_f32_16x16x32_bf16 v[10:13], v[148:151], v[196:199], v[10:13]
	v_mfma_f32_16x16x32_bf16 v[62:65], v[144:147], v[176:179], v[62:65]
	v_mfma_f32_16x16x32_bf16 v[58:61], v[152:155], v[176:179], v[58:61]
	v_mfma_f32_16x16x32_bf16 v[46:49], v[144:147], v[184:187], v[46:49]
	v_mfma_f32_16x16x32_bf16 v[42:45], v[152:155], v[184:187], v[42:45]
	v_mfma_f32_16x16x32_bf16 v[30:33], v[144:147], v[192:195], v[30:33]
	v_mfma_f32_16x16x32_bf16 v[26:29], v[152:155], v[192:195], v[26:29]
	v_mfma_f32_16x16x32_bf16 v[14:17], v[144:147], v[200:203], v[14:17]
	v_mfma_f32_16x16x32_bf16 v[10:13], v[152:155], v[200:203], v[10:13]
	v_mfma_f32_16x16x32_bf16 v[54:57], v[156:159], v[172:175], v[54:57]
	v_mfma_f32_16x16x32_bf16 v[50:53], v[164:167], v[172:175], v[50:53]
	v_mfma_f32_16x16x32_bf16 v[38:41], v[156:159], v[180:183], v[38:41]
	v_mfma_f32_16x16x32_bf16 v[34:37], v[164:167], v[180:183], v[34:37]
	v_mfma_f32_16x16x32_bf16 v[22:25], v[156:159], v[188:191], v[22:25]
	v_mfma_f32_16x16x32_bf16 v[18:21], v[164:167], v[188:191], v[18:21]
	v_mfma_f32_16x16x32_bf16 v[6:9], v[156:159], v[196:199], v[6:9]
	v_mfma_f32_16x16x32_bf16 v[2:5], v[164:167], v[196:199], v[2:5]
	v_mfma_f32_16x16x32_bf16 v[54:57], v[160:163], v[176:179], v[54:57]
	v_mfma_f32_16x16x32_bf16 v[50:53], v[168:171], v[176:179], v[50:53]
	v_mfma_f32_16x16x32_bf16 v[38:41], v[160:163], v[184:187], v[38:41]
	v_mfma_f32_16x16x32_bf16 v[34:37], v[168:171], v[184:187], v[34:37]
	v_mfma_f32_16x16x32_bf16 v[22:25], v[160:163], v[192:195], v[22:25]
	v_mfma_f32_16x16x32_bf16 v[18:21], v[168:171], v[192:195], v[18:21]
	v_mfma_f32_16x16x32_bf16 v[6:9], v[160:163], v[200:203], v[6:9]
	v_mfma_f32_16x16x32_bf16 v[2:5], v[168:171], v[200:203], v[2:5]
	s_barrier
	v_add_u32_e32 v152, s91, v138
	v_add_u32_e32 v168, s13, v138
	ds_read_b128 v[140:143], v152
	ds_read_b128 v[144:147], v152 offset:1024
	ds_read_b128 v[148:151], v152 offset:2048
	ds_read_b128 v[152:155], v152 offset:3072
	ds_read_b128 v[156:159], v168
	ds_read_b128 v[160:163], v168 offset:1024
	ds_read_b128 v[164:167], v168 offset:2048
	ds_read_b128 v[168:171], v168 offset:3072
	s_mov_b32 m0, s84
	ds_read_b128 v[172:175], v139 offset:32768
	ds_read_b128 v[176:179], v139 offset:33792
	ds_read_b128 v[180:183], v139 offset:34816
	ds_read_b128 v[184:187], v139 offset:35840
	ds_read_b128 v[188:191], v139 offset:36864
	ds_read_b128 v[192:195], v139 offset:37888
	ds_read_b128 v[196:199], v139 offset:38912
	global_load_lds_dwordx4 v128, s[52:53]
	s_mov_b32 m0, s90
	ds_read_b128 v[200:203], v139 offset:39936
	global_load_lds_dwordx4 v124, s[52:53]
	s_waitcnt vmcnt(8)
	s_waitcnt lgkmcnt(0)
	s_barrier
	s_waitcnt lgkmcnt(0)
	v_mfma_f32_16x16x32_bf16 v[134:137], v[140:143], v[172:175], v[134:137]
	v_mfma_f32_16x16x32_bf16 v[130:133], v[148:151], v[172:175], v[130:133]
	v_mfma_f32_16x16x32_bf16 v[110:113], v[140:143], v[180:183], v[110:113]
	v_mfma_f32_16x16x32_bf16 v[106:109], v[148:151], v[180:183], v[106:109]
	v_mfma_f32_16x16x32_bf16 v[94:97], v[140:143], v[188:191], v[94:97]
	v_mfma_f32_16x16x32_bf16 v[90:93], v[148:151], v[188:191], v[90:93]
	v_mfma_f32_16x16x32_bf16 v[78:81], v[140:143], v[196:199], v[78:81]
	v_mfma_f32_16x16x32_bf16 v[74:77], v[148:151], v[196:199], v[74:77]
	v_mfma_f32_16x16x32_bf16 v[134:137], v[144:147], v[176:179], v[134:137]
	v_mfma_f32_16x16x32_bf16 v[130:133], v[152:155], v[176:179], v[130:133]
	v_mfma_f32_16x16x32_bf16 v[110:113], v[144:147], v[184:187], v[110:113]
	v_mfma_f32_16x16x32_bf16 v[106:109], v[152:155], v[184:187], v[106:109]
	v_mfma_f32_16x16x32_bf16 v[94:97], v[144:147], v[192:195], v[94:97]
	v_mfma_f32_16x16x32_bf16 v[90:93], v[152:155], v[192:195], v[90:93]
	v_mfma_f32_16x16x32_bf16 v[78:81], v[144:147], v[200:203], v[78:81]
	v_mfma_f32_16x16x32_bf16 v[74:77], v[152:155], v[200:203], v[74:77]
	v_mfma_f32_16x16x32_bf16 v[118:121], v[156:159], v[172:175], v[118:121]
	v_mfma_f32_16x16x32_bf16 v[114:117], v[164:167], v[172:175], v[114:117]
	v_mfma_f32_16x16x32_bf16 v[102:105], v[156:159], v[180:183], v[102:105]
	v_mfma_f32_16x16x32_bf16 v[98:101], v[164:167], v[180:183], v[98:101]
	v_mfma_f32_16x16x32_bf16 v[86:89], v[156:159], v[188:191], v[86:89]
	v_mfma_f32_16x16x32_bf16 v[82:85], v[164:167], v[188:191], v[82:85]
	v_mfma_f32_16x16x32_bf16 v[70:73], v[156:159], v[196:199], v[70:73]
	v_mfma_f32_16x16x32_bf16 v[66:69], v[164:167], v[196:199], v[66:69]
	v_mfma_f32_16x16x32_bf16 v[118:121], v[160:163], v[176:179], v[118:121]
	v_mfma_f32_16x16x32_bf16 v[114:117], v[168:171], v[176:179], v[114:117]
	v_mfma_f32_16x16x32_bf16 v[102:105], v[160:163], v[184:187], v[102:105]
	v_mfma_f32_16x16x32_bf16 v[98:101], v[168:171], v[184:187], v[98:101]
	v_mfma_f32_16x16x32_bf16 v[86:89], v[160:163], v[192:195], v[86:89]
	v_mfma_f32_16x16x32_bf16 v[82:85], v[168:171], v[192:195], v[82:85]
	v_mfma_f32_16x16x32_bf16 v[70:73], v[160:163], v[200:203], v[70:73]
	v_mfma_f32_16x16x32_bf16 v[66:69], v[168:171], v[200:203], v[66:69]
	s_barrier
	s_mov_b32 m0, vcc_hi
	v_lshl_add_u64 v[204:205], v[204:205], 0, s[56:57]
	ds_read_b128 v[172:175], v139 offset:49152
	ds_read_b128 v[176:179], v139 offset:50176
	ds_read_b128 v[180:183], v139 offset:51200
	ds_read_b128 v[184:187], v139 offset:52224
	ds_read_b128 v[188:191], v139 offset:53248
	ds_read_b128 v[192:195], v139 offset:54272
	ds_read_b128 v[196:199], v139 offset:55296
	ds_read_b128 v[200:203], v139 offset:56320
	global_load_lds_dwordx4 v[204:205], off
	s_mov_b32 m0, vcc_lo
	v_lshl_add_u64 v[204:205], v[206:207], 0, s[56:57]
	global_load_lds_dwordx4 v[204:205], off
	s_mov_b32 m0, s50
	s_nop 0
	global_load_lds_dwordx4 v126, s[48:49]
	s_mov_b32 m0, s12
	s_nop 0
	global_load_lds_dwordx4 v122, s[48:49]
	s_mov_b32 m0, s68
	v_lshl_add_u64 v[204:205], v[208:209], 0, s[56:57]
	global_load_lds_dwordx4 v[204:205], off
	s_mov_b32 m0, s93
	v_lshl_add_u64 v[204:205], v[216:217], 0, s[56:57]
	global_load_lds_dwordx4 v[204:205], off
	s_waitcnt vmcnt(8)
	s_waitcnt lgkmcnt(0)
	s_barrier
	s_waitcnt lgkmcnt(0)
	v_mfma_f32_16x16x32_bf16 v[62:65], v[140:143], v[172:175], v[62:65]
	v_mfma_f32_16x16x32_bf16 v[58:61], v[148:151], v[172:175], v[58:61]
	v_mfma_f32_16x16x32_bf16 v[46:49], v[140:143], v[180:183], v[46:49]
	v_mfma_f32_16x16x32_bf16 v[42:45], v[148:151], v[180:183], v[42:45]
	v_mfma_f32_16x16x32_bf16 v[30:33], v[140:143], v[188:191], v[30:33]
	v_mfma_f32_16x16x32_bf16 v[26:29], v[148:151], v[188:191], v[26:29]
	v_mfma_f32_16x16x32_bf16 v[14:17], v[140:143], v[196:199], v[14:17]
	v_mfma_f32_16x16x32_bf16 v[10:13], v[148:151], v[196:199], v[10:13]
	v_mfma_f32_16x16x32_bf16 v[62:65], v[144:147], v[176:179], v[62:65]
	v_mfma_f32_16x16x32_bf16 v[58:61], v[152:155], v[176:179], v[58:61]
	v_mfma_f32_16x16x32_bf16 v[46:49], v[144:147], v[184:187], v[46:49]
	v_mfma_f32_16x16x32_bf16 v[42:45], v[152:155], v[184:187], v[42:45]
	v_mfma_f32_16x16x32_bf16 v[30:33], v[144:147], v[192:195], v[30:33]
	v_mfma_f32_16x16x32_bf16 v[26:29], v[152:155], v[192:195], v[26:29]
	v_mfma_f32_16x16x32_bf16 v[14:17], v[144:147], v[200:203], v[14:17]
	v_mfma_f32_16x16x32_bf16 v[10:13], v[152:155], v[200:203], v[10:13]
	v_mfma_f32_16x16x32_bf16 v[54:57], v[156:159], v[172:175], v[54:57]
	v_mfma_f32_16x16x32_bf16 v[50:53], v[164:167], v[172:175], v[50:53]
	v_mfma_f32_16x16x32_bf16 v[38:41], v[156:159], v[180:183], v[38:41]
	v_mfma_f32_16x16x32_bf16 v[34:37], v[164:167], v[180:183], v[34:37]
	v_mfma_f32_16x16x32_bf16 v[22:25], v[156:159], v[188:191], v[22:25]
	v_mfma_f32_16x16x32_bf16 v[18:21], v[164:167], v[188:191], v[18:21]
	v_mfma_f32_16x16x32_bf16 v[6:9], v[156:159], v[196:199], v[6:9]
	v_mfma_f32_16x16x32_bf16 v[2:5], v[164:167], v[196:199], v[2:5]
	v_mfma_f32_16x16x32_bf16 v[54:57], v[160:163], v[176:179], v[54:57]
	v_mfma_f32_16x16x32_bf16 v[50:53], v[168:171], v[176:179], v[50:53]
	v_mfma_f32_16x16x32_bf16 v[38:41], v[160:163], v[184:187], v[38:41]
	v_mfma_f32_16x16x32_bf16 v[34:37], v[168:171], v[184:187], v[34:37]
	v_mfma_f32_16x16x32_bf16 v[22:25], v[160:163], v[192:195], v[22:25]
	v_mfma_f32_16x16x32_bf16 v[18:21], v[168:171], v[192:195], v[18:21]
	v_mfma_f32_16x16x32_bf16 v[6:9], v[160:163], v[200:203], v[6:9]
	v_mfma_f32_16x16x32_bf16 v[2:5], v[168:171], v[200:203], v[2:5]
	s_barrier
	s_movk_i32 s12, 0x100
	s_andn2_b64 vcc, exec, s[46:47]
	s_mov_b64 s[48:49], -1
	s_mov_b64 s[46:47], 0
	s_cbranch_vccz .LBB0_2467
	s_andn2_b64 vcc, exec, s[40:41]
	s_cbranch_vccnz .LBB0_2459
	v_mov_b32_e32 v2, 0
	s_mov_b32 s14, s34
	s_mov_b32 s95, s36
	s_mov_b64 s[28:29], s[44:45]
	s_mov_b64 s[30:31], s[42:43]
	s_mov_b32 s94, s58
	v_mov_b32_e32 v3, v2
	v_mov_b32_e32 v4, v2
	v_mov_b32_e32 v5, v2
	v_mov_b32_e32 v6, v2
	v_mov_b32_e32 v7, v2
	v_mov_b32_e32 v8, v2
	v_mov_b32_e32 v9, v2
	v_mov_b32_e32 v18, v2
	v_mov_b32_e32 v19, v2
	v_mov_b32_e32 v20, v2
	v_mov_b32_e32 v21, v2
	v_mov_b32_e32 v22, v2
	v_mov_b32_e32 v23, v2
	v_mov_b32_e32 v24, v2
	v_mov_b32_e32 v25, v2
	v_mov_b32_e32 v34, v2
	v_mov_b32_e32 v35, v2
	v_mov_b32_e32 v36, v2
	v_mov_b32_e32 v37, v2
	v_mov_b32_e32 v38, v2
	v_mov_b32_e32 v39, v2
	v_mov_b32_e32 v40, v2
	v_mov_b32_e32 v41, v2
	v_mov_b32_e32 v50, v2
	v_mov_b32_e32 v51, v2
	v_mov_b32_e32 v52, v2
	v_mov_b32_e32 v53, v2
	v_mov_b32_e32 v54, v2
	v_mov_b32_e32 v55, v2
	v_mov_b32_e32 v56, v2
	v_mov_b32_e32 v57, v2
	v_mov_b32_e32 v10, v2
	v_mov_b32_e32 v11, v2
	v_mov_b32_e32 v12, v2
	v_mov_b32_e32 v13, v2
	v_mov_b32_e32 v14, v2
	v_mov_b32_e32 v15, v2
	v_mov_b32_e32 v16, v2
	v_mov_b32_e32 v17, v2
	v_mov_b32_e32 v26, v2
	v_mov_b32_e32 v27, v2
	v_mov_b32_e32 v28, v2
	v_mov_b32_e32 v29, v2
	v_mov_b32_e32 v30, v2
	v_mov_b32_e32 v31, v2
	v_mov_b32_e32 v32, v2
	v_mov_b32_e32 v33, v2
	v_mov_b32_e32 v42, v2
	v_mov_b32_e32 v43, v2
	v_mov_b32_e32 v44, v2
	v_mov_b32_e32 v45, v2
	v_mov_b32_e32 v46, v2
	v_mov_b32_e32 v47, v2
	v_mov_b32_e32 v48, v2
	v_mov_b32_e32 v49, v2
	v_mov_b32_e32 v58, v2
	v_mov_b32_e32 v59, v2
	v_mov_b32_e32 v60, v2
	v_mov_b32_e32 v61, v2
	v_mov_b32_e32 v62, v2
	v_mov_b32_e32 v63, v2
	v_mov_b32_e32 v64, v2
	v_mov_b32_e32 v65, v2
	v_mov_b32_e32 v66, v2
	v_mov_b32_e32 v67, v2
	v_mov_b32_e32 v68, v2
	v_mov_b32_e32 v69, v2
	v_mov_b32_e32 v70, v2
	v_mov_b32_e32 v71, v2
	v_mov_b32_e32 v72, v2
	v_mov_b32_e32 v73, v2
	v_mov_b32_e32 v82, v2
	v_mov_b32_e32 v83, v2
	v_mov_b32_e32 v84, v2
	v_mov_b32_e32 v85, v2
	v_mov_b32_e32 v86, v2
	v_mov_b32_e32 v87, v2
	v_mov_b32_e32 v88, v2
	v_mov_b32_e32 v89, v2
	v_mov_b32_e32 v98, v2
	v_mov_b32_e32 v99, v2
	v_mov_b32_e32 v100, v2
	v_mov_b32_e32 v101, v2
	v_mov_b32_e32 v102, v2
	v_mov_b32_e32 v103, v2
	v_mov_b32_e32 v104, v2
	v_mov_b32_e32 v105, v2
	v_mov_b32_e32 v114, v2
	v_mov_b32_e32 v115, v2
	v_mov_b32_e32 v116, v2
	v_mov_b32_e32 v117, v2
	v_mov_b32_e32 v118, v2
	v_mov_b32_e32 v119, v2
	v_mov_b32_e32 v120, v2
	v_mov_b32_e32 v121, v2
	v_mov_b32_e32 v74, v2
	v_mov_b32_e32 v75, v2
	v_mov_b32_e32 v76, v2
	v_mov_b32_e32 v77, v2
	v_mov_b32_e32 v78, v2
	v_mov_b32_e32 v79, v2
	v_mov_b32_e32 v80, v2
	v_mov_b32_e32 v81, v2
	v_mov_b32_e32 v90, v2
	v_mov_b32_e32 v91, v2
	v_mov_b32_e32 v92, v2
	v_mov_b32_e32 v93, v2
	v_mov_b32_e32 v94, v2
	v_mov_b32_e32 v95, v2
	v_mov_b32_e32 v96, v2
	v_mov_b32_e32 v97, v2
	v_mov_b32_e32 v106, v2
	v_mov_b32_e32 v107, v2
	v_mov_b32_e32 v108, v2
	v_mov_b32_e32 v109, v2
	v_mov_b32_e32 v110, v2
	v_mov_b32_e32 v111, v2
	v_mov_b32_e32 v112, v2
	v_mov_b32_e32 v113, v2
	v_mov_b32_e32 v130, v2
	v_mov_b32_e32 v131, v2
	v_mov_b32_e32 v132, v2
	v_mov_b32_e32 v133, v2
	v_mov_b32_e32 v134, v2
	v_mov_b32_e32 v135, v2
	v_mov_b32_e32 v136, v2
	v_mov_b32_e32 v137, v2
	s_branch .LBB0_2459

.Lnobar_c6:
	v_add_u32_e32 v167, 0x10000, v181
.LBB0_2626:
	s_add_u32 s26, s6, 0xfffc0080
	s_addc_u32 s27, s7, -1
	s_add_i32 s50, 0, 0x10000
	s_cmp_eq_u32 s49, 12
	s_cselect_b32 s29, s21, s27
	s_cselect_b32 s28, s33, s26
	s_cselect_b32 s27, s19, s48
	s_cselect_b32 s26, s40, s41
	s_add_i32 s58, 0, 0x14000
	ds_read_b128 v[130:133], v167
	ds_read_b128 v[134:137], v167 offset:1024
	ds_read_b128 v[138:141], v167 offset:2048
	ds_read_b128 v[142:145], v167 offset:3072
	ds_read_b128 v[146:149], v167 offset:16384
	ds_read_b128 v[150:153], v167 offset:17408
	ds_read_b128 v[154:157], v167 offset:18432
	ds_read_b128 v[170:173], v167 offset:19456
	s_add_i32 m0, s36, 0xc000
	ds_read_b128 v[174:177], v183
	ds_read_b128 v[184:187], v183 offset:1024
	ds_read_b128 v[188:191], v183 offset:2048
	ds_read_b128 v[192:195], v183 offset:3072
	ds_read_b128 v[196:199], v183 offset:4096
	ds_read_b128 v[200:203], v183 offset:5120
	ds_read_b128 v[204:207], v183 offset:6144
	global_load_lds_dwordx4 v168, s[6:7]
	s_add_i32 m0, s36, 0xe000
	ds_read_b128 v[216:219], v183 offset:7168
	global_load_lds_dwordx4 v166, s[6:7]
	s_waitcnt vmcnt(8) lgkmcnt(0)
	s_barrier
	v_mfma_f32_16x16x32_bf16 v[126:129], v[130:133], v[174:177], v[126:129]
	v_mfma_f32_16x16x32_bf16 v[122:125], v[138:141], v[174:177], v[122:125]
	v_mfma_f32_16x16x32_bf16 v[110:113], v[130:133], v[188:191], v[110:113]
	v_mfma_f32_16x16x32_bf16 v[106:109], v[138:141], v[188:191], v[106:109]
	v_mfma_f32_16x16x32_bf16 v[94:97], v[130:133], v[196:199], v[94:97]
	v_mfma_f32_16x16x32_bf16 v[90:93], v[138:141], v[196:199], v[90:93]
	v_mfma_f32_16x16x32_bf16 v[78:81], v[130:133], v[204:207], v[78:81]
	v_mfma_f32_16x16x32_bf16 v[74:77], v[138:141], v[204:207], v[74:77]
	v_mfma_f32_16x16x32_bf16 v[126:129], v[134:137], v[184:187], v[126:129]
	v_mfma_f32_16x16x32_bf16 v[122:125], v[142:145], v[184:187], v[122:125]
	v_mfma_f32_16x16x32_bf16 v[110:113], v[134:137], v[192:195], v[110:113]
	v_mfma_f32_16x16x32_bf16 v[106:109], v[142:145], v[192:195], v[106:109]
	v_mfma_f32_16x16x32_bf16 v[94:97], v[134:137], v[200:203], v[94:97]
	v_mfma_f32_16x16x32_bf16 v[90:93], v[142:145], v[200:203], v[90:93]
	v_mfma_f32_16x16x32_bf16 v[78:81], v[134:137], v[216:219], v[78:81]
	v_mfma_f32_16x16x32_bf16 v[74:77], v[142:145], v[216:219], v[74:77]
	v_mfma_f32_16x16x32_bf16 v[118:121], v[146:149], v[174:177], v[118:121]
	v_mfma_f32_16x16x32_bf16 v[114:117], v[154:157], v[174:177], v[114:117]
	v_mfma_f32_16x16x32_bf16 v[102:105], v[146:149], v[188:191], v[102:105]
	v_mfma_f32_16x16x32_bf16 v[98:101], v[154:157], v[188:191], v[98:101]
	v_mfma_f32_16x16x32_bf16 v[86:89], v[146:149], v[196:199], v[86:89]
	v_mfma_f32_16x16x32_bf16 v[82:85], v[154:157], v[196:199], v[82:85]
	v_mfma_f32_16x16x32_bf16 v[70:73], v[146:149], v[204:207], v[70:73]
	v_mfma_f32_16x16x32_bf16 v[66:69], v[154:157], v[204:207], v[66:69]
	v_mfma_f32_16x16x32_bf16 v[118:121], v[150:153], v[184:187], v[118:121]
	v_mfma_f32_16x16x32_bf16 v[114:117], v[170:173], v[184:187], v[114:117]
	v_mfma_f32_16x16x32_bf16 v[102:105], v[150:153], v[192:195], v[102:105]
	v_mfma_f32_16x16x32_bf16 v[98:101], v[170:173], v[192:195], v[98:101]
	v_mfma_f32_16x16x32_bf16 v[86:89], v[150:153], v[200:203], v[86:89]
	v_mfma_f32_16x16x32_bf16 v[82:85], v[170:173], v[200:203], v[82:85]
	v_mfma_f32_16x16x32_bf16 v[70:73], v[150:153], v[216:219], v[70:73]
	v_mfma_f32_16x16x32_bf16 v[66:69], v[170:173], v[216:219], v[66:69]
	s_barrier
	s_add_i32 s50, s50, s35
	v_lshl_add_u64 v[178:179], s[26:27], 0, v[162:163]
	s_mov_b32 m0, s50
	ds_read_b128 v[174:177], v183 offset:16384
	ds_read_b128 v[184:187], v183 offset:17408
	ds_read_b128 v[188:191], v183 offset:18432
	ds_read_b128 v[192:195], v183 offset:19456
	ds_read_b128 v[196:199], v183 offset:20480
	ds_read_b128 v[200:203], v183 offset:21504
	ds_read_b128 v[204:207], v183 offset:22528
	ds_read_b128 v[216:219], v183 offset:23552
	global_load_lds_dwordx4 v162, s[26:27]
	s_add_i32 m0, s50, 0x2000
	s_add_u32 s52, s26, 0x40000
	v_lshl_add_u64 v[208:209], s[26:27], 0, v[158:159]
	s_addc_u32 s53, s27, 0
	s_add_i32 s50, s58, s35
	global_load_lds_dwordx4 v158, s[26:27]
	s_mov_b32 m0, s50
	v_lshl_add_u64 v[222:223], s[28:29], 0, v[160:161]
	global_load_lds_dwordx4 v162, s[52:53]
	s_add_i32 m0, s50, 0x2000
	s_nop 0
	global_load_lds_dwordx4 v158, s[52:53]
	s_mov_b32 m0, s36
	v_lshl_add_u64 v[220:221], s[28:29], 0, v[164:165]
	global_load_lds_dwordx4 v164, s[28:29]
	s_mov_b32 m0, s37
	s_nop 0
	global_load_lds_dwordx4 v160, s[28:29]
	s_waitcnt vmcnt(8) lgkmcnt(0)
	s_barrier
	v_mfma_f32_16x16x32_bf16 v[62:65], v[130:133], v[174:177], v[62:65]
	v_mfma_f32_16x16x32_bf16 v[58:61], v[138:141], v[174:177], v[58:61]
	v_mfma_f32_16x16x32_bf16 v[46:49], v[130:133], v[188:191], v[46:49]
	v_mfma_f32_16x16x32_bf16 v[42:45], v[138:141], v[188:191], v[42:45]
	v_mfma_f32_16x16x32_bf16 v[30:33], v[130:133], v[196:199], v[30:33]
	v_mfma_f32_16x16x32_bf16 v[26:29], v[138:141], v[196:199], v[26:29]
	v_mfma_f32_16x16x32_bf16 v[14:17], v[130:133], v[204:207], v[14:17]
	v_mfma_f32_16x16x32_bf16 v[10:13], v[138:141], v[204:207], v[10:13]
	v_mfma_f32_16x16x32_bf16 v[62:65], v[134:137], v[184:187], v[62:65]
	v_mfma_f32_16x16x32_bf16 v[58:61], v[142:145], v[184:187], v[58:61]
	v_mfma_f32_16x16x32_bf16 v[46:49], v[134:137], v[192:195], v[46:49]
	v_mfma_f32_16x16x32_bf16 v[42:45], v[142:145], v[192:195], v[42:45]
	v_mfma_f32_16x16x32_bf16 v[30:33], v[134:137], v[200:203], v[30:33]
	v_mfma_f32_16x16x32_bf16 v[26:29], v[142:145], v[200:203], v[26:29]
	v_mfma_f32_16x16x32_bf16 v[14:17], v[134:137], v[216:219], v[14:17]
	v_mfma_f32_16x16x32_bf16 v[10:13], v[142:145], v[216:219], v[10:13]
	v_mfma_f32_16x16x32_bf16 v[54:57], v[146:149], v[174:177], v[54:57]
	v_mfma_f32_16x16x32_bf16 v[50:53], v[154:157], v[174:177], v[50:53]
	v_mfma_f32_16x16x32_bf16 v[38:41], v[146:149], v[188:191], v[38:41]
	v_mfma_f32_16x16x32_bf16 v[34:37], v[154:157], v[188:191], v[34:37]
	v_mfma_f32_16x16x32_bf16 v[22:25], v[146:149], v[196:199], v[22:25]
	v_mfma_f32_16x16x32_bf16 v[18:21], v[154:157], v[196:199], v[18:21]
	v_mfma_f32_16x16x32_bf16 v[6:9], v[146:149], v[204:207], v[6:9]
	v_mfma_f32_16x16x32_bf16 v[2:5], v[154:157], v[204:207], v[2:5]
	v_mfma_f32_16x16x32_bf16 v[54:57], v[150:153], v[184:187], v[54:57]
	v_mfma_f32_16x16x32_bf16 v[50:53], v[170:173], v[184:187], v[50:53]
	v_mfma_f32_16x16x32_bf16 v[38:41], v[150:153], v[192:195], v[38:41]
	v_mfma_f32_16x16x32_bf16 v[34:37], v[170:173], v[192:195], v[34:37]
	v_mfma_f32_16x16x32_bf16 v[22:25], v[150:153], v[200:203], v[22:25]
	v_mfma_f32_16x16x32_bf16 v[18:21], v[170:173], v[200:203], v[18:21]
	v_mfma_f32_16x16x32_bf16 v[6:9], v[150:153], v[216:219], v[6:9]
	v_mfma_f32_16x16x32_bf16 v[2:5], v[170:173], v[216:219], v[2:5]
	s_barrier
	s_add_i32 s50, 0, 0x18000
	s_add_i32 s52, 0, 0x1c000
	ds_read_b128 v[130:133], v167 offset:32768
	ds_read_b128 v[134:137], v167 offset:33792
	ds_read_b128 v[138:141], v167 offset:34816
	ds_read_b128 v[142:145], v167 offset:35840
	ds_read_b128 v[146:149], v167 offset:49152
	ds_read_b128 v[150:153], v167 offset:50176
	ds_read_b128 v[154:157], v167 offset:51200
	ds_read_b128 v[170:173], v167 offset:52224
	s_add_u32 s28, s28, 0x40000
	s_addc_u32 s29, s29, 0
	s_mov_b32 m0, s42
	ds_read_b128 v[174:177], v183 offset:32768
	ds_read_b128 v[184:187], v183 offset:33792
	ds_read_b128 v[188:191], v183 offset:34816
	ds_read_b128 v[192:195], v183 offset:35840
	ds_read_b128 v[196:199], v183 offset:36864
	ds_read_b128 v[200:203], v183 offset:37888
	ds_read_b128 v[204:207], v183 offset:38912
	global_load_lds_dwordx4 v164, s[28:29]
	s_mov_b32 m0, s43
	ds_read_b128 v[216:219], v183 offset:39936
	global_load_lds_dwordx4 v160, s[28:29]
	s_waitcnt vmcnt(8) lgkmcnt(0)
	s_barrier
	v_mfma_f32_16x16x32_bf16 v[126:129], v[130:133], v[174:177], v[126:129]
	v_mfma_f32_16x16x32_bf16 v[122:125], v[138:141], v[174:177], v[122:125]
	v_mfma_f32_16x16x32_bf16 v[110:113], v[130:133], v[188:191], v[110:113]
	v_mfma_f32_16x16x32_bf16 v[106:109], v[138:141], v[188:191], v[106:109]
	v_mfma_f32_16x16x32_bf16 v[94:97], v[130:133], v[196:199], v[94:97]
	v_mfma_f32_16x16x32_bf16 v[90:93], v[138:141], v[196:199], v[90:93]
	v_mfma_f32_16x16x32_bf16 v[78:81], v[130:133], v[204:207], v[78:81]
	v_mfma_f32_16x16x32_bf16 v[74:77], v[138:141], v[204:207], v[74:77]
	v_mfma_f32_16x16x32_bf16 v[126:129], v[134:137], v[184:187], v[126:129]
	v_mfma_f32_16x16x32_bf16 v[122:125], v[142:145], v[184:187], v[122:125]
	v_mfma_f32_16x16x32_bf16 v[110:113], v[134:137], v[192:195], v[110:113]
	v_mfma_f32_16x16x32_bf16 v[106:109], v[142:145], v[192:195], v[106:109]
	v_mfma_f32_16x16x32_bf16 v[94:97], v[134:137], v[200:203], v[94:97]
	v_mfma_f32_16x16x32_bf16 v[90:93], v[142:145], v[200:203], v[90:93]
	v_mfma_f32_16x16x32_bf16 v[78:81], v[134:137], v[216:219], v[78:81]
	v_mfma_f32_16x16x32_bf16 v[74:77], v[142:145], v[216:219], v[74:77]
	v_mfma_f32_16x16x32_bf16 v[118:121], v[146:149], v[174:177], v[118:121]
	v_mfma_f32_16x16x32_bf16 v[114:117], v[154:157], v[174:177], v[114:117]
	v_mfma_f32_16x16x32_bf16 v[102:105], v[146:149], v[188:191], v[102:105]
	v_mfma_f32_16x16x32_bf16 v[98:101], v[154:157], v[188:191], v[98:101]
	v_mfma_f32_16x16x32_bf16 v[86:89], v[146:149], v[196:199], v[86:89]
	v_mfma_f32_16x16x32_bf16 v[82:85], v[154:157], v[196:199], v[82:85]
	v_mfma_f32_16x16x32_bf16 v[70:73], v[146:149], v[204:207], v[70:73]
	v_mfma_f32_16x16x32_bf16 v[66:69], v[154:157], v[204:207], v[66:69]
	v_mfma_f32_16x16x32_bf16 v[118:121], v[150:153], v[184:187], v[118:121]
	v_mfma_f32_16x16x32_bf16 v[114:117], v[170:173], v[184:187], v[114:117]
	v_mfma_f32_16x16x32_bf16 v[102:105], v[150:153], v[192:195], v[102:105]
	v_mfma_f32_16x16x32_bf16 v[98:101], v[170:173], v[192:195], v[98:101]
	v_mfma_f32_16x16x32_bf16 v[86:89], v[150:153], v[200:203], v[86:89]
	v_mfma_f32_16x16x32_bf16 v[82:85], v[170:173], v[200:203], v[82:85]
	v_mfma_f32_16x16x32_bf16 v[70:73], v[150:153], v[216:219], v[70:73]
	v_mfma_f32_16x16x32_bf16 v[66:69], v[170:173], v[216:219], v[66:69]
	s_barrier
	s_add_i32 s28, s50, s35
	v_lshl_add_u64 v[178:179], v[178:179], 0, s[56:57]
	s_mov_b32 m0, s28
	ds_read_b128 v[174:177], v183 offset:49152
	ds_read_b128 v[184:187], v183 offset:50176
	ds_read_b128 v[188:191], v183 offset:51200
	ds_read_b128 v[192:195], v183 offset:52224
	ds_read_b128 v[196:199], v183 offset:53248
	ds_read_b128 v[200:203], v183 offset:54272
	ds_read_b128 v[204:207], v183 offset:55296
	ds_read_b128 v[216:219], v183 offset:56320
	global_load_lds_dwordx4 v[178:179], off
	s_add_i32 m0, s28, 0x2000
	s_add_u32 s26, s26, 0x40080
	v_lshl_add_u64 v[178:179], v[208:209], 0, s[56:57]
	s_addc_u32 s27, s27, 0
	s_add_i32 s28, s52, s35
	global_load_lds_dwordx4 v[178:179], off
	s_mov_b32 m0, s28
	s_nop 0
	global_load_lds_dwordx4 v162, s[26:27]
	s_add_i32 m0, s28, 0x2000
	s_nop 0
	global_load_lds_dwordx4 v158, s[26:27]
	s_mov_b32 m0, s44
	v_lshl_add_u64 v[178:179], v[220:221], 0, s[56:57]
	global_load_lds_dwordx4 v[178:179], off
	s_mov_b32 m0, s45
	v_lshl_add_u64 v[178:179], v[222:223], 0, s[56:57]
	global_load_lds_dwordx4 v[178:179], off
	s_waitcnt vmcnt(8) lgkmcnt(0)
	s_barrier
	v_mfma_f32_16x16x32_bf16 v[62:65], v[130:133], v[174:177], v[62:65]
	v_mfma_f32_16x16x32_bf16 v[58:61], v[138:141], v[174:177], v[58:61]
	v_mfma_f32_16x16x32_bf16 v[46:49], v[130:133], v[188:191], v[46:49]
	v_mfma_f32_16x16x32_bf16 v[42:45], v[138:141], v[188:191], v[42:45]
	v_mfma_f32_16x16x32_bf16 v[30:33], v[130:133], v[196:199], v[30:33]
	v_mfma_f32_16x16x32_bf16 v[26:29], v[138:141], v[196:199], v[26:29]
	v_mfma_f32_16x16x32_bf16 v[14:17], v[130:133], v[204:207], v[14:17]
	v_mfma_f32_16x16x32_bf16 v[10:13], v[138:141], v[204:207], v[10:13]
	v_mfma_f32_16x16x32_bf16 v[62:65], v[134:137], v[184:187], v[62:65]
	v_mfma_f32_16x16x32_bf16 v[58:61], v[142:145], v[184:187], v[58:61]
	v_mfma_f32_16x16x32_bf16 v[46:49], v[134:137], v[192:195], v[46:49]
	v_mfma_f32_16x16x32_bf16 v[42:45], v[142:145], v[192:195], v[42:45]
	v_mfma_f32_16x16x32_bf16 v[30:33], v[134:137], v[200:203], v[30:33]
	v_mfma_f32_16x16x32_bf16 v[26:29], v[142:145], v[200:203], v[26:29]
	v_mfma_f32_16x16x32_bf16 v[14:17], v[134:137], v[216:219], v[14:17]
	v_mfma_f32_16x16x32_bf16 v[10:13], v[142:145], v[216:219], v[10:13]
	v_mfma_f32_16x16x32_bf16 v[54:57], v[146:149], v[174:177], v[54:57]
	v_mfma_f32_16x16x32_bf16 v[50:53], v[154:157], v[174:177], v[50:53]
	v_mfma_f32_16x16x32_bf16 v[38:41], v[146:149], v[188:191], v[38:41]
	v_mfma_f32_16x16x32_bf16 v[34:37], v[154:157], v[188:191], v[34:37]
	v_mfma_f32_16x16x32_bf16 v[22:25], v[146:149], v[196:199], v[22:25]
	v_mfma_f32_16x16x32_bf16 v[18:21], v[154:157], v[196:199], v[18:21]
	v_mfma_f32_16x16x32_bf16 v[6:9], v[146:149], v[204:207], v[6:9]
	v_mfma_f32_16x16x32_bf16 v[2:5], v[154:157], v[204:207], v[2:5]
	v_mfma_f32_16x16x32_bf16 v[54:57], v[150:153], v[184:187], v[54:57]
	v_mfma_f32_16x16x32_bf16 v[50:53], v[170:173], v[184:187], v[50:53]
	v_mfma_f32_16x16x32_bf16 v[38:41], v[150:153], v[192:195], v[38:41]
	v_mfma_f32_16x16x32_bf16 v[34:37], v[170:173], v[192:195], v[34:37]
	v_mfma_f32_16x16x32_bf16 v[22:25], v[150:153], v[200:203], v[22:25]
	v_mfma_f32_16x16x32_bf16 v[18:21], v[170:173], v[200:203], v[18:21]
	v_mfma_f32_16x16x32_bf16 v[6:9], v[150:153], v[216:219], v[6:9]
	v_mfma_f32_16x16x32_bf16 v[2:5], v[170:173], v[216:219], v[2:5]
	s_barrier
	s_add_i32 s49, s49, 2
	s_add_u32 s41, s41, 0x100
	s_addc_u32 s48, s48, 0
	s_add_u32 s6, s6, 0x100
	s_addc_u32 s7, s7, 0
	s_cmp_gt_u32 s49, 13
	s_cbranch_scc0 .LBB0_2626
	s_and_b64 vcc, exec, s[16:17]
	s_cbranch_vccz .LBB0_2629
	s_barrier

.LBB0_2702:
	s_add_u32 s59, s36, 0x100
	s_addc_u32 s82, s37, 0
	s_ashr_i32 s29, s28, 31
	s_lshl_b64 s[30:31], s[28:29], 21
	s_add_u32 s34, s63, s30
	s_addc_u32 s35, s70, s31
	s_and_b64 s[30:31], s[42:43], exec
	s_cselect_b32 s29, s35, s25
	s_cselect_b32 s83, s34, s24
	s_ashr_i32 s27, s26, 31
	s_lshl_b64 s[30:31], s[26:27], 21
	s_add_u32 s30, s71, s30
	s_addc_u32 s31, s76, s31
	s_and_b64 s[44:45], s[42:43], exec
	s_cselect_b32 s27, s31, s37
	s_cselect_b32 s84, s30, s36
	s_add_u32 s36, s24, 0x100080
	s_addc_u32 s37, s25, 0
	v_lshl_add_u64 v[142:143], s[36:37], 0, v[138:139]
	v_lshl_add_u64 v[144:145], s[36:37], 0, v[140:141]
	s_mov_b32 s85, -2
	s_mov_b64 s[36:37], 0
	v_add_u32_e32 v241, 0x10000, v146
.LBB0_2703:
	s_add_u32 s44, s24, s36
	s_addc_u32 s45, s25, s37
	s_add_u32 s44, s44, 0x100
	s_addc_u32 s45, s45, 0
	s_add_u32 s50, s59, s36
	s_addc_u32 s64, s82, s37
	s_add_i32 s65, 0, 0x10000
	s_cmpk_eq_i32 s36, 0x1f00
	s_cselect_b32 s47, s29, s45
	s_cselect_b32 s46, s83, s44
	s_cselect_b32 s45, s27, s64
	s_cselect_b32 s44, s84, s50
	s_add_i32 s50, 0, 0x14000
	ds_read_b128 v[148:151], v241
	ds_read_b128 v[152:155], v241 offset:1024
	ds_read_b128 v[156:159], v241 offset:2048
	ds_read_b128 v[160:163], v241 offset:3072
	ds_read_b128 v[168:171], v241 offset:16384
	ds_read_b128 v[172:175], v241 offset:17408
	ds_read_b128 v[176:179], v241 offset:18432
	ds_read_b128 v[180:183], v241 offset:19456
	v_lshl_add_u64 v[164:165], v[144:145], 0, s[36:37]
	s_add_i32 m0, s4, 0xc000
	ds_read_b128 v[184:187], v147
	ds_read_b128 v[188:191], v147 offset:1024
	ds_read_b128 v[192:195], v147 offset:2048
	ds_read_b128 v[196:199], v147 offset:3072
	ds_read_b128 v[200:203], v147 offset:4096
	ds_read_b128 v[204:207], v147 offset:5120
	ds_read_b128 v[216:219], v147 offset:6144
	ds_read_b128 v[220:223], v147 offset:7168
	global_load_lds_dwordx4 v[164:165], off
	s_add_i32 m0, s4, 0xe000
	v_lshl_add_u64 v[164:165], v[142:143], 0, s[36:37]
	global_load_lds_dwordx4 v[164:165], off
	s_waitcnt vmcnt(8) lgkmcnt(0)
	s_barrier
	v_mfma_f32_16x16x32_bf16 v[134:137], v[148:151], v[184:187], v[134:137]
	v_mfma_f32_16x16x32_bf16 v[130:133], v[156:159], v[184:187], v[130:133]
	v_mfma_f32_16x16x32_bf16 v[110:113], v[148:151], v[192:195], v[110:113]
	v_mfma_f32_16x16x32_bf16 v[106:109], v[156:159], v[192:195], v[106:109]
	v_mfma_f32_16x16x32_bf16 v[94:97], v[148:151], v[200:203], v[94:97]
	v_mfma_f32_16x16x32_bf16 v[90:93], v[156:159], v[200:203], v[90:93]
	v_mfma_f32_16x16x32_bf16 v[78:81], v[148:151], v[216:219], v[78:81]
	v_mfma_f32_16x16x32_bf16 v[74:77], v[156:159], v[216:219], v[74:77]
	v_mfma_f32_16x16x32_bf16 v[134:137], v[152:155], v[188:191], v[134:137]
	v_mfma_f32_16x16x32_bf16 v[130:133], v[160:163], v[188:191], v[130:133]
	v_mfma_f32_16x16x32_bf16 v[110:113], v[152:155], v[196:199], v[110:113]
	v_mfma_f32_16x16x32_bf16 v[106:109], v[160:163], v[196:199], v[106:109]
	v_mfma_f32_16x16x32_bf16 v[94:97], v[152:155], v[204:207], v[94:97]
	v_mfma_f32_16x16x32_bf16 v[90:93], v[160:163], v[204:207], v[90:93]
	v_mfma_f32_16x16x32_bf16 v[78:81], v[152:155], v[220:223], v[78:81]
	v_mfma_f32_16x16x32_bf16 v[74:77], v[160:163], v[220:223], v[74:77]
	v_mfma_f32_16x16x32_bf16 v[122:125], v[168:171], v[184:187], v[122:125]
	v_mfma_f32_16x16x32_bf16 v[114:117], v[176:179], v[184:187], v[114:117]
	v_mfma_f32_16x16x32_bf16 v[102:105], v[168:171], v[192:195], v[102:105]
	v_mfma_f32_16x16x32_bf16 v[98:101], v[176:179], v[192:195], v[98:101]
	v_mfma_f32_16x16x32_bf16 v[86:89], v[168:171], v[200:203], v[86:89]
	v_mfma_f32_16x16x32_bf16 v[82:85], v[176:179], v[200:203], v[82:85]
	v_mfma_f32_16x16x32_bf16 v[70:73], v[168:171], v[216:219], v[70:73]
	v_mfma_f32_16x16x32_bf16 v[66:69], v[176:179], v[216:219], v[66:69]
	v_mfma_f32_16x16x32_bf16 v[122:125], v[172:175], v[188:191], v[122:125]
	v_mfma_f32_16x16x32_bf16 v[114:117], v[180:183], v[188:191], v[114:117]
	v_mfma_f32_16x16x32_bf16 v[102:105], v[172:175], v[196:199], v[102:105]
	v_mfma_f32_16x16x32_bf16 v[98:101], v[180:183], v[196:199], v[98:101]
	v_mfma_f32_16x16x32_bf16 v[86:89], v[172:175], v[204:207], v[86:89]
	v_mfma_f32_16x16x32_bf16 v[82:85], v[180:183], v[204:207], v[82:85]
	v_mfma_f32_16x16x32_bf16 v[70:73], v[172:175], v[220:223], v[70:73]
	v_mfma_f32_16x16x32_bf16 v[66:69], v[180:183], v[220:223], v[66:69]
	s_barrier
	s_add_i32 s64, s65, s77
	v_lshl_add_u64 v[164:165], s[44:45], 0, v[126:127]
	s_mov_b32 m0, s64
	ds_read_b128 v[184:187], v147 offset:16384
	ds_read_b128 v[188:191], v147 offset:17408
	ds_read_b128 v[192:195], v147 offset:18432
	ds_read_b128 v[196:199], v147 offset:19456
	ds_read_b128 v[200:203], v147 offset:20480
	ds_read_b128 v[204:207], v147 offset:21504
	ds_read_b128 v[216:219], v147 offset:22528
	ds_read_b128 v[220:223], v147 offset:23552
	global_load_lds_dwordx4 v126, s[44:45]
	s_add_i32 m0, s64, 0x2000
	s_add_u32 s92, s44, 0x100000
	v_lshl_add_u64 v[208:209], s[44:45], 0, v[118:119]
	s_addc_u32 s93, s45, 0
	s_add_i32 s50, s50, s77
	global_load_lds_dwordx4 v118, s[44:45]
	s_mov_b32 m0, s50
	v_lshl_add_u64 v[242:243], s[46:47], 0, v[120:121]
	global_load_lds_dwordx4 v126, s[92:93]
	s_add_i32 m0, s50, 0x2000
	s_nop 0
	global_load_lds_dwordx4 v118, s[92:93]
	s_mov_b32 m0, s4
	v_lshl_add_u64 v[224:225], s[46:47], 0, v[128:129]
	global_load_lds_dwordx4 v128, s[46:47]
	s_mov_b32 m0, s33
	s_nop 0
	global_load_lds_dwordx4 v120, s[46:47]
	s_waitcnt vmcnt(8) lgkmcnt(0)
	s_barrier
	v_mfma_f32_16x16x32_bf16 v[62:65], v[148:151], v[184:187], v[62:65]
	v_mfma_f32_16x16x32_bf16 v[58:61], v[156:159], v[184:187], v[58:61]
	v_mfma_f32_16x16x32_bf16 v[46:49], v[148:151], v[192:195], v[46:49]
	v_mfma_f32_16x16x32_bf16 v[42:45], v[156:159], v[192:195], v[42:45]
	v_mfma_f32_16x16x32_bf16 v[30:33], v[148:151], v[200:203], v[30:33]
	v_mfma_f32_16x16x32_bf16 v[26:29], v[156:159], v[200:203], v[26:29]
	v_mfma_f32_16x16x32_bf16 v[14:17], v[148:151], v[216:219], v[14:17]
	v_mfma_f32_16x16x32_bf16 v[10:13], v[156:159], v[216:219], v[10:13]
	v_mfma_f32_16x16x32_bf16 v[62:65], v[152:155], v[188:191], v[62:65]
	v_mfma_f32_16x16x32_bf16 v[58:61], v[160:163], v[188:191], v[58:61]
	v_mfma_f32_16x16x32_bf16 v[46:49], v[152:155], v[196:199], v[46:49]
	v_mfma_f32_16x16x32_bf16 v[42:45], v[160:163], v[196:199], v[42:45]
	v_mfma_f32_16x16x32_bf16 v[30:33], v[152:155], v[204:207], v[30:33]
	v_mfma_f32_16x16x32_bf16 v[26:29], v[160:163], v[204:207], v[26:29]
	v_mfma_f32_16x16x32_bf16 v[14:17], v[152:155], v[220:223], v[14:17]
	v_mfma_f32_16x16x32_bf16 v[10:13], v[160:163], v[220:223], v[10:13]
	v_mfma_f32_16x16x32_bf16 v[54:57], v[168:171], v[184:187], v[54:57]
	v_mfma_f32_16x16x32_bf16 v[50:53], v[176:179], v[184:187], v[50:53]
	v_mfma_f32_16x16x32_bf16 v[38:41], v[168:171], v[192:195], v[38:41]
	v_mfma_f32_16x16x32_bf16 v[34:37], v[176:179], v[192:195], v[34:37]
	v_mfma_f32_16x16x32_bf16 v[22:25], v[168:171], v[200:203], v[22:25]
	v_mfma_f32_16x16x32_bf16 v[18:21], v[176:179], v[200:203], v[18:21]
	v_mfma_f32_16x16x32_bf16 v[6:9], v[168:171], v[216:219], v[6:9]
	v_mfma_f32_16x16x32_bf16 v[2:5], v[176:179], v[216:219], v[2:5]
	v_mfma_f32_16x16x32_bf16 v[54:57], v[172:175], v[188:191], v[54:57]
	v_mfma_f32_16x16x32_bf16 v[50:53], v[180:183], v[188:191], v[50:53]
	v_mfma_f32_16x16x32_bf16 v[38:41], v[172:175], v[196:199], v[38:41]
	v_mfma_f32_16x16x32_bf16 v[34:37], v[180:183], v[196:199], v[34:37]
	v_mfma_f32_16x16x32_bf16 v[22:25], v[172:175], v[204:207], v[22:25]
	v_mfma_f32_16x16x32_bf16 v[18:21], v[180:183], v[204:207], v[18:21]
	v_mfma_f32_16x16x32_bf16 v[6:9], v[172:175], v[220:223], v[6:9]
	v_mfma_f32_16x16x32_bf16 v[2:5], v[180:183], v[220:223], v[2:5]
	s_barrier
	s_add_i32 s50, 0, 0x18000
	s_add_i32 s64, 0, 0x1c000
	ds_read_b128 v[148:151], v241 offset:32768
	ds_read_b128 v[152:155], v241 offset:33792
	ds_read_b128 v[156:159], v241 offset:34816
	ds_read_b128 v[160:163], v241 offset:35840
	ds_read_b128 v[168:171], v241 offset:49152
	ds_read_b128 v[172:175], v241 offset:50176
	ds_read_b128 v[176:179], v241 offset:51200
	ds_read_b128 v[180:183], v241 offset:52224
	s_add_u32 s46, s46, 0x100000
	s_addc_u32 s47, s47, 0
	s_mov_b32 m0, s78
	ds_read_b128 v[184:187], v147 offset:32768
	ds_read_b128 v[188:191], v147 offset:33792
	ds_read_b128 v[192:195], v147 offset:34816
	ds_read_b128 v[196:199], v147 offset:35840
	ds_read_b128 v[200:203], v147 offset:36864
	ds_read_b128 v[204:207], v147 offset:37888
	ds_read_b128 v[216:219], v147 offset:38912
	ds_read_b128 v[220:223], v147 offset:39936
	global_load_lds_dwordx4 v128, s[46:47]
	s_mov_b32 m0, s79
	v_lshl_add_u64 v[244:245], s[46:47], 0, v[120:121]
	global_load_lds_dwordx4 v120, s[46:47]
	s_waitcnt vmcnt(8) lgkmcnt(0)
	s_barrier
	v_mfma_f32_16x16x32_bf16 v[134:137], v[148:151], v[184:187], v[134:137]
	v_mfma_f32_16x16x32_bf16 v[130:133], v[156:159], v[184:187], v[130:133]
	v_mfma_f32_16x16x32_bf16 v[110:113], v[148:151], v[192:195], v[110:113]
	v_mfma_f32_16x16x32_bf16 v[106:109], v[156:159], v[192:195], v[106:109]
	v_mfma_f32_16x16x32_bf16 v[94:97], v[148:151], v[200:203], v[94:97]
	v_mfma_f32_16x16x32_bf16 v[90:93], v[156:159], v[200:203], v[90:93]
	v_mfma_f32_16x16x32_bf16 v[78:81], v[148:151], v[216:219], v[78:81]
	v_mfma_f32_16x16x32_bf16 v[74:77], v[156:159], v[216:219], v[74:77]
	v_mfma_f32_16x16x32_bf16 v[134:137], v[152:155], v[188:191], v[134:137]
	v_mfma_f32_16x16x32_bf16 v[130:133], v[160:163], v[188:191], v[130:133]
	v_mfma_f32_16x16x32_bf16 v[110:113], v[152:155], v[196:199], v[110:113]
	v_mfma_f32_16x16x32_bf16 v[106:109], v[160:163], v[196:199], v[106:109]
	v_mfma_f32_16x16x32_bf16 v[94:97], v[152:155], v[204:207], v[94:97]
	v_mfma_f32_16x16x32_bf16 v[90:93], v[160:163], v[204:207], v[90:93]
	v_mfma_f32_16x16x32_bf16 v[78:81], v[152:155], v[220:223], v[78:81]
	v_mfma_f32_16x16x32_bf16 v[74:77], v[160:163], v[220:223], v[74:77]
	v_mfma_f32_16x16x32_bf16 v[122:125], v[168:171], v[184:187], v[122:125]
	v_mfma_f32_16x16x32_bf16 v[114:117], v[176:179], v[184:187], v[114:117]
	v_mfma_f32_16x16x32_bf16 v[102:105], v[168:171], v[192:195], v[102:105]
	v_mfma_f32_16x16x32_bf16 v[98:101], v[176:179], v[192:195], v[98:101]
	v_mfma_f32_16x16x32_bf16 v[86:89], v[168:171], v[200:203], v[86:89]
	v_mfma_f32_16x16x32_bf16 v[82:85], v[176:179], v[200:203], v[82:85]
	v_mfma_f32_16x16x32_bf16 v[70:73], v[168:171], v[216:219], v[70:73]
	v_mfma_f32_16x16x32_bf16 v[66:69], v[176:179], v[216:219], v[66:69]
	v_mfma_f32_16x16x32_bf16 v[122:125], v[172:175], v[188:191], v[122:125]
	v_mfma_f32_16x16x32_bf16 v[114:117], v[180:183], v[188:191], v[114:117]
	v_mfma_f32_16x16x32_bf16 v[102:105], v[172:175], v[196:199], v[102:105]
	v_mfma_f32_16x16x32_bf16 v[98:101], v[180:183], v[196:199], v[98:101]
	v_mfma_f32_16x16x32_bf16 v[86:89], v[172:175], v[204:207], v[86:89]
	v_mfma_f32_16x16x32_bf16 v[82:85], v[180:183], v[204:207], v[82:85]
	v_mfma_f32_16x16x32_bf16 v[70:73], v[172:175], v[220:223], v[70:73]
	v_mfma_f32_16x16x32_bf16 v[66:69], v[180:183], v[220:223], v[66:69]
	s_barrier
	s_add_i32 s46, s50, s77
	v_lshl_add_u64 v[164:165], v[164:165], 0, s[56:57]
	s_mov_b32 m0, s46
	ds_read_b128 v[184:187], v147 offset:49152
	ds_read_b128 v[188:191], v147 offset:50176
	ds_read_b128 v[192:195], v147 offset:51200
	ds_read_b128 v[196:199], v147 offset:52224
	ds_read_b128 v[200:203], v147 offset:53248
	ds_read_b128 v[204:207], v147 offset:54272
	ds_read_b128 v[216:219], v147 offset:55296
	ds_read_b128 v[220:223], v147 offset:56320
	global_load_lds_dwordx4 v[164:165], off
	s_add_i32 m0, s46, 0x2000
	s_add_u32 s44, s44, 0x100080
	v_lshl_add_u64 v[164:165], v[208:209], 0, s[56:57]
	s_addc_u32 s45, s45, 0
	s_add_i32 s46, s64, s77
	global_load_lds_dwordx4 v[164:165], off
	s_mov_b32 m0, s46
	s_nop 0
	global_load_lds_dwordx4 v126, s[44:45]
	s_add_i32 m0, s46, 0x2000
	s_nop 0
	global_load_lds_dwordx4 v118, s[44:45]
	s_mov_b32 m0, s80
	v_lshl_add_u64 v[164:165], v[224:225], 0, s[56:57]
	global_load_lds_dwordx4 v[164:165], off
	s_mov_b32 m0, s81
	v_lshl_add_u64 v[164:165], v[242:243], 0, s[56:57]
	global_load_lds_dwordx4 v[164:165], off
	s_waitcnt vmcnt(8) lgkmcnt(0)
	s_barrier
	v_mfma_f32_16x16x32_bf16 v[62:65], v[148:151], v[184:187], v[62:65]
	v_mfma_f32_16x16x32_bf16 v[58:61], v[156:159], v[184:187], v[58:61]
	v_mfma_f32_16x16x32_bf16 v[46:49], v[148:151], v[192:195], v[46:49]
	v_mfma_f32_16x16x32_bf16 v[42:45], v[156:159], v[192:195], v[42:45]
	v_mfma_f32_16x16x32_bf16 v[30:33], v[148:151], v[200:203], v[30:33]
	v_mfma_f32_16x16x32_bf16 v[26:29], v[156:159], v[200:203], v[26:29]
	v_mfma_f32_16x16x32_bf16 v[14:17], v[148:151], v[216:219], v[14:17]
	v_mfma_f32_16x16x32_bf16 v[10:13], v[156:159], v[216:219], v[10:13]
	v_mfma_f32_16x16x32_bf16 v[62:65], v[152:155], v[188:191], v[62:65]
	v_mfma_f32_16x16x32_bf16 v[58:61], v[160:163], v[188:191], v[58:61]
	v_mfma_f32_16x16x32_bf16 v[46:49], v[152:155], v[196:199], v[46:49]
	v_mfma_f32_16x16x32_bf16 v[42:45], v[160:163], v[196:199], v[42:45]
	v_mfma_f32_16x16x32_bf16 v[30:33], v[152:155], v[204:207], v[30:33]
	v_mfma_f32_16x16x32_bf16 v[26:29], v[160:163], v[204:207], v[26:29]
	v_mfma_f32_16x16x32_bf16 v[14:17], v[152:155], v[220:223], v[14:17]
	v_mfma_f32_16x16x32_bf16 v[10:13], v[160:163], v[220:223], v[10:13]
	v_mfma_f32_16x16x32_bf16 v[54:57], v[168:171], v[184:187], v[54:57]
	v_mfma_f32_16x16x32_bf16 v[50:53], v[176:179], v[184:187], v[50:53]
	v_mfma_f32_16x16x32_bf16 v[38:41], v[168:171], v[192:195], v[38:41]
	v_mfma_f32_16x16x32_bf16 v[34:37], v[176:179], v[192:195], v[34:37]
	v_mfma_f32_16x16x32_bf16 v[22:25], v[168:171], v[200:203], v[22:25]
	v_mfma_f32_16x16x32_bf16 v[18:21], v[176:179], v[200:203], v[18:21]
	v_mfma_f32_16x16x32_bf16 v[6:9], v[168:171], v[216:219], v[6:9]
	v_mfma_f32_16x16x32_bf16 v[2:5], v[176:179], v[216:219], v[2:5]
	v_mfma_f32_16x16x32_bf16 v[54:57], v[172:175], v[188:191], v[54:57]
	v_mfma_f32_16x16x32_bf16 v[50:53], v[180:183], v[188:191], v[50:53]
	v_mfma_f32_16x16x32_bf16 v[38:41], v[172:175], v[196:199], v[38:41]
	v_mfma_f32_16x16x32_bf16 v[34:37], v[180:183], v[196:199], v[34:37]
	v_mfma_f32_16x16x32_bf16 v[22:25], v[172:175], v[204:207], v[22:25]
	v_mfma_f32_16x16x32_bf16 v[18:21], v[180:183], v[204:207], v[18:21]
	v_mfma_f32_16x16x32_bf16 v[6:9], v[172:175], v[220:223], v[6:9]
	v_mfma_f32_16x16x32_bf16 v[2:5], v[180:183], v[220:223], v[2:5]
	s_barrier
	s_add_i32 s85, s85, 2
	s_add_u32 s36, s36, 0x100
	s_addc_u32 s37, s37, 0
	s_cmp_gt_u32 s85, 61
	s_cbranch_scc0 .LBB0_2703
	s_add_u32 s36, s59, 0xffffff00
	s_addc_u32 s37, s82, -1
	s_andn2_b64 vcc, exec, s[42:43]
	s_cbranch_vccnz .LBB0_2706
	v_mov_b32_e32 v2, 0
	s_mov_b32 s12, s26
	s_mov_b32 s53, s28
	s_mov_b64 s[24:25], s[34:35]
	s_mov_b32 s68, s58
	v_mov_b32_e32 v3, v2
	v_mov_b32_e32 v4, v2
	v_mov_b32_e32 v5, v2
	v_mov_b32_e32 v6, v2
	v_mov_b32_e32 v7, v2
	v_mov_b32_e32 v8, v2
	v_mov_b32_e32 v9, v2
	v_mov_b32_e32 v18, v2
	v_mov_b32_e32 v19, v2
	v_mov_b32_e32 v20, v2
	v_mov_b32_e32 v21, v2
	v_mov_b32_e32 v22, v2
	v_mov_b32_e32 v23, v2
	v_mov_b32_e32 v24, v2
	v_mov_b32_e32 v25, v2
	v_mov_b32_e32 v34, v2
	v_mov_b32_e32 v35, v2
	v_mov_b32_e32 v36, v2
	v_mov_b32_e32 v37, v2
	v_mov_b32_e32 v38, v2
	v_mov_b32_e32 v39, v2
	v_mov_b32_e32 v40, v2
	v_mov_b32_e32 v41, v2
	v_mov_b32_e32 v50, v2
	v_mov_b32_e32 v51, v2
	v_mov_b32_e32 v52, v2
	v_mov_b32_e32 v53, v2
	v_mov_b32_e32 v54, v2
	v_mov_b32_e32 v55, v2
	v_mov_b32_e32 v56, v2
	v_mov_b32_e32 v57, v2
	v_mov_b32_e32 v10, v2
	v_mov_b32_e32 v11, v2
	v_mov_b32_e32 v12, v2
	v_mov_b32_e32 v13, v2
	v_mov_b32_e32 v14, v2
	v_mov_b32_e32 v15, v2
	v_mov_b32_e32 v16, v2
	v_mov_b32_e32 v17, v2
	v_mov_b32_e32 v26, v2
	v_mov_b32_e32 v27, v2
	v_mov_b32_e32 v28, v2
	v_mov_b32_e32 v29, v2
	v_mov_b32_e32 v30, v2
	v_mov_b32_e32 v31, v2
	v_mov_b32_e32 v32, v2
	v_mov_b32_e32 v33, v2
	v_mov_b32_e32 v42, v2
	v_mov_b32_e32 v43, v2
	v_mov_b32_e32 v44, v2
	v_mov_b32_e32 v45, v2
	v_mov_b32_e32 v46, v2
	v_mov_b32_e32 v47, v2
	v_mov_b32_e32 v48, v2
	v_mov_b32_e32 v49, v2
	v_mov_b32_e32 v58, v2
	v_mov_b32_e32 v59, v2
	v_mov_b32_e32 v60, v2
	v_mov_b32_e32 v61, v2
	v_mov_b32_e32 v62, v2
	v_mov_b32_e32 v63, v2
	v_mov_b32_e32 v64, v2
	v_mov_b32_e32 v65, v2
	v_mov_b32_e32 v66, v2
	v_mov_b32_e32 v67, v2
	v_mov_b32_e32 v68, v2
	v_mov_b32_e32 v69, v2
	v_mov_b32_e32 v70, v2
	v_mov_b32_e32 v71, v2
	v_mov_b32_e32 v72, v2
	v_mov_b32_e32 v73, v2
	v_mov_b32_e32 v82, v2
	v_mov_b32_e32 v83, v2
	v_mov_b32_e32 v84, v2
	v_mov_b32_e32 v85, v2
	v_mov_b32_e32 v86, v2
	v_mov_b32_e32 v87, v2
	v_mov_b32_e32 v88, v2
	v_mov_b32_e32 v89, v2
	v_mov_b32_e32 v98, v2
	v_mov_b32_e32 v99, v2
	v_mov_b32_e32 v100, v2
	v_mov_b32_e32 v101, v2
	v_mov_b32_e32 v102, v2
	v_mov_b32_e32 v103, v2
	v_mov_b32_e32 v104, v2
	v_mov_b32_e32 v105, v2
	v_mov_b32_e32 v114, v2
	v_mov_b32_e32 v115, v2
	v_mov_b32_e32 v116, v2
	v_mov_b32_e32 v117, v2
	v_mov_b32_e32 v122, v2
	v_mov_b32_e32 v123, v2
	v_mov_b32_e32 v124, v2
	v_mov_b32_e32 v125, v2
	v_mov_b32_e32 v74, v2
	v_mov_b32_e32 v75, v2
	v_mov_b32_e32 v76, v2
	v_mov_b32_e32 v77, v2
	v_mov_b32_e32 v78, v2
	v_mov_b32_e32 v79, v2
	v_mov_b32_e32 v80, v2
	v_mov_b32_e32 v81, v2
	v_mov_b32_e32 v90, v2
	v_mov_b32_e32 v91, v2
	v_mov_b32_e32 v92, v2
	v_mov_b32_e32 v93, v2
	v_mov_b32_e32 v94, v2
	v_mov_b32_e32 v95, v2
	v_mov_b32_e32 v96, v2
	v_mov_b32_e32 v97, v2
	v_mov_b32_e32 v106, v2
	v_mov_b32_e32 v107, v2
	v_mov_b32_e32 v108, v2
	v_mov_b32_e32 v109, v2
	v_mov_b32_e32 v110, v2
	v_mov_b32_e32 v111, v2
	v_mov_b32_e32 v112, v2
	v_mov_b32_e32 v113, v2
	v_mov_b32_e32 v130, v2
	v_mov_b32_e32 v131, v2
	v_mov_b32_e32 v132, v2
	v_mov_b32_e32 v133, v2
	v_mov_b32_e32 v134, v2
	v_mov_b32_e32 v135, v2
	v_mov_b32_e32 v136, v2
	v_mov_b32_e32 v137, v2
	s_movk_i32 s92, 0x2b20
	s_andn2_b64 vcc, exec, s[40:41]
	s_cbranch_vccnz .LBB0_2707
	s_branch .LBB0_2708

.LBB0_2795:
	s_add_u32 s59, s36, 0x100
	s_addc_u32 s81, s37, 0
	s_ashr_i32 s29, s28, 31
	s_lshl_b64 s[30:31], s[28:29], 21
	s_add_u32 s34, s53, s30
	s_addc_u32 s35, s62, s31
	s_and_b64 s[30:31], s[42:43], exec
	s_cselect_b32 s29, s35, s25
	s_cselect_b32 s82, s34, s24
	s_ashr_i32 s27, s26, 31
	s_lshl_b64 s[30:31], s[26:27], 21
	s_add_u32 s30, s63, s30
	s_addc_u32 s31, s70, s31
	s_and_b64 s[44:45], s[42:43], exec
	s_cselect_b32 s27, s31, s37
	s_cselect_b32 s83, s30, s36
	s_add_u32 s36, s24, 0x100080
	s_addc_u32 s37, s25, 0
	v_lshl_add_u64 v[142:143], s[36:37], 0, v[138:139]
	v_lshl_add_u64 v[144:145], s[36:37], 0, v[140:141]
	s_mov_b32 s84, -2
	s_mov_b64 s[36:37], 0
	v_add_u32_e32 v241, 0x10000, v146
.LBB0_2796:
	s_add_u32 s44, s24, s36
	s_addc_u32 s45, s25, s37
	s_add_u32 s44, s44, 0x100
	s_addc_u32 s45, s45, 0
	s_add_u32 s50, s59, s36
	s_addc_u32 s64, s81, s37
	s_add_i32 s65, 0, 0x10000
	s_cmpk_eq_i32 s36, 0x1f00
	s_cselect_b32 s47, s29, s45
	s_cselect_b32 s46, s82, s44
	s_cselect_b32 s45, s27, s64
	s_cselect_b32 s44, s83, s50
	s_add_i32 s50, 0, 0x14000
	ds_read_b128 v[148:151], v241
	ds_read_b128 v[152:155], v241 offset:1024
	ds_read_b128 v[156:159], v241 offset:2048
	ds_read_b128 v[160:163], v241 offset:3072
	ds_read_b128 v[168:171], v241 offset:16384
	ds_read_b128 v[172:175], v241 offset:17408
	ds_read_b128 v[176:179], v241 offset:18432
	ds_read_b128 v[180:183], v241 offset:19456
	v_lshl_add_u64 v[164:165], v[144:145], 0, s[36:37]
	s_add_i32 m0, s4, 0xc000
	ds_read_b128 v[184:187], v147
	ds_read_b128 v[188:191], v147 offset:1024
	ds_read_b128 v[192:195], v147 offset:2048
	ds_read_b128 v[196:199], v147 offset:3072
	ds_read_b128 v[200:203], v147 offset:4096
	ds_read_b128 v[204:207], v147 offset:5120
	ds_read_b128 v[216:219], v147 offset:6144
	ds_read_b128 v[220:223], v147 offset:7168
	global_load_lds_dwordx4 v[164:165], off
	s_add_i32 m0, s4, 0xe000
	v_lshl_add_u64 v[164:165], v[142:143], 0, s[36:37]
	global_load_lds_dwordx4 v[164:165], off
	s_waitcnt vmcnt(8) lgkmcnt(0)
	s_barrier
	v_mfma_f32_16x16x32_bf16 v[134:137], v[148:151], v[184:187], v[134:137]
	v_mfma_f32_16x16x32_bf16 v[130:133], v[156:159], v[184:187], v[130:133]
	v_mfma_f32_16x16x32_bf16 v[110:113], v[148:151], v[192:195], v[110:113]
	v_mfma_f32_16x16x32_bf16 v[106:109], v[156:159], v[192:195], v[106:109]
	v_mfma_f32_16x16x32_bf16 v[94:97], v[148:151], v[200:203], v[94:97]
	v_mfma_f32_16x16x32_bf16 v[90:93], v[156:159], v[200:203], v[90:93]
	v_mfma_f32_16x16x32_bf16 v[78:81], v[148:151], v[216:219], v[78:81]
	v_mfma_f32_16x16x32_bf16 v[74:77], v[156:159], v[216:219], v[74:77]
	v_mfma_f32_16x16x32_bf16 v[134:137], v[152:155], v[188:191], v[134:137]
	v_mfma_f32_16x16x32_bf16 v[130:133], v[160:163], v[188:191], v[130:133]
	v_mfma_f32_16x16x32_bf16 v[110:113], v[152:155], v[196:199], v[110:113]
	v_mfma_f32_16x16x32_bf16 v[106:109], v[160:163], v[196:199], v[106:109]
	v_mfma_f32_16x16x32_bf16 v[94:97], v[152:155], v[204:207], v[94:97]
	v_mfma_f32_16x16x32_bf16 v[90:93], v[160:163], v[204:207], v[90:93]
	v_mfma_f32_16x16x32_bf16 v[78:81], v[152:155], v[220:223], v[78:81]
	v_mfma_f32_16x16x32_bf16 v[74:77], v[160:163], v[220:223], v[74:77]
	v_mfma_f32_16x16x32_bf16 v[122:125], v[168:171], v[184:187], v[122:125]
	v_mfma_f32_16x16x32_bf16 v[114:117], v[176:179], v[184:187], v[114:117]
	v_mfma_f32_16x16x32_bf16 v[102:105], v[168:171], v[192:195], v[102:105]
	v_mfma_f32_16x16x32_bf16 v[98:101], v[176:179], v[192:195], v[98:101]
	v_mfma_f32_16x16x32_bf16 v[86:89], v[168:171], v[200:203], v[86:89]
	v_mfma_f32_16x16x32_bf16 v[82:85], v[176:179], v[200:203], v[82:85]
	v_mfma_f32_16x16x32_bf16 v[70:73], v[168:171], v[216:219], v[70:73]
	v_mfma_f32_16x16x32_bf16 v[66:69], v[176:179], v[216:219], v[66:69]
	v_mfma_f32_16x16x32_bf16 v[122:125], v[172:175], v[188:191], v[122:125]
	v_mfma_f32_16x16x32_bf16 v[114:117], v[180:183], v[188:191], v[114:117]
	v_mfma_f32_16x16x32_bf16 v[102:105], v[172:175], v[196:199], v[102:105]
	v_mfma_f32_16x16x32_bf16 v[98:101], v[180:183], v[196:199], v[98:101]
	v_mfma_f32_16x16x32_bf16 v[86:89], v[172:175], v[204:207], v[86:89]
	v_mfma_f32_16x16x32_bf16 v[82:85], v[180:183], v[204:207], v[82:85]
	v_mfma_f32_16x16x32_bf16 v[70:73], v[172:175], v[220:223], v[70:73]
	v_mfma_f32_16x16x32_bf16 v[66:69], v[180:183], v[220:223], v[66:69]
	s_barrier
	s_add_i32 s64, s65, s71
	v_lshl_add_u64 v[164:165], s[44:45], 0, v[126:127]
	s_mov_b32 m0, s64
	ds_read_b128 v[184:187], v147 offset:16384
	ds_read_b128 v[188:191], v147 offset:17408
	ds_read_b128 v[192:195], v147 offset:18432
	ds_read_b128 v[196:199], v147 offset:19456
	ds_read_b128 v[200:203], v147 offset:20480
	ds_read_b128 v[204:207], v147 offset:21504
	ds_read_b128 v[216:219], v147 offset:22528
	ds_read_b128 v[220:223], v147 offset:23552
	global_load_lds_dwordx4 v126, s[44:45]
	s_add_i32 m0, s64, 0x2000
	s_add_u32 s92, s44, 0x100000
	v_lshl_add_u64 v[208:209], s[44:45], 0, v[118:119]
	s_addc_u32 s93, s45, 0
	s_add_i32 s50, s50, s71
	global_load_lds_dwordx4 v118, s[44:45]
	s_mov_b32 m0, s50
	v_lshl_add_u64 v[242:243], s[46:47], 0, v[120:121]
	global_load_lds_dwordx4 v126, s[92:93]
	s_add_i32 m0, s50, 0x2000
	s_nop 0
	global_load_lds_dwordx4 v118, s[92:93]
	s_mov_b32 m0, s4
	v_lshl_add_u64 v[224:225], s[46:47], 0, v[128:129]
	global_load_lds_dwordx4 v128, s[46:47]
	s_mov_b32 m0, s33
	s_nop 0
	global_load_lds_dwordx4 v120, s[46:47]
	s_waitcnt vmcnt(8) lgkmcnt(0)
	s_barrier
	v_mfma_f32_16x16x32_bf16 v[62:65], v[148:151], v[184:187], v[62:65]
	v_mfma_f32_16x16x32_bf16 v[58:61], v[156:159], v[184:187], v[58:61]
	v_mfma_f32_16x16x32_bf16 v[46:49], v[148:151], v[192:195], v[46:49]
	v_mfma_f32_16x16x32_bf16 v[42:45], v[156:159], v[192:195], v[42:45]
	v_mfma_f32_16x16x32_bf16 v[30:33], v[148:151], v[200:203], v[30:33]
	v_mfma_f32_16x16x32_bf16 v[26:29], v[156:159], v[200:203], v[26:29]
	v_mfma_f32_16x16x32_bf16 v[14:17], v[148:151], v[216:219], v[14:17]
	v_mfma_f32_16x16x32_bf16 v[10:13], v[156:159], v[216:219], v[10:13]
	v_mfma_f32_16x16x32_bf16 v[62:65], v[152:155], v[188:191], v[62:65]
	v_mfma_f32_16x16x32_bf16 v[58:61], v[160:163], v[188:191], v[58:61]
	v_mfma_f32_16x16x32_bf16 v[46:49], v[152:155], v[196:199], v[46:49]
	v_mfma_f32_16x16x32_bf16 v[42:45], v[160:163], v[196:199], v[42:45]
	v_mfma_f32_16x16x32_bf16 v[30:33], v[152:155], v[204:207], v[30:33]
	v_mfma_f32_16x16x32_bf16 v[26:29], v[160:163], v[204:207], v[26:29]
	v_mfma_f32_16x16x32_bf16 v[14:17], v[152:155], v[220:223], v[14:17]
	v_mfma_f32_16x16x32_bf16 v[10:13], v[160:163], v[220:223], v[10:13]
	v_mfma_f32_16x16x32_bf16 v[54:57], v[168:171], v[184:187], v[54:57]
	v_mfma_f32_16x16x32_bf16 v[50:53], v[176:179], v[184:187], v[50:53]
	v_mfma_f32_16x16x32_bf16 v[38:41], v[168:171], v[192:195], v[38:41]
	v_mfma_f32_16x16x32_bf16 v[34:37], v[176:179], v[192:195], v[34:37]
	v_mfma_f32_16x16x32_bf16 v[22:25], v[168:171], v[200:203], v[22:25]
	v_mfma_f32_16x16x32_bf16 v[18:21], v[176:179], v[200:203], v[18:21]
	v_mfma_f32_16x16x32_bf16 v[6:9], v[168:171], v[216:219], v[6:9]
	v_mfma_f32_16x16x32_bf16 v[2:5], v[176:179], v[216:219], v[2:5]
	v_mfma_f32_16x16x32_bf16 v[54:57], v[172:175], v[188:191], v[54:57]
	v_mfma_f32_16x16x32_bf16 v[50:53], v[180:183], v[188:191], v[50:53]
	v_mfma_f32_16x16x32_bf16 v[38:41], v[172:175], v[196:199], v[38:41]
	v_mfma_f32_16x16x32_bf16 v[34:37], v[180:183], v[196:199], v[34:37]
	v_mfma_f32_16x16x32_bf16 v[22:25], v[172:175], v[204:207], v[22:25]
	v_mfma_f32_16x16x32_bf16 v[18:21], v[180:183], v[204:207], v[18:21]
	v_mfma_f32_16x16x32_bf16 v[6:9], v[172:175], v[220:223], v[6:9]
	v_mfma_f32_16x16x32_bf16 v[2:5], v[180:183], v[220:223], v[2:5]
	s_barrier
	s_add_i32 s50, 0, 0x18000
	s_add_i32 s64, 0, 0x1c000
	ds_read_b128 v[148:151], v241 offset:32768
	ds_read_b128 v[152:155], v241 offset:33792
	ds_read_b128 v[156:159], v241 offset:34816
	ds_read_b128 v[160:163], v241 offset:35840
	ds_read_b128 v[168:171], v241 offset:49152
	ds_read_b128 v[172:175], v241 offset:50176
	ds_read_b128 v[176:179], v241 offset:51200
	ds_read_b128 v[180:183], v241 offset:52224
	s_add_u32 s46, s46, 0x100000
	s_addc_u32 s47, s47, 0
	s_mov_b32 m0, s76
	ds_read_b128 v[184:187], v147 offset:32768
	ds_read_b128 v[188:191], v147 offset:33792
	ds_read_b128 v[192:195], v147 offset:34816
	ds_read_b128 v[196:199], v147 offset:35840
	ds_read_b128 v[200:203], v147 offset:36864
	ds_read_b128 v[204:207], v147 offset:37888
	ds_read_b128 v[216:219], v147 offset:38912
	ds_read_b128 v[220:223], v147 offset:39936
	global_load_lds_dwordx4 v128, s[46:47]
	s_mov_b32 m0, s77
	v_lshl_add_u64 v[244:245], s[46:47], 0, v[120:121]
	global_load_lds_dwordx4 v120, s[46:47]
	s_waitcnt vmcnt(8) lgkmcnt(0)
	s_barrier
	v_mfma_f32_16x16x32_bf16 v[134:137], v[148:151], v[184:187], v[134:137]
	v_mfma_f32_16x16x32_bf16 v[130:133], v[156:159], v[184:187], v[130:133]
	v_mfma_f32_16x16x32_bf16 v[110:113], v[148:151], v[192:195], v[110:113]
	v_mfma_f32_16x16x32_bf16 v[106:109], v[156:159], v[192:195], v[106:109]
	v_mfma_f32_16x16x32_bf16 v[94:97], v[148:151], v[200:203], v[94:97]
	v_mfma_f32_16x16x32_bf16 v[90:93], v[156:159], v[200:203], v[90:93]
	v_mfma_f32_16x16x32_bf16 v[78:81], v[148:151], v[216:219], v[78:81]
	v_mfma_f32_16x16x32_bf16 v[74:77], v[156:159], v[216:219], v[74:77]
	v_mfma_f32_16x16x32_bf16 v[134:137], v[152:155], v[188:191], v[134:137]
	v_mfma_f32_16x16x32_bf16 v[130:133], v[160:163], v[188:191], v[130:133]
	v_mfma_f32_16x16x32_bf16 v[110:113], v[152:155], v[196:199], v[110:113]
	v_mfma_f32_16x16x32_bf16 v[106:109], v[160:163], v[196:199], v[106:109]
	v_mfma_f32_16x16x32_bf16 v[94:97], v[152:155], v[204:207], v[94:97]
	v_mfma_f32_16x16x32_bf16 v[90:93], v[160:163], v[204:207], v[90:93]
	v_mfma_f32_16x16x32_bf16 v[78:81], v[152:155], v[220:223], v[78:81]
	v_mfma_f32_16x16x32_bf16 v[74:77], v[160:163], v[220:223], v[74:77]
	v_mfma_f32_16x16x32_bf16 v[122:125], v[168:171], v[184:187], v[122:125]
	v_mfma_f32_16x16x32_bf16 v[114:117], v[176:179], v[184:187], v[114:117]
	v_mfma_f32_16x16x32_bf16 v[102:105], v[168:171], v[192:195], v[102:105]
	v_mfma_f32_16x16x32_bf16 v[98:101], v[176:179], v[192:195], v[98:101]
	v_mfma_f32_16x16x32_bf16 v[86:89], v[168:171], v[200:203], v[86:89]
	v_mfma_f32_16x16x32_bf16 v[82:85], v[176:179], v[200:203], v[82:85]
	v_mfma_f32_16x16x32_bf16 v[70:73], v[168:171], v[216:219], v[70:73]
	v_mfma_f32_16x16x32_bf16 v[66:69], v[176:179], v[216:219], v[66:69]
	v_mfma_f32_16x16x32_bf16 v[122:125], v[172:175], v[188:191], v[122:125]
	v_mfma_f32_16x16x32_bf16 v[114:117], v[180:183], v[188:191], v[114:117]
	v_mfma_f32_16x16x32_bf16 v[102:105], v[172:175], v[196:199], v[102:105]
	v_mfma_f32_16x16x32_bf16 v[98:101], v[180:183], v[196:199], v[98:101]
	v_mfma_f32_16x16x32_bf16 v[86:89], v[172:175], v[204:207], v[86:89]
	v_mfma_f32_16x16x32_bf16 v[82:85], v[180:183], v[204:207], v[82:85]
	v_mfma_f32_16x16x32_bf16 v[70:73], v[172:175], v[220:223], v[70:73]
	v_mfma_f32_16x16x32_bf16 v[66:69], v[180:183], v[220:223], v[66:69]
	s_barrier
	s_add_i32 s46, s50, s71
	v_lshl_add_u64 v[164:165], v[164:165], 0, s[56:57]
	s_mov_b32 m0, s46
	ds_read_b128 v[184:187], v147 offset:49152
	ds_read_b128 v[188:191], v147 offset:50176
	ds_read_b128 v[192:195], v147 offset:51200
	ds_read_b128 v[196:199], v147 offset:52224
	ds_read_b128 v[200:203], v147 offset:53248
	ds_read_b128 v[204:207], v147 offset:54272
	ds_read_b128 v[216:219], v147 offset:55296
	ds_read_b128 v[220:223], v147 offset:56320
	global_load_lds_dwordx4 v[164:165], off
	s_add_i32 m0, s46, 0x2000
	s_add_u32 s44, s44, 0x100080
	v_lshl_add_u64 v[164:165], v[208:209], 0, s[56:57]
	s_addc_u32 s45, s45, 0
	s_add_i32 s46, s64, s71
	global_load_lds_dwordx4 v[164:165], off
	s_mov_b32 m0, s46
	s_nop 0
	global_load_lds_dwordx4 v126, s[44:45]
	s_add_i32 m0, s46, 0x2000
	s_nop 0
	global_load_lds_dwordx4 v118, s[44:45]
	s_mov_b32 m0, s78
	v_lshl_add_u64 v[164:165], v[224:225], 0, s[56:57]
	global_load_lds_dwordx4 v[164:165], off
	s_mov_b32 m0, s79
	v_lshl_add_u64 v[164:165], v[242:243], 0, s[56:57]
	global_load_lds_dwordx4 v[164:165], off
	s_waitcnt vmcnt(8) lgkmcnt(0)
	s_barrier
	v_mfma_f32_16x16x32_bf16 v[62:65], v[148:151], v[184:187], v[62:65]
	v_mfma_f32_16x16x32_bf16 v[58:61], v[156:159], v[184:187], v[58:61]
	v_mfma_f32_16x16x32_bf16 v[46:49], v[148:151], v[192:195], v[46:49]
	v_mfma_f32_16x16x32_bf16 v[42:45], v[156:159], v[192:195], v[42:45]
	v_mfma_f32_16x16x32_bf16 v[30:33], v[148:151], v[200:203], v[30:33]
	v_mfma_f32_16x16x32_bf16 v[26:29], v[156:159], v[200:203], v[26:29]
	v_mfma_f32_16x16x32_bf16 v[14:17], v[148:151], v[216:219], v[14:17]
	v_mfma_f32_16x16x32_bf16 v[10:13], v[156:159], v[216:219], v[10:13]
	v_mfma_f32_16x16x32_bf16 v[62:65], v[152:155], v[188:191], v[62:65]
	v_mfma_f32_16x16x32_bf16 v[58:61], v[160:163], v[188:191], v[58:61]
	v_mfma_f32_16x16x32_bf16 v[46:49], v[152:155], v[196:199], v[46:49]
	v_mfma_f32_16x16x32_bf16 v[42:45], v[160:163], v[196:199], v[42:45]
	v_mfma_f32_16x16x32_bf16 v[30:33], v[152:155], v[204:207], v[30:33]
	v_mfma_f32_16x16x32_bf16 v[26:29], v[160:163], v[204:207], v[26:29]
	v_mfma_f32_16x16x32_bf16 v[14:17], v[152:155], v[220:223], v[14:17]
	v_mfma_f32_16x16x32_bf16 v[10:13], v[160:163], v[220:223], v[10:13]
	v_mfma_f32_16x16x32_bf16 v[54:57], v[168:171], v[184:187], v[54:57]
	v_mfma_f32_16x16x32_bf16 v[50:53], v[176:179], v[184:187], v[50:53]
	v_mfma_f32_16x16x32_bf16 v[38:41], v[168:171], v[192:195], v[38:41]
	v_mfma_f32_16x16x32_bf16 v[34:37], v[176:179], v[192:195], v[34:37]
	v_mfma_f32_16x16x32_bf16 v[22:25], v[168:171], v[200:203], v[22:25]
	v_mfma_f32_16x16x32_bf16 v[18:21], v[176:179], v[200:203], v[18:21]
	v_mfma_f32_16x16x32_bf16 v[6:9], v[168:171], v[216:219], v[6:9]
	v_mfma_f32_16x16x32_bf16 v[2:5], v[176:179], v[216:219], v[2:5]
	v_mfma_f32_16x16x32_bf16 v[54:57], v[172:175], v[188:191], v[54:57]
	v_mfma_f32_16x16x32_bf16 v[50:53], v[180:183], v[188:191], v[50:53]
	v_mfma_f32_16x16x32_bf16 v[38:41], v[172:175], v[196:199], v[38:41]
	v_mfma_f32_16x16x32_bf16 v[34:37], v[180:183], v[196:199], v[34:37]
	v_mfma_f32_16x16x32_bf16 v[22:25], v[172:175], v[204:207], v[22:25]
	v_mfma_f32_16x16x32_bf16 v[18:21], v[180:183], v[204:207], v[18:21]
	v_mfma_f32_16x16x32_bf16 v[6:9], v[172:175], v[220:223], v[6:9]
	v_mfma_f32_16x16x32_bf16 v[2:5], v[180:183], v[220:223], v[2:5]
	s_barrier
	s_add_i32 s84, s84, 2
	s_add_u32 s36, s36, 0x100
	s_addc_u32 s37, s37, 0
	s_cmp_gt_u32 s84, 61
	s_cbranch_scc0 .LBB0_2796
	s_add_u32 s36, s59, 0xffffff00
	s_addc_u32 s37, s81, -1
	s_andn2_b64 vcc, exec, s[42:43]
	s_cbranch_vccnz .LBB0_2799
	v_mov_b32_e32 v2, 0
	s_mov_b32 s12, s26
	s_mov_b32 s80, s28
	s_mov_b64 s[24:25], s[34:35]
	s_mov_b32 s68, s58
	v_mov_b32_e32 v3, v2
	v_mov_b32_e32 v4, v2
	v_mov_b32_e32 v5, v2
	v_mov_b32_e32 v6, v2
	v_mov_b32_e32 v7, v2
	v_mov_b32_e32 v8, v2
	v_mov_b32_e32 v9, v2
	v_mov_b32_e32 v18, v2
	v_mov_b32_e32 v19, v2
	v_mov_b32_e32 v20, v2
	v_mov_b32_e32 v21, v2
	v_mov_b32_e32 v22, v2
	v_mov_b32_e32 v23, v2
	v_mov_b32_e32 v24, v2
	v_mov_b32_e32 v25, v2
	v_mov_b32_e32 v34, v2
	v_mov_b32_e32 v35, v2
	v_mov_b32_e32 v36, v2
	v_mov_b32_e32 v37, v2
	v_mov_b32_e32 v38, v2
	v_mov_b32_e32 v39, v2
	v_mov_b32_e32 v40, v2
	v_mov_b32_e32 v41, v2
	v_mov_b32_e32 v50, v2
	v_mov_b32_e32 v51, v2
	v_mov_b32_e32 v52, v2
	v_mov_b32_e32 v53, v2
	v_mov_b32_e32 v54, v2
	v_mov_b32_e32 v55, v2
	v_mov_b32_e32 v56, v2
	v_mov_b32_e32 v57, v2
	v_mov_b32_e32 v10, v2
	v_mov_b32_e32 v11, v2
	v_mov_b32_e32 v12, v2
	v_mov_b32_e32 v13, v2
	v_mov_b32_e32 v14, v2
	v_mov_b32_e32 v15, v2
	v_mov_b32_e32 v16, v2
	v_mov_b32_e32 v17, v2
	v_mov_b32_e32 v26, v2
	v_mov_b32_e32 v27, v2
	v_mov_b32_e32 v28, v2
	v_mov_b32_e32 v29, v2
	v_mov_b32_e32 v30, v2
	v_mov_b32_e32 v31, v2
	v_mov_b32_e32 v32, v2
	v_mov_b32_e32 v33, v2
	v_mov_b32_e32 v42, v2
	v_mov_b32_e32 v43, v2
	v_mov_b32_e32 v44, v2
	v_mov_b32_e32 v45, v2
	v_mov_b32_e32 v46, v2
	v_mov_b32_e32 v47, v2
	v_mov_b32_e32 v48, v2
	v_mov_b32_e32 v49, v2
	v_mov_b32_e32 v58, v2
	v_mov_b32_e32 v59, v2
	v_mov_b32_e32 v60, v2
	v_mov_b32_e32 v61, v2
	v_mov_b32_e32 v62, v2
	v_mov_b32_e32 v63, v2
	v_mov_b32_e32 v64, v2
	v_mov_b32_e32 v65, v2
	v_mov_b32_e32 v66, v2
	v_mov_b32_e32 v67, v2
	v_mov_b32_e32 v68, v2
	v_mov_b32_e32 v69, v2
	v_mov_b32_e32 v70, v2
	v_mov_b32_e32 v71, v2
	v_mov_b32_e32 v72, v2
	v_mov_b32_e32 v73, v2
	v_mov_b32_e32 v82, v2
	v_mov_b32_e32 v83, v2
	v_mov_b32_e32 v84, v2
	v_mov_b32_e32 v85, v2
	v_mov_b32_e32 v86, v2
	v_mov_b32_e32 v87, v2
	v_mov_b32_e32 v88, v2
	v_mov_b32_e32 v89, v2
	v_mov_b32_e32 v98, v2
	v_mov_b32_e32 v99, v2
	v_mov_b32_e32 v100, v2
	v_mov_b32_e32 v101, v2
	v_mov_b32_e32 v102, v2
	v_mov_b32_e32 v103, v2
	v_mov_b32_e32 v104, v2
	v_mov_b32_e32 v105, v2
	v_mov_b32_e32 v114, v2
	v_mov_b32_e32 v115, v2
	v_mov_b32_e32 v116, v2
	v_mov_b32_e32 v117, v2
	v_mov_b32_e32 v122, v2
	v_mov_b32_e32 v123, v2
	v_mov_b32_e32 v124, v2
	v_mov_b32_e32 v125, v2
	v_mov_b32_e32 v74, v2
	v_mov_b32_e32 v75, v2
	v_mov_b32_e32 v76, v2
	v_mov_b32_e32 v77, v2
	v_mov_b32_e32 v78, v2
	v_mov_b32_e32 v79, v2
	v_mov_b32_e32 v80, v2
	v_mov_b32_e32 v81, v2
	v_mov_b32_e32 v90, v2
	v_mov_b32_e32 v91, v2
	v_mov_b32_e32 v92, v2
	v_mov_b32_e32 v93, v2
	v_mov_b32_e32 v94, v2
	v_mov_b32_e32 v95, v2
	v_mov_b32_e32 v96, v2
	v_mov_b32_e32 v97, v2
	v_mov_b32_e32 v106, v2
	v_mov_b32_e32 v107, v2
	v_mov_b32_e32 v108, v2
	v_mov_b32_e32 v109, v2
	v_mov_b32_e32 v110, v2
	v_mov_b32_e32 v111, v2
	v_mov_b32_e32 v112, v2
	v_mov_b32_e32 v113, v2
	v_mov_b32_e32 v130, v2
	v_mov_b32_e32 v131, v2
	v_mov_b32_e32 v132, v2
	v_mov_b32_e32 v133, v2
	v_mov_b32_e32 v134, v2
	v_mov_b32_e32 v135, v2
	v_mov_b32_e32 v136, v2
	v_mov_b32_e32 v137, v2
	s_movk_i32 s92, 0x2b20
	s_andn2_b64 vcc, exec, s[40:41]
	s_cbranch_vccnz .LBB0_2800
	s_branch .LBB0_2801

.LBB0_2890:
	s_add_u32 s59, s36, 0x100
	s_addc_u32 s81, s37, 0
	s_ashr_i32 s29, s28, 31
	s_lshl_b64 s[30:31], s[28:29], 21
	s_add_u32 s34, s62, s30
	s_addc_u32 s35, s63, s31
	s_and_b64 s[30:31], s[42:43], exec
	s_cselect_b32 s29, s35, s25
	s_cselect_b32 s82, s34, s24
	s_ashr_i32 s27, s26, 31
	s_lshl_b64 s[30:31], s[26:27], 21
	s_add_u32 s30, s70, s30
	s_addc_u32 s31, s71, s31
	s_and_b64 s[44:45], s[42:43], exec
	s_cselect_b32 s27, s31, s37
	s_cselect_b32 s83, s30, s36
	s_add_u32 s36, s24, 0x100080
	s_addc_u32 s37, s25, 0
	v_lshl_add_u64 v[142:143], s[36:37], 0, v[138:139]
	v_lshl_add_u64 v[144:145], s[36:37], 0, v[140:141]
	s_mov_b32 s84, -2
	s_mov_b64 s[36:37], 0
	v_add_u32_e32 v225, 0x10000, v146
.LBB0_2891:
	s_add_u32 s44, s24, s36
	s_addc_u32 s45, s25, s37
	s_add_u32 s44, s44, 0x100
	s_addc_u32 s45, s45, 0
	s_add_u32 s50, s59, s36
	s_addc_u32 s64, s81, s37
	s_add_i32 s65, 0, 0x10000
	s_cmpk_eq_i32 s36, 0x1f00
	s_cselect_b32 s47, s29, s45
	s_cselect_b32 s46, s82, s44
	s_cselect_b32 s45, s27, s64
	s_cselect_b32 s44, s83, s50
	s_add_i32 s50, 0, 0x14000
	ds_read_b128 v[148:151], v225
	ds_read_b128 v[152:155], v225 offset:1024
	ds_read_b128 v[156:159], v225 offset:2048
	ds_read_b128 v[160:163], v225 offset:3072
	ds_read_b128 v[168:171], v225 offset:16384
	ds_read_b128 v[172:175], v225 offset:17408
	ds_read_b128 v[176:179], v225 offset:18432
	ds_read_b128 v[180:183], v225 offset:19456
	v_lshl_add_u64 v[164:165], v[144:145], 0, s[36:37]
	s_add_i32 m0, s4, 0xc000
	ds_read_b128 v[184:187], v147
	ds_read_b128 v[188:191], v147 offset:1024
	ds_read_b128 v[192:195], v147 offset:2048
	ds_read_b128 v[196:199], v147 offset:3072
	ds_read_b128 v[200:203], v147 offset:4096
	ds_read_b128 v[204:207], v147 offset:5120
	ds_read_b128 v[216:219], v147 offset:6144
	ds_read_b128 v[220:223], v147 offset:7168
	global_load_lds_dwordx4 v[164:165], off
	s_add_i32 m0, s4, 0xe000
	v_lshl_add_u64 v[164:165], v[142:143], 0, s[36:37]
	global_load_lds_dwordx4 v[164:165], off
	s_waitcnt vmcnt(8) lgkmcnt(0)
	s_barrier
	v_mfma_f32_16x16x32_bf16 v[134:137], v[148:151], v[184:187], v[134:137]
	v_mfma_f32_16x16x32_bf16 v[130:133], v[156:159], v[184:187], v[130:133]
	v_mfma_f32_16x16x32_bf16 v[110:113], v[148:151], v[192:195], v[110:113]
	v_mfma_f32_16x16x32_bf16 v[106:109], v[156:159], v[192:195], v[106:109]
	v_mfma_f32_16x16x32_bf16 v[94:97], v[148:151], v[200:203], v[94:97]
	v_mfma_f32_16x16x32_bf16 v[90:93], v[156:159], v[200:203], v[90:93]
	v_mfma_f32_16x16x32_bf16 v[78:81], v[148:151], v[216:219], v[78:81]
	v_mfma_f32_16x16x32_bf16 v[74:77], v[156:159], v[216:219], v[74:77]
	v_mfma_f32_16x16x32_bf16 v[134:137], v[152:155], v[188:191], v[134:137]
	v_mfma_f32_16x16x32_bf16 v[130:133], v[160:163], v[188:191], v[130:133]
	v_mfma_f32_16x16x32_bf16 v[110:113], v[152:155], v[196:199], v[110:113]
	v_mfma_f32_16x16x32_bf16 v[106:109], v[160:163], v[196:199], v[106:109]
	v_mfma_f32_16x16x32_bf16 v[94:97], v[152:155], v[204:207], v[94:97]
	v_mfma_f32_16x16x32_bf16 v[90:93], v[160:163], v[204:207], v[90:93]
	v_mfma_f32_16x16x32_bf16 v[78:81], v[152:155], v[220:223], v[78:81]
	v_mfma_f32_16x16x32_bf16 v[74:77], v[160:163], v[220:223], v[74:77]
	v_mfma_f32_16x16x32_bf16 v[118:121], v[168:171], v[184:187], v[118:121]
	v_mfma_f32_16x16x32_bf16 v[114:117], v[176:179], v[184:187], v[114:117]
	v_mfma_f32_16x16x32_bf16 v[102:105], v[168:171], v[192:195], v[102:105]
	v_mfma_f32_16x16x32_bf16 v[98:101], v[176:179], v[192:195], v[98:101]
	v_mfma_f32_16x16x32_bf16 v[86:89], v[168:171], v[200:203], v[86:89]
	v_mfma_f32_16x16x32_bf16 v[82:85], v[176:179], v[200:203], v[82:85]
	v_mfma_f32_16x16x32_bf16 v[70:73], v[168:171], v[216:219], v[70:73]
	v_mfma_f32_16x16x32_bf16 v[66:69], v[176:179], v[216:219], v[66:69]
	v_mfma_f32_16x16x32_bf16 v[118:121], v[172:175], v[188:191], v[118:121]
	v_mfma_f32_16x16x32_bf16 v[114:117], v[180:183], v[188:191], v[114:117]
	v_mfma_f32_16x16x32_bf16 v[102:105], v[172:175], v[196:199], v[102:105]
	v_mfma_f32_16x16x32_bf16 v[98:101], v[180:183], v[196:199], v[98:101]
	v_mfma_f32_16x16x32_bf16 v[86:89], v[172:175], v[204:207], v[86:89]
	v_mfma_f32_16x16x32_bf16 v[82:85], v[180:183], v[204:207], v[82:85]
	v_mfma_f32_16x16x32_bf16 v[70:73], v[172:175], v[220:223], v[70:73]
	v_mfma_f32_16x16x32_bf16 v[66:69], v[180:183], v[220:223], v[66:69]
	s_barrier
	s_add_i32 s64, s65, s76
	v_lshl_add_u64 v[164:165], s[44:45], 0, v[126:127]
	s_mov_b32 m0, s64
	ds_read_b128 v[184:187], v147 offset:16384
	ds_read_b128 v[188:191], v147 offset:17408
	ds_read_b128 v[192:195], v147 offset:18432
	ds_read_b128 v[196:199], v147 offset:19456
	ds_read_b128 v[200:203], v147 offset:20480
	ds_read_b128 v[204:207], v147 offset:21504
	ds_read_b128 v[216:219], v147 offset:22528
	ds_read_b128 v[220:223], v147 offset:23552
	global_load_lds_dwordx4 v126, s[44:45]
	s_add_i32 m0, s64, 0x2000
	s_add_u32 s92, s44, 0x100000
	v_lshl_add_u64 v[208:209], s[44:45], 0, v[122:123]
	s_addc_u32 s93, s45, 0
	s_add_i32 s50, s50, s76
	global_load_lds_dwordx4 v122, s[44:45]
	s_mov_b32 m0, s50
	v_lshl_add_u64 v[242:243], s[46:47], 0, v[124:125]
	global_load_lds_dwordx4 v126, s[92:93]
	s_add_i32 m0, s50, 0x2000
	s_nop 0
	global_load_lds_dwordx4 v122, s[92:93]
	s_mov_b32 m0, s4
	v_lshl_add_u64 v[240:241], s[46:47], 0, v[128:129]
	global_load_lds_dwordx4 v128, s[46:47]
	s_mov_b32 m0, s33
	s_nop 0
	global_load_lds_dwordx4 v124, s[46:47]
	s_waitcnt vmcnt(8) lgkmcnt(0)
	s_barrier
	v_mfma_f32_16x16x32_bf16 v[62:65], v[148:151], v[184:187], v[62:65]
	v_mfma_f32_16x16x32_bf16 v[58:61], v[156:159], v[184:187], v[58:61]
	v_mfma_f32_16x16x32_bf16 v[46:49], v[148:151], v[192:195], v[46:49]
	v_mfma_f32_16x16x32_bf16 v[42:45], v[156:159], v[192:195], v[42:45]
	v_mfma_f32_16x16x32_bf16 v[30:33], v[148:151], v[200:203], v[30:33]
	v_mfma_f32_16x16x32_bf16 v[26:29], v[156:159], v[200:203], v[26:29]
	v_mfma_f32_16x16x32_bf16 v[14:17], v[148:151], v[216:219], v[14:17]
	v_mfma_f32_16x16x32_bf16 v[10:13], v[156:159], v[216:219], v[10:13]
	v_mfma_f32_16x16x32_bf16 v[62:65], v[152:155], v[188:191], v[62:65]
	v_mfma_f32_16x16x32_bf16 v[58:61], v[160:163], v[188:191], v[58:61]
	v_mfma_f32_16x16x32_bf16 v[46:49], v[152:155], v[196:199], v[46:49]
	v_mfma_f32_16x16x32_bf16 v[42:45], v[160:163], v[196:199], v[42:45]
	v_mfma_f32_16x16x32_bf16 v[30:33], v[152:155], v[204:207], v[30:33]
	v_mfma_f32_16x16x32_bf16 v[26:29], v[160:163], v[204:207], v[26:29]
	v_mfma_f32_16x16x32_bf16 v[14:17], v[152:155], v[220:223], v[14:17]
	v_mfma_f32_16x16x32_bf16 v[10:13], v[160:163], v[220:223], v[10:13]
	v_mfma_f32_16x16x32_bf16 v[54:57], v[168:171], v[184:187], v[54:57]
	v_mfma_f32_16x16x32_bf16 v[50:53], v[176:179], v[184:187], v[50:53]
	v_mfma_f32_16x16x32_bf16 v[38:41], v[168:171], v[192:195], v[38:41]
	v_mfma_f32_16x16x32_bf16 v[34:37], v[176:179], v[192:195], v[34:37]
	v_mfma_f32_16x16x32_bf16 v[22:25], v[168:171], v[200:203], v[22:25]
	v_mfma_f32_16x16x32_bf16 v[18:21], v[176:179], v[200:203], v[18:21]
	v_mfma_f32_16x16x32_bf16 v[6:9], v[168:171], v[216:219], v[6:9]
	v_mfma_f32_16x16x32_bf16 v[2:5], v[176:179], v[216:219], v[2:5]
	v_mfma_f32_16x16x32_bf16 v[54:57], v[172:175], v[188:191], v[54:57]
	v_mfma_f32_16x16x32_bf16 v[50:53], v[180:183], v[188:191], v[50:53]
	v_mfma_f32_16x16x32_bf16 v[38:41], v[172:175], v[196:199], v[38:41]
	v_mfma_f32_16x16x32_bf16 v[34:37], v[180:183], v[196:199], v[34:37]
	v_mfma_f32_16x16x32_bf16 v[22:25], v[172:175], v[204:207], v[22:25]
	v_mfma_f32_16x16x32_bf16 v[18:21], v[180:183], v[204:207], v[18:21]
	v_mfma_f32_16x16x32_bf16 v[6:9], v[172:175], v[220:223], v[6:9]
	v_mfma_f32_16x16x32_bf16 v[2:5], v[180:183], v[220:223], v[2:5]
	s_barrier
	s_add_i32 s50, 0, 0x18000
	s_add_i32 s64, 0, 0x1c000
	ds_read_b128 v[148:151], v225 offset:32768
	ds_read_b128 v[152:155], v225 offset:33792
	ds_read_b128 v[156:159], v225 offset:34816
	ds_read_b128 v[160:163], v225 offset:35840
	ds_read_b128 v[168:171], v225 offset:49152
	ds_read_b128 v[172:175], v225 offset:50176
	ds_read_b128 v[176:179], v225 offset:51200
	ds_read_b128 v[180:183], v225 offset:52224
	s_add_u32 s46, s46, 0x100000
	s_addc_u32 s47, s47, 0
	s_mov_b32 m0, s77
	ds_read_b128 v[184:187], v147 offset:32768
	ds_read_b128 v[188:191], v147 offset:33792
	ds_read_b128 v[192:195], v147 offset:34816
	ds_read_b128 v[196:199], v147 offset:35840
	ds_read_b128 v[200:203], v147 offset:36864
	ds_read_b128 v[204:207], v147 offset:37888
	ds_read_b128 v[216:219], v147 offset:38912
	ds_read_b128 v[220:223], v147 offset:39936
	global_load_lds_dwordx4 v128, s[46:47]
	s_mov_b32 m0, s78
	v_lshl_add_u64 v[244:245], s[46:47], 0, v[124:125]
	global_load_lds_dwordx4 v124, s[46:47]
	s_waitcnt vmcnt(8) lgkmcnt(0)
	s_barrier
	v_mfma_f32_16x16x32_bf16 v[134:137], v[148:151], v[184:187], v[134:137]
	v_mfma_f32_16x16x32_bf16 v[130:133], v[156:159], v[184:187], v[130:133]
	v_mfma_f32_16x16x32_bf16 v[110:113], v[148:151], v[192:195], v[110:113]
	v_mfma_f32_16x16x32_bf16 v[106:109], v[156:159], v[192:195], v[106:109]
	v_mfma_f32_16x16x32_bf16 v[94:97], v[148:151], v[200:203], v[94:97]
	v_mfma_f32_16x16x32_bf16 v[90:93], v[156:159], v[200:203], v[90:93]
	v_mfma_f32_16x16x32_bf16 v[78:81], v[148:151], v[216:219], v[78:81]
	v_mfma_f32_16x16x32_bf16 v[74:77], v[156:159], v[216:219], v[74:77]
	v_mfma_f32_16x16x32_bf16 v[134:137], v[152:155], v[188:191], v[134:137]
	v_mfma_f32_16x16x32_bf16 v[130:133], v[160:163], v[188:191], v[130:133]
	v_mfma_f32_16x16x32_bf16 v[110:113], v[152:155], v[196:199], v[110:113]
	v_mfma_f32_16x16x32_bf16 v[106:109], v[160:163], v[196:199], v[106:109]
	v_mfma_f32_16x16x32_bf16 v[94:97], v[152:155], v[204:207], v[94:97]
	v_mfma_f32_16x16x32_bf16 v[90:93], v[160:163], v[204:207], v[90:93]
	v_mfma_f32_16x16x32_bf16 v[78:81], v[152:155], v[220:223], v[78:81]
	v_mfma_f32_16x16x32_bf16 v[74:77], v[160:163], v[220:223], v[74:77]
	v_mfma_f32_16x16x32_bf16 v[118:121], v[168:171], v[184:187], v[118:121]
	v_mfma_f32_16x16x32_bf16 v[114:117], v[176:179], v[184:187], v[114:117]
	v_mfma_f32_16x16x32_bf16 v[102:105], v[168:171], v[192:195], v[102:105]
	v_mfma_f32_16x16x32_bf16 v[98:101], v[176:179], v[192:195], v[98:101]
	v_mfma_f32_16x16x32_bf16 v[86:89], v[168:171], v[200:203], v[86:89]
	v_mfma_f32_16x16x32_bf16 v[82:85], v[176:179], v[200:203], v[82:85]
	v_mfma_f32_16x16x32_bf16 v[70:73], v[168:171], v[216:219], v[70:73]
	v_mfma_f32_16x16x32_bf16 v[66:69], v[176:179], v[216:219], v[66:69]
	v_mfma_f32_16x16x32_bf16 v[118:121], v[172:175], v[188:191], v[118:121]
	v_mfma_f32_16x16x32_bf16 v[114:117], v[180:183], v[188:191], v[114:117]
	v_mfma_f32_16x16x32_bf16 v[102:105], v[172:175], v[196:199], v[102:105]
	v_mfma_f32_16x16x32_bf16 v[98:101], v[180:183], v[196:199], v[98:101]
	v_mfma_f32_16x16x32_bf16 v[86:89], v[172:175], v[204:207], v[86:89]
	v_mfma_f32_16x16x32_bf16 v[82:85], v[180:183], v[204:207], v[82:85]
	v_mfma_f32_16x16x32_bf16 v[70:73], v[172:175], v[220:223], v[70:73]
	v_mfma_f32_16x16x32_bf16 v[66:69], v[180:183], v[220:223], v[66:69]
	s_barrier
	s_add_i32 s46, s50, s76
	v_lshl_add_u64 v[164:165], v[164:165], 0, s[56:57]
	s_mov_b32 m0, s46
	ds_read_b128 v[184:187], v147 offset:49152
	ds_read_b128 v[188:191], v147 offset:50176
	ds_read_b128 v[192:195], v147 offset:51200
	ds_read_b128 v[196:199], v147 offset:52224
	ds_read_b128 v[200:203], v147 offset:53248
	ds_read_b128 v[204:207], v147 offset:54272
	ds_read_b128 v[216:219], v147 offset:55296
	ds_read_b128 v[220:223], v147 offset:56320
	global_load_lds_dwordx4 v[164:165], off
	s_add_i32 m0, s46, 0x2000
	s_add_u32 s44, s44, 0x100080
	v_lshl_add_u64 v[164:165], v[208:209], 0, s[56:57]
	s_addc_u32 s45, s45, 0
	s_add_i32 s46, s64, s76
	global_load_lds_dwordx4 v[164:165], off
	s_mov_b32 m0, s46
	s_nop 0
	global_load_lds_dwordx4 v126, s[44:45]
	s_add_i32 m0, s46, 0x2000
	s_nop 0
	global_load_lds_dwordx4 v122, s[44:45]
	s_mov_b32 m0, s79
	v_lshl_add_u64 v[164:165], v[240:241], 0, s[56:57]
	global_load_lds_dwordx4 v[164:165], off
	s_mov_b32 m0, s80
	v_lshl_add_u64 v[164:165], v[242:243], 0, s[56:57]
	global_load_lds_dwordx4 v[164:165], off
	s_waitcnt vmcnt(8) lgkmcnt(0)
	s_barrier
	v_mfma_f32_16x16x32_bf16 v[62:65], v[148:151], v[184:187], v[62:65]
	v_mfma_f32_16x16x32_bf16 v[58:61], v[156:159], v[184:187], v[58:61]
	v_mfma_f32_16x16x32_bf16 v[46:49], v[148:151], v[192:195], v[46:49]
	v_mfma_f32_16x16x32_bf16 v[42:45], v[156:159], v[192:195], v[42:45]
	v_mfma_f32_16x16x32_bf16 v[30:33], v[148:151], v[200:203], v[30:33]
	v_mfma_f32_16x16x32_bf16 v[26:29], v[156:159], v[200:203], v[26:29]
	v_mfma_f32_16x16x32_bf16 v[14:17], v[148:151], v[216:219], v[14:17]
	v_mfma_f32_16x16x32_bf16 v[10:13], v[156:159], v[216:219], v[10:13]
	v_mfma_f32_16x16x32_bf16 v[62:65], v[152:155], v[188:191], v[62:65]
	v_mfma_f32_16x16x32_bf16 v[58:61], v[160:163], v[188:191], v[58:61]
	v_mfma_f32_16x16x32_bf16 v[46:49], v[152:155], v[196:199], v[46:49]
	v_mfma_f32_16x16x32_bf16 v[42:45], v[160:163], v[196:199], v[42:45]
	v_mfma_f32_16x16x32_bf16 v[30:33], v[152:155], v[204:207], v[30:33]
	v_mfma_f32_16x16x32_bf16 v[26:29], v[160:163], v[204:207], v[26:29]
	v_mfma_f32_16x16x32_bf16 v[14:17], v[152:155], v[220:223], v[14:17]
	v_mfma_f32_16x16x32_bf16 v[10:13], v[160:163], v[220:223], v[10:13]
	v_mfma_f32_16x16x32_bf16 v[54:57], v[168:171], v[184:187], v[54:57]
	v_mfma_f32_16x16x32_bf16 v[50:53], v[176:179], v[184:187], v[50:53]
	v_mfma_f32_16x16x32_bf16 v[38:41], v[168:171], v[192:195], v[38:41]
	v_mfma_f32_16x16x32_bf16 v[34:37], v[176:179], v[192:195], v[34:37]
	v_mfma_f32_16x16x32_bf16 v[22:25], v[168:171], v[200:203], v[22:25]
	v_mfma_f32_16x16x32_bf16 v[18:21], v[176:179], v[200:203], v[18:21]
	v_mfma_f32_16x16x32_bf16 v[6:9], v[168:171], v[216:219], v[6:9]
	v_mfma_f32_16x16x32_bf16 v[2:5], v[176:179], v[216:219], v[2:5]
	v_mfma_f32_16x16x32_bf16 v[54:57], v[172:175], v[188:191], v[54:57]
	v_mfma_f32_16x16x32_bf16 v[50:53], v[180:183], v[188:191], v[50:53]
	v_mfma_f32_16x16x32_bf16 v[38:41], v[172:175], v[196:199], v[38:41]
	v_mfma_f32_16x16x32_bf16 v[34:37], v[180:183], v[196:199], v[34:37]
	v_mfma_f32_16x16x32_bf16 v[22:25], v[172:175], v[204:207], v[22:25]
	v_mfma_f32_16x16x32_bf16 v[18:21], v[180:183], v[204:207], v[18:21]
	v_mfma_f32_16x16x32_bf16 v[6:9], v[172:175], v[220:223], v[6:9]
	v_mfma_f32_16x16x32_bf16 v[2:5], v[180:183], v[220:223], v[2:5]
	s_barrier
	s_add_i32 s84, s84, 2
	s_add_u32 s36, s36, 0x100
	s_addc_u32 s37, s37, 0
	s_cmp_gt_u32 s84, 61
	s_cbranch_scc0 .LBB0_2891
	s_add_u32 s36, s59, 0xffffff00
	s_addc_u32 s37, s81, -1
	s_andn2_b64 vcc, exec, s[42:43]
	s_cbranch_vccnz .LBB0_2894
	v_mov_b32_e32 v2, 0
	s_mov_b32 s20, s26
	s_mov_b32 s52, s28
	s_mov_b64 s[24:25], s[34:35]
	s_mov_b32 s68, s58
	v_mov_b32_e32 v3, v2
	v_mov_b32_e32 v4, v2
	v_mov_b32_e32 v5, v2
	v_mov_b32_e32 v6, v2
	v_mov_b32_e32 v7, v2
	v_mov_b32_e32 v8, v2
	v_mov_b32_e32 v9, v2
	v_mov_b32_e32 v18, v2
	v_mov_b32_e32 v19, v2
	v_mov_b32_e32 v20, v2
	v_mov_b32_e32 v21, v2
	v_mov_b32_e32 v22, v2
	v_mov_b32_e32 v23, v2
	v_mov_b32_e32 v24, v2
	v_mov_b32_e32 v25, v2
	v_mov_b32_e32 v34, v2
	v_mov_b32_e32 v35, v2
	v_mov_b32_e32 v36, v2
	v_mov_b32_e32 v37, v2
	v_mov_b32_e32 v38, v2
	v_mov_b32_e32 v39, v2
	v_mov_b32_e32 v40, v2
	v_mov_b32_e32 v41, v2
	v_mov_b32_e32 v50, v2
	v_mov_b32_e32 v51, v2
	v_mov_b32_e32 v52, v2
	v_mov_b32_e32 v53, v2
	v_mov_b32_e32 v54, v2
	v_mov_b32_e32 v55, v2
	v_mov_b32_e32 v56, v2
	v_mov_b32_e32 v57, v2
	v_mov_b32_e32 v10, v2
	v_mov_b32_e32 v11, v2
	v_mov_b32_e32 v12, v2
	v_mov_b32_e32 v13, v2
	v_mov_b32_e32 v14, v2
	v_mov_b32_e32 v15, v2
	v_mov_b32_e32 v16, v2
	v_mov_b32_e32 v17, v2
	v_mov_b32_e32 v26, v2
	v_mov_b32_e32 v27, v2
	v_mov_b32_e32 v28, v2
	v_mov_b32_e32 v29, v2
	v_mov_b32_e32 v30, v2
	v_mov_b32_e32 v31, v2
	v_mov_b32_e32 v32, v2
	v_mov_b32_e32 v33, v2
	v_mov_b32_e32 v42, v2
	v_mov_b32_e32 v43, v2
	v_mov_b32_e32 v44, v2
	v_mov_b32_e32 v45, v2
	v_mov_b32_e32 v46, v2
	v_mov_b32_e32 v47, v2
	v_mov_b32_e32 v48, v2
	v_mov_b32_e32 v49, v2
	v_mov_b32_e32 v58, v2
	v_mov_b32_e32 v59, v2
	v_mov_b32_e32 v60, v2
	v_mov_b32_e32 v61, v2
	v_mov_b32_e32 v62, v2
	v_mov_b32_e32 v63, v2
	v_mov_b32_e32 v64, v2
	v_mov_b32_e32 v65, v2
	v_mov_b32_e32 v66, v2
	v_mov_b32_e32 v67, v2
	v_mov_b32_e32 v68, v2
	v_mov_b32_e32 v69, v2
	v_mov_b32_e32 v70, v2
	v_mov_b32_e32 v71, v2
	v_mov_b32_e32 v72, v2
	v_mov_b32_e32 v73, v2
	v_mov_b32_e32 v82, v2
	v_mov_b32_e32 v83, v2
	v_mov_b32_e32 v84, v2
	v_mov_b32_e32 v85, v2
	v_mov_b32_e32 v86, v2
	v_mov_b32_e32 v87, v2
	v_mov_b32_e32 v88, v2
	v_mov_b32_e32 v89, v2
	v_mov_b32_e32 v98, v2
	v_mov_b32_e32 v99, v2
	v_mov_b32_e32 v100, v2
	v_mov_b32_e32 v101, v2
	v_mov_b32_e32 v102, v2
	v_mov_b32_e32 v103, v2
	v_mov_b32_e32 v104, v2
	v_mov_b32_e32 v105, v2
	v_mov_b32_e32 v114, v2
	v_mov_b32_e32 v115, v2
	v_mov_b32_e32 v116, v2
	v_mov_b32_e32 v117, v2
	v_mov_b32_e32 v118, v2
	v_mov_b32_e32 v119, v2
	v_mov_b32_e32 v120, v2
	v_mov_b32_e32 v121, v2
	v_mov_b32_e32 v74, v2
	v_mov_b32_e32 v75, v2
	v_mov_b32_e32 v76, v2
	v_mov_b32_e32 v77, v2
	v_mov_b32_e32 v78, v2
	v_mov_b32_e32 v79, v2
	v_mov_b32_e32 v80, v2
	v_mov_b32_e32 v81, v2
	v_mov_b32_e32 v90, v2
	v_mov_b32_e32 v91, v2
	v_mov_b32_e32 v92, v2
	v_mov_b32_e32 v93, v2
	v_mov_b32_e32 v94, v2
	v_mov_b32_e32 v95, v2
	v_mov_b32_e32 v96, v2
	v_mov_b32_e32 v97, v2
	v_mov_b32_e32 v106, v2
	v_mov_b32_e32 v107, v2
	v_mov_b32_e32 v108, v2
	v_mov_b32_e32 v109, v2
	v_mov_b32_e32 v110, v2
	v_mov_b32_e32 v111, v2
	v_mov_b32_e32 v112, v2
	v_mov_b32_e32 v113, v2
	v_mov_b32_e32 v130, v2
	v_mov_b32_e32 v131, v2
	v_mov_b32_e32 v132, v2
	v_mov_b32_e32 v133, v2
	v_mov_b32_e32 v134, v2
	v_mov_b32_e32 v135, v2
	v_mov_b32_e32 v136, v2
	v_mov_b32_e32 v137, v2
	s_movk_i32 s92, 0x2b20
	s_andn2_b64 vcc, exec, s[40:41]
	s_cbranch_vccnz .LBB0_2895
	s_branch .LBB0_2896

.LBB0_2981:
	s_add_u32 s59, s36, 0x100
	s_addc_u32 s79, s37, 0
	s_ashr_i32 s29, s28, 31
	s_lshl_b64 s[30:31], s[28:29], 21
	s_add_u32 s34, s49, s30
	s_addc_u32 s35, s52, s31
	s_and_b64 s[30:31], s[40:41], exec
	s_cselect_b32 s29, s35, s25
	s_cselect_b32 s80, s34, s24
	s_ashr_i32 s27, s26, 31
	s_lshl_b64 s[30:31], s[26:27], 21
	s_add_u32 s30, s53, s30
	s_addc_u32 s31, s62, s31
	s_and_b64 s[42:43], s[40:41], exec
	s_cselect_b32 s27, s31, s37
	s_cselect_b32 s81, s30, s36
	s_add_u32 s36, s24, 0x100080
	s_addc_u32 s37, s25, 0
	v_lshl_add_u64 v[142:143], s[36:37], 0, v[138:139]
	v_lshl_add_u64 v[144:145], s[36:37], 0, v[140:141]
	s_mov_b32 s82, -2
	s_mov_b64 s[36:37], 0
	v_add_u32_e32 v225, 0x10000, v146
.LBB0_2982:
	s_add_u32 s42, s24, s36
	s_addc_u32 s43, s25, s37
	s_add_u32 s42, s42, 0x100
	s_addc_u32 s43, s43, 0
	s_add_u32 s50, s59, s36
	s_addc_u32 s64, s79, s37
	s_add_i32 s65, 0, 0x10000
	s_cmpk_eq_i32 s36, 0x1f00
	s_cselect_b32 s45, s29, s43
	s_cselect_b32 s44, s80, s42
	s_cselect_b32 s43, s27, s64
	s_cselect_b32 s42, s81, s50
	s_add_i32 s50, 0, 0x14000
	ds_read_b128 v[148:151], v225
	ds_read_b128 v[152:155], v225 offset:1024
	ds_read_b128 v[156:159], v225 offset:2048
	ds_read_b128 v[160:163], v225 offset:3072
	ds_read_b128 v[164:167], v225 offset:16384
	ds_read_b128 v[168:171], v225 offset:17408
	ds_read_b128 v[172:175], v225 offset:18432
	ds_read_b128 v[176:179], v225 offset:19456
	v_lshl_add_u64 v[208:209], v[144:145], 0, s[36:37]
	s_add_i32 m0, s4, 0xc000
	ds_read_b128 v[180:183], v147
	ds_read_b128 v[184:187], v147 offset:1024
	ds_read_b128 v[188:191], v147 offset:2048
	ds_read_b128 v[192:195], v147 offset:3072
	ds_read_b128 v[196:199], v147 offset:4096
	ds_read_b128 v[200:203], v147 offset:5120
	ds_read_b128 v[204:207], v147 offset:6144
	ds_read_b128 v[216:219], v147 offset:7168
	global_load_lds_dwordx4 v[208:209], off
	s_add_i32 m0, s4, 0xe000
	v_lshl_add_u64 v[208:209], v[142:143], 0, s[36:37]
	global_load_lds_dwordx4 v[208:209], off
	s_waitcnt vmcnt(8) lgkmcnt(0)
	s_barrier
	v_mfma_f32_16x16x32_bf16 v[134:137], v[148:151], v[180:183], v[134:137]
	v_mfma_f32_16x16x32_bf16 v[130:133], v[156:159], v[180:183], v[130:133]
	v_mfma_f32_16x16x32_bf16 v[110:113], v[148:151], v[188:191], v[110:113]
	v_mfma_f32_16x16x32_bf16 v[106:109], v[156:159], v[188:191], v[106:109]
	v_mfma_f32_16x16x32_bf16 v[94:97], v[148:151], v[196:199], v[94:97]
	v_mfma_f32_16x16x32_bf16 v[90:93], v[156:159], v[196:199], v[90:93]
	v_mfma_f32_16x16x32_bf16 v[78:81], v[148:151], v[204:207], v[78:81]
	v_mfma_f32_16x16x32_bf16 v[74:77], v[156:159], v[204:207], v[74:77]
	v_mfma_f32_16x16x32_bf16 v[134:137], v[152:155], v[184:187], v[134:137]
	v_mfma_f32_16x16x32_bf16 v[130:133], v[160:163], v[184:187], v[130:133]
	v_mfma_f32_16x16x32_bf16 v[110:113], v[152:155], v[192:195], v[110:113]
	v_mfma_f32_16x16x32_bf16 v[106:109], v[160:163], v[192:195], v[106:109]
	v_mfma_f32_16x16x32_bf16 v[94:97], v[152:155], v[200:203], v[94:97]
	v_mfma_f32_16x16x32_bf16 v[90:93], v[160:163], v[200:203], v[90:93]
	v_mfma_f32_16x16x32_bf16 v[78:81], v[152:155], v[216:219], v[78:81]
	v_mfma_f32_16x16x32_bf16 v[74:77], v[160:163], v[216:219], v[74:77]
	v_mfma_f32_16x16x32_bf16 v[118:121], v[164:167], v[180:183], v[118:121]
	v_mfma_f32_16x16x32_bf16 v[114:117], v[172:175], v[180:183], v[114:117]
	v_mfma_f32_16x16x32_bf16 v[102:105], v[164:167], v[188:191], v[102:105]
	v_mfma_f32_16x16x32_bf16 v[98:101], v[172:175], v[188:191], v[98:101]
	v_mfma_f32_16x16x32_bf16 v[86:89], v[164:167], v[196:199], v[86:89]
	v_mfma_f32_16x16x32_bf16 v[82:85], v[172:175], v[196:199], v[82:85]
	v_mfma_f32_16x16x32_bf16 v[70:73], v[164:167], v[204:207], v[70:73]
	v_mfma_f32_16x16x32_bf16 v[66:69], v[172:175], v[204:207], v[66:69]
	v_mfma_f32_16x16x32_bf16 v[118:121], v[168:171], v[184:187], v[118:121]
	v_mfma_f32_16x16x32_bf16 v[114:117], v[176:179], v[184:187], v[114:117]
	v_mfma_f32_16x16x32_bf16 v[102:105], v[168:171], v[192:195], v[102:105]
	v_mfma_f32_16x16x32_bf16 v[98:101], v[176:179], v[192:195], v[98:101]
	v_mfma_f32_16x16x32_bf16 v[86:89], v[168:171], v[200:203], v[86:89]
	v_mfma_f32_16x16x32_bf16 v[82:85], v[176:179], v[200:203], v[82:85]
	v_mfma_f32_16x16x32_bf16 v[70:73], v[168:171], v[216:219], v[70:73]
	v_mfma_f32_16x16x32_bf16 v[66:69], v[176:179], v[216:219], v[66:69]
	s_barrier
	s_add_i32 s64, s65, s63
	v_lshl_add_u64 v[208:209], s[42:43], 0, v[126:127]
	s_mov_b32 m0, s64
	ds_read_b128 v[180:183], v147 offset:16384
	ds_read_b128 v[184:187], v147 offset:17408
	ds_read_b128 v[188:191], v147 offset:18432
	ds_read_b128 v[192:195], v147 offset:19456
	ds_read_b128 v[196:199], v147 offset:20480
	ds_read_b128 v[200:203], v147 offset:21504
	ds_read_b128 v[204:207], v147 offset:22528
	ds_read_b128 v[216:219], v147 offset:23552
	global_load_lds_dwordx4 v126, s[42:43]
	s_add_i32 m0, s64, 0x2000
	s_add_u32 s84, s42, 0x100000
	v_lshl_add_u64 v[220:221], s[42:43], 0, v[122:123]
	s_addc_u32 s85, s43, 0
	s_add_i32 s50, s50, s63
	global_load_lds_dwordx4 v122, s[42:43]
	s_mov_b32 m0, s50
	v_lshl_add_u64 v[240:241], s[44:45], 0, v[124:125]
	global_load_lds_dwordx4 v126, s[84:85]
	s_add_i32 m0, s50, 0x2000
	s_nop 0
	global_load_lds_dwordx4 v122, s[84:85]
	s_mov_b32 m0, s4
	v_lshl_add_u64 v[222:223], s[44:45], 0, v[128:129]
	global_load_lds_dwordx4 v128, s[44:45]
	s_mov_b32 m0, s33
	s_nop 0
	global_load_lds_dwordx4 v124, s[44:45]
	s_waitcnt vmcnt(8) lgkmcnt(0)
	s_barrier
	v_mfma_f32_16x16x32_bf16 v[62:65], v[148:151], v[180:183], v[62:65]
	v_mfma_f32_16x16x32_bf16 v[58:61], v[156:159], v[180:183], v[58:61]
	v_mfma_f32_16x16x32_bf16 v[46:49], v[148:151], v[188:191], v[46:49]
	v_mfma_f32_16x16x32_bf16 v[42:45], v[156:159], v[188:191], v[42:45]
	v_mfma_f32_16x16x32_bf16 v[30:33], v[148:151], v[196:199], v[30:33]
	v_mfma_f32_16x16x32_bf16 v[26:29], v[156:159], v[196:199], v[26:29]
	v_mfma_f32_16x16x32_bf16 v[14:17], v[148:151], v[204:207], v[14:17]
	v_mfma_f32_16x16x32_bf16 v[10:13], v[156:159], v[204:207], v[10:13]
	v_mfma_f32_16x16x32_bf16 v[62:65], v[152:155], v[184:187], v[62:65]
	v_mfma_f32_16x16x32_bf16 v[58:61], v[160:163], v[184:187], v[58:61]
	v_mfma_f32_16x16x32_bf16 v[46:49], v[152:155], v[192:195], v[46:49]
	v_mfma_f32_16x16x32_bf16 v[42:45], v[160:163], v[192:195], v[42:45]
	v_mfma_f32_16x16x32_bf16 v[30:33], v[152:155], v[200:203], v[30:33]
	v_mfma_f32_16x16x32_bf16 v[26:29], v[160:163], v[200:203], v[26:29]
	v_mfma_f32_16x16x32_bf16 v[14:17], v[152:155], v[216:219], v[14:17]
	v_mfma_f32_16x16x32_bf16 v[10:13], v[160:163], v[216:219], v[10:13]
	v_mfma_f32_16x16x32_bf16 v[54:57], v[164:167], v[180:183], v[54:57]
	v_mfma_f32_16x16x32_bf16 v[50:53], v[172:175], v[180:183], v[50:53]
	v_mfma_f32_16x16x32_bf16 v[38:41], v[164:167], v[188:191], v[38:41]
	v_mfma_f32_16x16x32_bf16 v[34:37], v[172:175], v[188:191], v[34:37]
	v_mfma_f32_16x16x32_bf16 v[22:25], v[164:167], v[196:199], v[22:25]
	v_mfma_f32_16x16x32_bf16 v[18:21], v[172:175], v[196:199], v[18:21]
	v_mfma_f32_16x16x32_bf16 v[6:9], v[164:167], v[204:207], v[6:9]
	v_mfma_f32_16x16x32_bf16 v[2:5], v[172:175], v[204:207], v[2:5]
	v_mfma_f32_16x16x32_bf16 v[54:57], v[168:171], v[184:187], v[54:57]
	v_mfma_f32_16x16x32_bf16 v[50:53], v[176:179], v[184:187], v[50:53]
	v_mfma_f32_16x16x32_bf16 v[38:41], v[168:171], v[192:195], v[38:41]
	v_mfma_f32_16x16x32_bf16 v[34:37], v[176:179], v[192:195], v[34:37]
	v_mfma_f32_16x16x32_bf16 v[22:25], v[168:171], v[200:203], v[22:25]
	v_mfma_f32_16x16x32_bf16 v[18:21], v[176:179], v[200:203], v[18:21]
	v_mfma_f32_16x16x32_bf16 v[6:9], v[168:171], v[216:219], v[6:9]
	v_mfma_f32_16x16x32_bf16 v[2:5], v[176:179], v[216:219], v[2:5]
	s_barrier
	s_add_i32 s50, 0, 0x18000
	s_add_i32 s64, 0, 0x1c000
	ds_read_b128 v[148:151], v225 offset:32768
	ds_read_b128 v[152:155], v225 offset:33792
	ds_read_b128 v[156:159], v225 offset:34816
	ds_read_b128 v[160:163], v225 offset:35840
	ds_read_b128 v[164:167], v225 offset:49152
	ds_read_b128 v[168:171], v225 offset:50176
	ds_read_b128 v[172:175], v225 offset:51200
	ds_read_b128 v[176:179], v225 offset:52224
	s_add_u32 s44, s44, 0x100000
	s_addc_u32 s45, s45, 0
	s_mov_b32 m0, s70
	ds_read_b128 v[180:183], v147 offset:32768
	ds_read_b128 v[184:187], v147 offset:33792
	ds_read_b128 v[188:191], v147 offset:34816
	ds_read_b128 v[192:195], v147 offset:35840
	ds_read_b128 v[196:199], v147 offset:36864
	ds_read_b128 v[200:203], v147 offset:37888
	ds_read_b128 v[204:207], v147 offset:38912
	ds_read_b128 v[216:219], v147 offset:39936
	global_load_lds_dwordx4 v128, s[44:45]
	s_mov_b32 m0, s71
	v_lshl_add_u64 v[242:243], s[44:45], 0, v[124:125]
	global_load_lds_dwordx4 v124, s[44:45]
	s_waitcnt vmcnt(8) lgkmcnt(0)
	s_barrier
	v_mfma_f32_16x16x32_bf16 v[134:137], v[148:151], v[180:183], v[134:137]
	v_mfma_f32_16x16x32_bf16 v[130:133], v[156:159], v[180:183], v[130:133]
	v_mfma_f32_16x16x32_bf16 v[110:113], v[148:151], v[188:191], v[110:113]
	v_mfma_f32_16x16x32_bf16 v[106:109], v[156:159], v[188:191], v[106:109]
	v_mfma_f32_16x16x32_bf16 v[94:97], v[148:151], v[196:199], v[94:97]
	v_mfma_f32_16x16x32_bf16 v[90:93], v[156:159], v[196:199], v[90:93]
	v_mfma_f32_16x16x32_bf16 v[78:81], v[148:151], v[204:207], v[78:81]
	v_mfma_f32_16x16x32_bf16 v[74:77], v[156:159], v[204:207], v[74:77]
	v_mfma_f32_16x16x32_bf16 v[134:137], v[152:155], v[184:187], v[134:137]
	v_mfma_f32_16x16x32_bf16 v[130:133], v[160:163], v[184:187], v[130:133]
	v_mfma_f32_16x16x32_bf16 v[110:113], v[152:155], v[192:195], v[110:113]
	v_mfma_f32_16x16x32_bf16 v[106:109], v[160:163], v[192:195], v[106:109]
	v_mfma_f32_16x16x32_bf16 v[94:97], v[152:155], v[200:203], v[94:97]
	v_mfma_f32_16x16x32_bf16 v[90:93], v[160:163], v[200:203], v[90:93]
	v_mfma_f32_16x16x32_bf16 v[78:81], v[152:155], v[216:219], v[78:81]
	v_mfma_f32_16x16x32_bf16 v[74:77], v[160:163], v[216:219], v[74:77]
	v_mfma_f32_16x16x32_bf16 v[118:121], v[164:167], v[180:183], v[118:121]
	v_mfma_f32_16x16x32_bf16 v[114:117], v[172:175], v[180:183], v[114:117]
	v_mfma_f32_16x16x32_bf16 v[102:105], v[164:167], v[188:191], v[102:105]
	v_mfma_f32_16x16x32_bf16 v[98:101], v[172:175], v[188:191], v[98:101]
	v_mfma_f32_16x16x32_bf16 v[86:89], v[164:167], v[196:199], v[86:89]
	v_mfma_f32_16x16x32_bf16 v[82:85], v[172:175], v[196:199], v[82:85]
	v_mfma_f32_16x16x32_bf16 v[70:73], v[164:167], v[204:207], v[70:73]
	v_mfma_f32_16x16x32_bf16 v[66:69], v[172:175], v[204:207], v[66:69]
	v_mfma_f32_16x16x32_bf16 v[118:121], v[168:171], v[184:187], v[118:121]
	v_mfma_f32_16x16x32_bf16 v[114:117], v[176:179], v[184:187], v[114:117]
	v_mfma_f32_16x16x32_bf16 v[102:105], v[168:171], v[192:195], v[102:105]
	v_mfma_f32_16x16x32_bf16 v[98:101], v[176:179], v[192:195], v[98:101]
	v_mfma_f32_16x16x32_bf16 v[86:89], v[168:171], v[200:203], v[86:89]
	v_mfma_f32_16x16x32_bf16 v[82:85], v[176:179], v[200:203], v[82:85]
	v_mfma_f32_16x16x32_bf16 v[70:73], v[168:171], v[216:219], v[70:73]
	v_mfma_f32_16x16x32_bf16 v[66:69], v[176:179], v[216:219], v[66:69]
	s_barrier
	s_add_i32 s44, s50, s63
	v_lshl_add_u64 v[208:209], v[208:209], 0, s[56:57]
	s_mov_b32 m0, s44
	ds_read_b128 v[180:183], v147 offset:49152
	ds_read_b128 v[184:187], v147 offset:50176
	ds_read_b128 v[188:191], v147 offset:51200
	ds_read_b128 v[192:195], v147 offset:52224
	ds_read_b128 v[196:199], v147 offset:53248
	ds_read_b128 v[200:203], v147 offset:54272
	ds_read_b128 v[204:207], v147 offset:55296
	ds_read_b128 v[216:219], v147 offset:56320
	global_load_lds_dwordx4 v[208:209], off
	s_add_i32 m0, s44, 0x2000
	s_add_u32 s42, s42, 0x100080
	v_lshl_add_u64 v[208:209], v[220:221], 0, s[56:57]
	s_addc_u32 s43, s43, 0
	s_add_i32 s44, s64, s63
	global_load_lds_dwordx4 v[208:209], off
	s_mov_b32 m0, s44
	s_nop 0
	global_load_lds_dwordx4 v126, s[42:43]
	s_add_i32 m0, s44, 0x2000
	s_nop 0
	global_load_lds_dwordx4 v122, s[42:43]
	s_mov_b32 m0, s76
	v_lshl_add_u64 v[208:209], v[222:223], 0, s[56:57]
	global_load_lds_dwordx4 v[208:209], off
	s_mov_b32 m0, s77
	v_lshl_add_u64 v[208:209], v[240:241], 0, s[56:57]
	global_load_lds_dwordx4 v[208:209], off
	s_waitcnt vmcnt(8) lgkmcnt(0)
	s_barrier
	v_mfma_f32_16x16x32_bf16 v[62:65], v[148:151], v[180:183], v[62:65]
	v_mfma_f32_16x16x32_bf16 v[58:61], v[156:159], v[180:183], v[58:61]
	v_mfma_f32_16x16x32_bf16 v[46:49], v[148:151], v[188:191], v[46:49]
	v_mfma_f32_16x16x32_bf16 v[42:45], v[156:159], v[188:191], v[42:45]
	v_mfma_f32_16x16x32_bf16 v[30:33], v[148:151], v[196:199], v[30:33]
	v_mfma_f32_16x16x32_bf16 v[26:29], v[156:159], v[196:199], v[26:29]
	v_mfma_f32_16x16x32_bf16 v[14:17], v[148:151], v[204:207], v[14:17]
	v_mfma_f32_16x16x32_bf16 v[10:13], v[156:159], v[204:207], v[10:13]
	v_mfma_f32_16x16x32_bf16 v[62:65], v[152:155], v[184:187], v[62:65]
	v_mfma_f32_16x16x32_bf16 v[58:61], v[160:163], v[184:187], v[58:61]
	v_mfma_f32_16x16x32_bf16 v[46:49], v[152:155], v[192:195], v[46:49]
	v_mfma_f32_16x16x32_bf16 v[42:45], v[160:163], v[192:195], v[42:45]
	v_mfma_f32_16x16x32_bf16 v[30:33], v[152:155], v[200:203], v[30:33]
	v_mfma_f32_16x16x32_bf16 v[26:29], v[160:163], v[200:203], v[26:29]
	v_mfma_f32_16x16x32_bf16 v[14:17], v[152:155], v[216:219], v[14:17]
	v_mfma_f32_16x16x32_bf16 v[10:13], v[160:163], v[216:219], v[10:13]
	v_mfma_f32_16x16x32_bf16 v[54:57], v[164:167], v[180:183], v[54:57]
	v_mfma_f32_16x16x32_bf16 v[50:53], v[172:175], v[180:183], v[50:53]
	v_mfma_f32_16x16x32_bf16 v[38:41], v[164:167], v[188:191], v[38:41]
	v_mfma_f32_16x16x32_bf16 v[34:37], v[172:175], v[188:191], v[34:37]
	v_mfma_f32_16x16x32_bf16 v[22:25], v[164:167], v[196:199], v[22:25]
	v_mfma_f32_16x16x32_bf16 v[18:21], v[172:175], v[196:199], v[18:21]
	v_mfma_f32_16x16x32_bf16 v[6:9], v[164:167], v[204:207], v[6:9]
	v_mfma_f32_16x16x32_bf16 v[2:5], v[172:175], v[204:207], v[2:5]
	v_mfma_f32_16x16x32_bf16 v[54:57], v[168:171], v[184:187], v[54:57]
	v_mfma_f32_16x16x32_bf16 v[50:53], v[176:179], v[184:187], v[50:53]
	v_mfma_f32_16x16x32_bf16 v[38:41], v[168:171], v[192:195], v[38:41]
	v_mfma_f32_16x16x32_bf16 v[34:37], v[176:179], v[192:195], v[34:37]
	v_mfma_f32_16x16x32_bf16 v[22:25], v[168:171], v[200:203], v[22:25]
	v_mfma_f32_16x16x32_bf16 v[18:21], v[176:179], v[200:203], v[18:21]
	v_mfma_f32_16x16x32_bf16 v[6:9], v[168:171], v[216:219], v[6:9]
	v_mfma_f32_16x16x32_bf16 v[2:5], v[176:179], v[216:219], v[2:5]
	s_barrier
	s_add_i32 s82, s82, 2
	s_add_u32 s36, s36, 0x100
	s_addc_u32 s37, s37, 0
	s_cmp_gt_u32 s82, 61
	s_cbranch_scc0 .LBB0_2982
	s_add_u32 s36, s59, 0xffffff00
	s_addc_u32 s37, s79, -1
	s_andn2_b64 vcc, exec, s[40:41]
	s_cbranch_vccnz .LBB0_2985
	v_mov_b32_e32 v2, 0
	s_mov_b32 s20, s26
	s_mov_b32 s78, s28
	s_mov_b64 s[24:25], s[34:35]
	s_mov_b32 s68, s58
	v_mov_b32_e32 v3, v2
	v_mov_b32_e32 v4, v2
	v_mov_b32_e32 v5, v2
	v_mov_b32_e32 v6, v2
	v_mov_b32_e32 v7, v2
	v_mov_b32_e32 v8, v2
	v_mov_b32_e32 v9, v2
	v_mov_b32_e32 v18, v2
	v_mov_b32_e32 v19, v2
	v_mov_b32_e32 v20, v2
	v_mov_b32_e32 v21, v2
	v_mov_b32_e32 v22, v2
	v_mov_b32_e32 v23, v2
	v_mov_b32_e32 v24, v2
	v_mov_b32_e32 v25, v2
	v_mov_b32_e32 v34, v2
	v_mov_b32_e32 v35, v2
	v_mov_b32_e32 v36, v2
	v_mov_b32_e32 v37, v2
	v_mov_b32_e32 v38, v2
	v_mov_b32_e32 v39, v2
	v_mov_b32_e32 v40, v2
	v_mov_b32_e32 v41, v2
	v_mov_b32_e32 v50, v2
	v_mov_b32_e32 v51, v2
	v_mov_b32_e32 v52, v2
	v_mov_b32_e32 v53, v2
	v_mov_b32_e32 v54, v2
	v_mov_b32_e32 v55, v2
	v_mov_b32_e32 v56, v2
	v_mov_b32_e32 v57, v2
	v_mov_b32_e32 v10, v2
	v_mov_b32_e32 v11, v2
	v_mov_b32_e32 v12, v2
	v_mov_b32_e32 v13, v2
	v_mov_b32_e32 v14, v2
	v_mov_b32_e32 v15, v2
	v_mov_b32_e32 v16, v2
	v_mov_b32_e32 v17, v2
	v_mov_b32_e32 v26, v2
	v_mov_b32_e32 v27, v2
	v_mov_b32_e32 v28, v2
	v_mov_b32_e32 v29, v2
	v_mov_b32_e32 v30, v2
	v_mov_b32_e32 v31, v2
	v_mov_b32_e32 v32, v2
	v_mov_b32_e32 v33, v2
	v_mov_b32_e32 v42, v2
	v_mov_b32_e32 v43, v2
	v_mov_b32_e32 v44, v2
	v_mov_b32_e32 v45, v2
	v_mov_b32_e32 v46, v2
	v_mov_b32_e32 v47, v2
	v_mov_b32_e32 v48, v2
	v_mov_b32_e32 v49, v2
	v_mov_b32_e32 v58, v2
	v_mov_b32_e32 v59, v2
	v_mov_b32_e32 v60, v2
	v_mov_b32_e32 v61, v2
	v_mov_b32_e32 v62, v2
	v_mov_b32_e32 v63, v2
	v_mov_b32_e32 v64, v2
	v_mov_b32_e32 v65, v2
	v_mov_b32_e32 v66, v2
	v_mov_b32_e32 v67, v2
	v_mov_b32_e32 v68, v2
	v_mov_b32_e32 v69, v2
	v_mov_b32_e32 v70, v2
	v_mov_b32_e32 v71, v2
	v_mov_b32_e32 v72, v2
	v_mov_b32_e32 v73, v2
	v_mov_b32_e32 v82, v2
	v_mov_b32_e32 v83, v2
	v_mov_b32_e32 v84, v2
	v_mov_b32_e32 v85, v2
	v_mov_b32_e32 v86, v2
	v_mov_b32_e32 v87, v2
	v_mov_b32_e32 v88, v2
	v_mov_b32_e32 v89, v2
	v_mov_b32_e32 v98, v2
	v_mov_b32_e32 v99, v2
	v_mov_b32_e32 v100, v2
	v_mov_b32_e32 v101, v2
	v_mov_b32_e32 v102, v2
	v_mov_b32_e32 v103, v2
	v_mov_b32_e32 v104, v2
	v_mov_b32_e32 v105, v2
	v_mov_b32_e32 v114, v2
	v_mov_b32_e32 v115, v2
	v_mov_b32_e32 v116, v2
	v_mov_b32_e32 v117, v2
	v_mov_b32_e32 v118, v2
	v_mov_b32_e32 v119, v2
	v_mov_b32_e32 v120, v2
	v_mov_b32_e32 v121, v2
	v_mov_b32_e32 v74, v2
	v_mov_b32_e32 v75, v2
	v_mov_b32_e32 v76, v2
	v_mov_b32_e32 v77, v2
	v_mov_b32_e32 v78, v2
	v_mov_b32_e32 v79, v2
	v_mov_b32_e32 v80, v2
	v_mov_b32_e32 v81, v2
	v_mov_b32_e32 v90, v2
	v_mov_b32_e32 v91, v2
	v_mov_b32_e32 v92, v2
	v_mov_b32_e32 v93, v2
	v_mov_b32_e32 v94, v2
	v_mov_b32_e32 v95, v2
	v_mov_b32_e32 v96, v2
	v_mov_b32_e32 v97, v2
	v_mov_b32_e32 v106, v2
	v_mov_b32_e32 v107, v2
	v_mov_b32_e32 v108, v2
	v_mov_b32_e32 v109, v2
	v_mov_b32_e32 v110, v2
	v_mov_b32_e32 v111, v2
	v_mov_b32_e32 v112, v2
	v_mov_b32_e32 v113, v2
	v_mov_b32_e32 v130, v2
	v_mov_b32_e32 v131, v2
	v_mov_b32_e32 v132, v2
	v_mov_b32_e32 v133, v2
	v_mov_b32_e32 v134, v2
	v_mov_b32_e32 v135, v2
	v_mov_b32_e32 v136, v2
	v_mov_b32_e32 v137, v2
	s_andn2_b64 vcc, exec, s[38:39]
	s_cbranch_vccnz .LBB0_2986
	s_branch .LBB0_2987
